# speedup vs baseline: 1.0285x; 1.0029x over previous
.LBB1_3:
	s_load_dwordx4 s[20:23], s[0:1], 0x0
	s_load_dwordx2 s[28:29], s[0:1], 0x20
	s_setprio 3
	v_lshrrev_b32_e32 v1, 3, v0
	v_and_b32_e32 v172, 63, v0
	s_lshl_b32 s3, s2, 5
	v_and_b32_e32 v171, 24, v1
	v_mov_b32_e32 v163, 0
	v_or_b32_e32 v162, s3, v171
	v_lshlrev_b32_e32 v158, 4, v172
	v_mov_b32_e32 v159, v163
	s_waitcnt lgkmcnt(0)
	v_lshl_add_u64 v[2:3], s[20:21], 0, v[158:159]
	v_lshlrev_b32_e32 v6, 12, v162
	v_mov_b32_e32 v7, v163
	v_lshl_add_u64 v[6:7], v[2:3], 0, v[6:7]
	s_movk_i32 s4, 0x4000
	v_add_co_u32_e32 v8, vcc, s4, v6
	s_movk_i32 s6, 0x5000
	s_nop 0
	v_addc_co_u32_e32 v9, vcc, 0, v7, vcc
	v_add_co_u32_e32 v62, vcc, s6, v6
	v_lshlrev_b64 v[4:5], 12, v[162:163]
	s_nop 0
	v_addc_co_u32_e32 v63, vcc, 0, v7, vcc
	s_movk_i32 s4, 0x6000
	v_lshl_add_u64 v[4:5], v[2:3], 0, v[4:5]
	v_or_b32_e32 v132, 1, v162
	v_mov_b32_e32 v133, v163
	v_or_b32_e32 v130, 2, v162
	v_mov_b32_e32 v131, v163
	v_add_co_u32_e32 v38, vcc, s4, v6
	v_or_b32_e32 v164, 3, v162
	v_mov_b32_e32 v165, v163
	global_load_dwordx4 v[122:125], v[4:5], off nt
	global_load_dwordx4 v[102:105], v[4:5], off offset:1024 nt
	global_load_dwordx4 v[86:89], v[4:5], off offset:2048 nt
	global_load_dwordx4 v[74:77], v[4:5], off offset:3072 nt
	v_lshlrev_b64 v[4:5], 12, v[132:133]
	v_lshlrev_b64 v[10:11], 12, v[130:131]
	v_addc_co_u32_e32 v39, vcc, 0, v7, vcc
	v_lshlrev_b64 v[12:13], 12, v[164:165]
	v_lshl_add_u64 v[4:5], v[2:3], 0, v[4:5]
	v_lshl_add_u64 v[10:11], v[2:3], 0, v[10:11]
	v_lshl_add_u64 v[2:3], v[2:3], 0, v[12:13]
	v_add_co_u32_e32 v134, vcc, 0x7000, v6
	global_load_dwordx4 v[50:53], v[62:63], off nt
	global_load_dwordx4 v[34:37], v[62:63], off offset:1024 nt
	v_addc_co_u32_e32 v135, vcc, 0, v7, vcc
	global_load_dwordx4 v[26:29], v[62:63], off offset:2048 nt
	global_load_dwordx4 v[14:17], v[62:63], off offset:3072 nt
	global_load_dwordx4 v[46:49], v[8:9], off offset:1024 nt
	global_load_dwordx4 v[30:33], v[8:9], off offset:2048 nt
	global_load_dwordx4 v[18:21], v[8:9], off offset:3072 nt
	global_load_dwordx4 v[126:129], v[4:5], off nt
	global_load_dwordx4 v[110:113], v[4:5], off offset:1024 nt
	global_load_dwordx4 v[94:97], v[4:5], off offset:2048 nt
	global_load_dwordx4 v[82:85], v[4:5], off offset:3072 nt
	global_load_dwordx4 v[118:121], v[10:11], off nt
	global_load_dwordx4 v[106:109], v[10:11], off offset:1024 nt
	global_load_dwordx4 v[90:93], v[10:11], off offset:2048 nt
	global_load_dwordx4 v[78:81], v[10:11], off offset:3072 nt
	global_load_dwordx4 v[58:61], v[38:39], off nt
	global_load_dwordx4 v[42:45], v[38:39], off offset:1024 nt
	global_load_dwordx4 v[22:25], v[38:39], off offset:2048 nt
	s_nop 0
	global_load_dwordx4 v[10:13], v[38:39], off offset:3072 nt
	global_load_dwordx4 v[114:117], v[2:3], off nt
	global_load_dwordx4 v[98:101], v[2:3], off offset:1024 nt
	global_load_dwordx4 v[70:73], v[2:3], off offset:2048 nt
	global_load_dwordx4 v[66:69], v[2:3], off offset:3072 nt
	global_load_dwordx4 v[54:57], v[134:135], off nt
	global_load_dwordx4 v[38:41], v[134:135], off offset:1024 nt
	global_load_dwordx4 v[6:9], v[134:135], off offset:2048 nt
	s_nop 0
	global_load_dwordx4 v[62:65], v[62:63], off offset:-4096 nt
	s_nop 0
	global_load_dwordx4 v[2:5], v[134:135], off offset:3072 nt
	s_movk_i32 s7, 0x7000
	v_cmp_gt_u32_e32 vcc, 32, v0
	s_and_saveexec_b64 s[4:5], vcc
	v_lshl_add_u32 v1, v0, 2, 0
	v_add_u32_e32 v1, 0x10000, v1
	ds_write_b32 v1, v163
	s_or_b64 exec, exec, s[4:5]
	v_lshlrev_b32_e32 v160, 4, v0
	v_mov_b32_e32 v161, v163
	v_lshl_add_u64 v[202:203], s[22:23], 0, v[160:161]
	v_add_co_u32_e32 v134, vcc, 0x1000, v202
	s_mov_b32 s4, 0x9000
	s_nop 0
	v_addc_co_u32_e32 v135, vcc, 0, v203, vcc
	v_add_co_u32_e32 v138, vcc, 0x2000, v202
	v_bfe_u32 v1, v0, 2, 2
	s_nop 0
	v_addc_co_u32_e32 v139, vcc, 0, v203, vcc
	v_add_co_u32_e32 v146, vcc, 0x3000, v202
	global_load_dwordx4 v[134:137], v[134:135], off
	s_nop 0
	global_load_dwordx4 v[138:141], v[138:139], off
	v_addc_co_u32_e32 v147, vcc, 0, v203, vcc
	v_add_co_u32_e32 v154, vcc, s6, v202
	global_load_dwordx4 v[142:145], v160, s[22:23]
	s_nop 0
	global_load_dwordx4 v[146:149], v[146:147], off
	v_addc_co_u32_e32 v155, vcc, 0, v203, vcc
	v_add_co_u32_e32 v174, vcc, s7, v202
	global_load_dwordx4 v[150:153], v[154:155], off offset:-4096
	s_nop 0
	global_load_dwordx4 v[154:157], v[154:155], off
	v_addc_co_u32_e32 v175, vcc, 0, v203, vcc
	v_add_co_u32_e32 v182, vcc, s4, v202
	s_mov_b32 s4, 0xb000
	s_nop 0
	v_addc_co_u32_e32 v183, vcc, 0, v203, vcc
	v_add_co_u32_e32 v190, vcc, s4, v202
	s_mov_b32 s4, 0xd000
	s_nop 0
	v_addc_co_u32_e32 v191, vcc, 0, v203, vcc
	v_add_co_u32_e32 v198, vcc, s4, v202
	s_mov_b32 s4, 0xf000
	s_nop 0
	v_addc_co_u32_e32 v199, vcc, 0, v203, vcc
	v_add_co_u32_e32 v206, vcc, s4, v202
	global_load_dwordx4 v[166:169], v[174:175], off offset:-4096
	s_nop 0
	global_load_dwordx4 v[174:177], v[174:175], off
	v_addc_co_u32_e32 v207, vcc, 0, v203, vcc
	global_load_dwordx4 v[178:181], v[182:183], off offset:-4096
	s_nop 0
	global_load_dwordx4 v[182:185], v[182:183], off
	s_nop 0
	global_load_dwordx4 v[186:189], v[190:191], off offset:-4096
	s_nop 0
	global_load_dwordx4 v[190:193], v[190:191], off
	s_nop 0
	global_load_dwordx4 v[194:197], v[198:199], off offset:-4096
	s_nop 0
	global_load_dwordx4 v[198:201], v[198:199], off
	s_nop 0
	global_load_dwordx4 v[202:205], v[206:207], off offset:-4096
	s_nop 0
	global_load_dwordx4 v[206:209], v[206:207], off
	v_lshlrev_b32_e32 v159, 1, v0
	v_bfe_u32 v161, v0, 2, 1
	v_lshrrev_b32_e32 v170, 4, v0
	v_or_b32_e32 v173, 0x100, v0
	v_and_or_b32 v1, v160, 48, v1
	v_and_b32_e32 v159, 6, v159
	v_lshrrev_b32_e32 v173, 4, v173
	v_bitop3_b32 v170, v161, v170, v159 bitop3:0x36
	v_lshl_add_u32 v1, v1, 10, 0
	v_bitop3_b32 v173, v173, v161, v159 bitop3:0x1e
	v_lshl_add_u32 v170, v170, 4, v1
	v_or_b32_e32 v210, 0x200, v0
	v_lshl_add_u32 v173, v173, 4, v1
	v_lshrrev_b32_e32 v210, 4, v210
	v_bitop3_b32 v210, v210, v161, v159 bitop3:0x1e
	v_lshlrev_b64 v[132:133], 11, v[132:133]
	v_lshl_add_u64 v[132:133], s[28:29], 0, v[132:133]
	v_lshlrev_b64 v[130:131], 11, v[130:131]
	v_lshl_add_u64 v[130:131], s[28:29], 0, v[130:131]
	s_waitcnt vmcnt(13)
	ds_write_b128 v170, v[142:145]
	ds_write_b128 v173, v[134:137]
	v_or_b32_e32 v135, 0x300, v0
	v_lshrrev_b32_e32 v135, 4, v135
	v_bitop3_b32 v135, v135, v161, v159 bitop3:0x1e
	v_lshl_add_u32 v134, v210, 4, v1
	v_lshl_add_u32 v1, v135, 4, v1
	ds_write_b128 v134, v[138:141]
	s_waitcnt vmcnt(12)
	ds_write_b128 v1, v[146:149]
	s_waitcnt vmcnt(11)
	ds_write_b128 v170, v[150:153] offset:4096
	s_waitcnt vmcnt(10)
	ds_write_b128 v173, v[154:157] offset:4096
	s_waitcnt vmcnt(9)
	ds_write_b128 v134, v[166:169] offset:4096
	s_waitcnt vmcnt(8)
	ds_write_b128 v1, v[174:177] offset:4096
	s_waitcnt vmcnt(7)
	ds_write_b128 v170, v[178:181] offset:8192
	s_waitcnt vmcnt(6)
	ds_write_b128 v173, v[182:185] offset:8192
	s_waitcnt vmcnt(5)
	ds_write_b128 v134, v[186:189] offset:8192
	s_waitcnt vmcnt(4)
	ds_write_b128 v1, v[190:193] offset:8192
	s_waitcnt vmcnt(3)
	ds_write_b128 v170, v[194:197] offset:12288
	s_waitcnt vmcnt(2)
	ds_write_b128 v173, v[198:201] offset:12288
	s_waitcnt vmcnt(1)
	ds_write_b128 v134, v[202:205] offset:12288
	s_waitcnt vmcnt(0)
	ds_write_b128 v1, v[206:209] offset:12288
	v_lshlrev_b64 v[134:135], 11, v[162:163]
	v_lshl_add_u64 v[134:135], s[28:29], 0, v[134:135]
	v_lshlrev_b32_e32 v166, 3, v172
	v_mov_b32_e32 v167, v163
	v_cvt_pk_f16_f32 v137, v124, v125
	v_cvt_pk_f16_f32 v136, v122, v123
	v_lshl_add_u64 v[134:135], v[134:135], 0, v[166:167]
	s_waitcnt lgkmcnt(0)
	s_barrier
	global_store_dwordx2 v[134:135], v[136:137], off sc1
	v_cvt_pk_f16_f32 v137, v104, v105
	v_cvt_pk_f16_f32 v136, v102, v103
	global_store_dwordx2 v[134:135], v[136:137], off offset:512 sc1
	v_cvt_pk_f16_f32 v137, v88, v89
	v_cvt_pk_f16_f32 v136, v86, v87
	global_store_dwordx2 v[134:135], v[136:137], off offset:1024 sc1
	v_cvt_pk_f16_f32 v137, v76, v77
	v_cvt_pk_f16_f32 v136, v74, v75
	global_store_dwordx2 v[134:135], v[136:137], off offset:1536 sc1
	v_cvt_pk_f16_f32 v135, v128, v129
	v_cvt_pk_f16_f32 v134, v126, v127
	v_lshl_add_u64 v[132:133], v[132:133], 0, v[166:167]
	global_store_dwordx2 v[132:133], v[134:135], off sc1
	v_cvt_pk_f16_f32 v135, v112, v113
	v_cvt_pk_f16_f32 v134, v110, v111
	global_store_dwordx2 v[132:133], v[134:135], off offset:512 sc1
	v_cvt_pk_f16_f32 v135, v96, v97
	v_cvt_pk_f16_f32 v134, v94, v95
	global_store_dwordx2 v[132:133], v[134:135], off offset:1024 sc1
	v_cvt_pk_f16_f32 v135, v84, v85
	v_cvt_pk_f16_f32 v134, v82, v83
	global_store_dwordx2 v[132:133], v[134:135], off offset:1536 sc1
	v_cvt_pk_f16_f32 v133, v120, v121
	v_cvt_pk_f16_f32 v132, v118, v119
	v_lshl_add_u64 v[130:131], v[130:131], 0, v[166:167]
	global_store_dwordx2 v[130:131], v[132:133], off sc1
	v_cvt_pk_f16_f32 v133, v108, v109
	v_cvt_pk_f16_f32 v132, v106, v107
	global_store_dwordx2 v[130:131], v[132:133], off offset:512 sc1
	v_cvt_pk_f16_f32 v133, v92, v93
	v_cvt_pk_f16_f32 v132, v90, v91
	global_store_dwordx2 v[130:131], v[132:133], off offset:1024 sc1
	v_cvt_pk_f16_f32 v133, v80, v81
	v_cvt_pk_f16_f32 v132, v78, v79
	global_store_dwordx2 v[130:131], v[132:133], off offset:1536 sc1
	v_xor_b32_e32 v130, 2, v172
	v_lshl_add_u32 v161, v130, 4, 0
	v_xor_b32_e32 v130, 4, v172
	v_lshl_add_u32 v168, v130, 4, 0
	v_lshl_add_u32 v1, v172, 4, 0
	ds_read_b128 v[134:137], v168 offset:32768
	ds_read_b128 v[142:145], v1
	ds_read_b128 v[138:141], v161 offset:16384
	v_xor_b32_e32 v130, 6, v172
	v_lshl_add_u32 v163, v130, 4, 0
	ds_read_b128 v[130:133], v163 offset:49152
	ds_read_b128 v[146:149], v1 offset:2048
	s_waitcnt lgkmcnt(4)
	v_fma_f32 v207, v122, v134, 0
	v_fma_f32 v179, v126, v134, 0
	v_fma_f32 v211, v118, v134, 0
	v_fma_f32 v188, v114, v134, 0
	v_xor_b32_e32 v134, 1, v172
	s_waitcnt lgkmcnt(3)
	v_fma_f32 v173, v122, v144, 0
	v_fma_f32 v189, v126, v144, 0
	v_fma_f32 v218, v118, v144, 0
	v_fma_f32 v197, v114, v144, 0
	v_lshl_add_u32 v144, v134, 4, 0
	v_xor_b32_e32 v134, 3, v172
	v_fma_f32 v159, v122, v145, 0
	s_waitcnt lgkmcnt(2)
	v_fma_f32 v205, v122, v138, 0
	v_fma_f32 v204, v122, v139, 0
	v_fma_f32 v203, v122, v140, 0
	v_fma_f32 v200, v122, v141, 0
	v_fma_f32 v187, v126, v145, 0
	v_fma_f32 v186, v126, v138, 0
	v_fma_f32 v183, v126, v139, 0
	v_fma_f32 v181, v126, v140, 0
	v_fma_f32 v180, v126, v141, 0
	v_fma_f32 v221, v118, v142, 0
	v_fma_f32 v219, v118, v143, 0
	v_fma_f32 v216, v118, v145, 0
	v_fma_f32 v215, v118, v138, 0
	v_fma_f32 v214, v118, v139, 0
	v_fma_f32 v213, v118, v140, 0
	v_fma_f32 v212, v118, v141, 0
	v_fma_f32 v210, v118, v135, 0
	v_fma_f32 v209, v118, v136, 0
	v_fma_f32 v208, v118, v137, 0
	v_fma_f32 v196, v114, v145, 0
	v_fma_f32 v195, v114, v138, 0
	v_fma_f32 v194, v114, v139, 0
	v_fma_f32 v191, v114, v140, 0
	v_fma_f32 v190, v114, v141, 0
	ds_read_b128 v[138:141], v144 offset:1024
	v_lshl_add_u32 v145, v134, 4, 0
	v_xor_b32_e32 v134, 5, v172
	s_waitcnt lgkmcnt(2)
	v_fma_f32 v235, v118, v130, 0
	v_fma_f32 v233, v118, v131, 0
	v_fma_f32 v232, v118, v132, 0
	v_fma_f32 v231, v118, v133, 0
	v_xor_b32_e32 v118, 7, v172
	ds_read_b128 v[222:225], v145 offset:17408
	v_lshl_add_u32 v169, v134, 4, 0
	v_lshl_add_u32 v170, v118, 4, 0
	ds_read_b128 v[150:153], v161 offset:18432
	ds_read_b128 v[154:157], v168 offset:34816
	v_fma_f32 v206, v122, v135, 0
	v_fma_f32 v202, v122, v136, 0
	v_fma_f32 v201, v122, v137, 0
	v_fma_f32 v178, v126, v135, 0
	v_fma_f32 v177, v126, v136, 0
	v_fma_f32 v176, v126, v137, 0
	v_fma_f32 v185, v114, v135, 0
	v_fma_f32 v184, v114, v136, 0
	v_fma_f32 v182, v114, v137, 0
	ds_read_b128 v[226:229], v169 offset:33792
	ds_read_b128 v[134:137], v144 offset:3072
	ds_read_b128 v[236:239], v169 offset:35840
	ds_read_b128 v[244:247], v170 offset:50176
	v_fma_f32 v175, v122, v142, 0
	v_fma_f32 v174, v122, v143, 0
	v_fma_f32 v193, v126, v142, 0
	v_fma_f32 v192, v126, v143, 0
	v_fma_f32 v199, v114, v142, 0
	v_fma_f32 v198, v114, v143, 0
	s_waitcnt lgkmcnt(7)
	v_fmac_f32_e32 v175, v123, v138
	v_fmac_f32_e32 v174, v123, v139
	v_fmac_f32_e32 v173, v123, v140
	v_fmac_f32_e32 v159, v123, v141
	v_fmac_f32_e32 v193, v127, v138
	v_fmac_f32_e32 v192, v127, v139
	v_fmac_f32_e32 v189, v127, v140
	v_fmac_f32_e32 v187, v127, v141
	v_fmac_f32_e32 v221, v119, v138
	v_fmac_f32_e32 v219, v119, v139
	v_fmac_f32_e32 v218, v119, v140
	v_fmac_f32_e32 v216, v119, v141
	v_fmac_f32_e32 v199, v115, v138
	v_fmac_f32_e32 v198, v115, v139
	v_fmac_f32_e32 v197, v115, v140
	v_fmac_f32_e32 v196, v115, v141
	ds_read_b128 v[138:141], v145 offset:19456
	ds_read_b128 v[240:243], v163 offset:51200
	s_waitcnt lgkmcnt(8)
	v_fmac_f32_e32 v205, v123, v222
	v_fmac_f32_e32 v204, v123, v223
	v_fmac_f32_e32 v203, v123, v224
	v_fmac_f32_e32 v200, v123, v225
	v_fmac_f32_e32 v186, v127, v222
	v_fmac_f32_e32 v183, v127, v223
	v_fmac_f32_e32 v181, v127, v224
	v_fmac_f32_e32 v180, v127, v225
	v_fmac_f32_e32 v215, v119, v222
	v_fmac_f32_e32 v214, v119, v223
	v_fmac_f32_e32 v213, v119, v224
	v_fmac_f32_e32 v212, v119, v225
	v_fmac_f32_e32 v195, v115, v222
	v_fmac_f32_e32 v194, v115, v223
	v_fmac_f32_e32 v191, v115, v224
	v_fmac_f32_e32 v190, v115, v225
	s_waitcnt lgkmcnt(5)
	v_fmac_f32_e32 v207, v123, v226
	v_fmac_f32_e32 v206, v123, v227
	v_fmac_f32_e32 v202, v123, v228
	v_fmac_f32_e32 v201, v123, v229
	v_fmac_f32_e32 v179, v127, v226
	v_fmac_f32_e32 v178, v127, v227
	v_fmac_f32_e32 v177, v127, v228
	v_fmac_f32_e32 v176, v127, v229
	v_fmac_f32_e32 v211, v119, v226
	v_fmac_f32_e32 v210, v119, v227
	v_fmac_f32_e32 v209, v119, v228
	v_fmac_f32_e32 v208, v119, v229
	v_fmac_f32_e32 v188, v115, v226
	v_fmac_f32_e32 v185, v115, v227
	v_fmac_f32_e32 v184, v115, v228
	v_fmac_f32_e32 v182, v115, v229
	v_fma_f32 v234, v122, v130, 0
	v_fma_f32 v230, v122, v131, 0
	v_fma_f32 v229, v122, v132, 0
	v_fma_f32 v228, v122, v133, 0
	v_fma_f32 v224, v126, v130, 0
	v_fma_f32 v223, v126, v131, 0
	v_fma_f32 v222, v126, v132, 0
	v_fma_f32 v217, v126, v133, 0
	v_fma_f32 v227, v114, v130, 0
	v_fma_f32 v226, v114, v131, 0
	v_fma_f32 v225, v114, v132, 0
	v_fma_f32 v220, v114, v133, 0
	ds_read_b128 v[130:133], v170 offset:52224
	s_waitcnt lgkmcnt(3)
	v_fmac_f32_e32 v235, v119, v244
	v_fmac_f32_e32 v233, v119, v245
	v_fmac_f32_e32 v232, v119, v246
	v_fmac_f32_e32 v231, v119, v247
	v_lshlrev_b64 v[118:119], 11, v[164:165]
	v_lshl_add_u64 v[118:119], s[28:29], 0, v[118:119]
	v_fmac_f32_e32 v234, v123, v244
	v_fmac_f32_e32 v230, v123, v245
	v_fmac_f32_e32 v229, v123, v246
	v_fmac_f32_e32 v228, v123, v247
	v_fmac_f32_e32 v224, v127, v244
	v_fmac_f32_e32 v223, v127, v245
	v_fmac_f32_e32 v222, v127, v246
	v_fmac_f32_e32 v217, v127, v247
	v_fmac_f32_e32 v227, v115, v244
	v_fmac_f32_e32 v226, v115, v245
	v_fmac_f32_e32 v225, v115, v246
	v_fmac_f32_e32 v220, v115, v247
	v_lshl_add_u64 v[142:143], v[118:119], 0, v[166:167]
	v_cvt_pk_f16_f32 v119, v116, v117
	v_cvt_pk_f16_f32 v118, v114, v115
	v_cvt_pk_f16_f32 v115, v100, v101
	v_cvt_pk_f16_f32 v114, v98, v99
	v_fmac_f32_e32 v175, v124, v146
	v_fmac_f32_e32 v174, v124, v147
	v_fmac_f32_e32 v173, v124, v148
	v_fmac_f32_e32 v159, v124, v149
	v_fmac_f32_e32 v193, v128, v146
	v_fmac_f32_e32 v192, v128, v147
	v_fmac_f32_e32 v189, v128, v148
	v_fmac_f32_e32 v187, v128, v149
	v_fmac_f32_e32 v221, v120, v146
	v_fmac_f32_e32 v219, v120, v147
	v_fmac_f32_e32 v218, v120, v148
	v_fmac_f32_e32 v216, v120, v149
	v_fmac_f32_e32 v199, v116, v146
	v_fmac_f32_e32 v198, v116, v147
	v_fmac_f32_e32 v197, v116, v148
	v_fmac_f32_e32 v196, v116, v149
	v_fmac_f32_e32 v205, v124, v150
	v_fmac_f32_e32 v204, v124, v151
	v_fmac_f32_e32 v203, v124, v152
	v_fmac_f32_e32 v200, v124, v153
	v_fmac_f32_e32 v186, v128, v150
	v_fmac_f32_e32 v183, v128, v151
	v_fmac_f32_e32 v181, v128, v152
	v_fmac_f32_e32 v180, v128, v153
	v_fmac_f32_e32 v215, v120, v150
	v_fmac_f32_e32 v214, v120, v151
	v_fmac_f32_e32 v213, v120, v152
	v_fmac_f32_e32 v212, v120, v153
	v_fmac_f32_e32 v195, v116, v150
	v_fmac_f32_e32 v194, v116, v151
	v_fmac_f32_e32 v191, v116, v152
	v_fmac_f32_e32 v190, v116, v153
	v_fmac_f32_e32 v207, v124, v154
	v_fmac_f32_e32 v206, v124, v155
	v_fmac_f32_e32 v202, v124, v156
	v_fmac_f32_e32 v201, v124, v157
	v_fmac_f32_e32 v179, v128, v154
	v_fmac_f32_e32 v178, v128, v155
	v_fmac_f32_e32 v177, v128, v156
	v_fmac_f32_e32 v176, v128, v157
	s_waitcnt lgkmcnt(1)
	v_fmac_f32_e32 v234, v124, v240
	v_fmac_f32_e32 v230, v124, v241
	v_fmac_f32_e32 v229, v124, v242
	v_fmac_f32_e32 v228, v124, v243
	v_fmac_f32_e32 v224, v128, v240
	v_fmac_f32_e32 v223, v128, v241
	v_fmac_f32_e32 v222, v128, v242
	v_fmac_f32_e32 v217, v128, v243
	v_fmac_f32_e32 v235, v120, v240
	v_fmac_f32_e32 v233, v120, v241
	v_fmac_f32_e32 v232, v120, v242
	v_fmac_f32_e32 v231, v120, v243
	v_fmac_f32_e32 v227, v116, v240
	v_fmac_f32_e32 v226, v116, v241
	v_fmac_f32_e32 v225, v116, v242
	v_fmac_f32_e32 v220, v116, v243
	global_store_dwordx2 v[142:143], v[118:119], off sc1
	global_store_dwordx2 v[142:143], v[114:115], off offset:512 sc1
	v_fmac_f32_e32 v175, v125, v134
	v_fmac_f32_e32 v174, v125, v135
	v_fmac_f32_e32 v173, v125, v136
	v_fmac_f32_e32 v159, v125, v137
	v_fmac_f32_e32 v205, v125, v138
	v_fmac_f32_e32 v204, v125, v139
	v_fmac_f32_e32 v203, v125, v140
	v_fmac_f32_e32 v200, v125, v141
	v_fmac_f32_e32 v207, v125, v236
	v_fmac_f32_e32 v206, v125, v237
	v_fmac_f32_e32 v202, v125, v238
	v_fmac_f32_e32 v201, v125, v239
	s_waitcnt lgkmcnt(0)
	v_fmac_f32_e32 v234, v125, v130
	v_fmac_f32_e32 v230, v125, v131
	v_fmac_f32_e32 v229, v125, v132
	v_fmac_f32_e32 v228, v125, v133
	v_fmac_f32_e32 v193, v129, v134
	v_fmac_f32_e32 v192, v129, v135
	v_fmac_f32_e32 v189, v129, v136
	v_fmac_f32_e32 v187, v129, v137
	v_fmac_f32_e32 v186, v129, v138
	v_fmac_f32_e32 v183, v129, v139
	v_fmac_f32_e32 v181, v129, v140
	v_fmac_f32_e32 v180, v129, v141
	v_fmac_f32_e32 v179, v129, v236
	v_fmac_f32_e32 v178, v129, v237
	v_fmac_f32_e32 v177, v129, v238
	v_fmac_f32_e32 v176, v129, v239
	v_fmac_f32_e32 v224, v129, v130
	v_fmac_f32_e32 v223, v129, v131
	v_fmac_f32_e32 v222, v129, v132
	v_fmac_f32_e32 v217, v129, v133
	v_fmac_f32_e32 v221, v121, v134
	v_fmac_f32_e32 v219, v121, v135
	v_fmac_f32_e32 v218, v121, v136
	v_fmac_f32_e32 v216, v121, v137
	v_fmac_f32_e32 v215, v121, v138
	v_fmac_f32_e32 v214, v121, v139
	v_fmac_f32_e32 v213, v121, v140
	v_fmac_f32_e32 v212, v121, v141
	v_fmac_f32_e32 v235, v121, v130
	v_fmac_f32_e32 v233, v121, v131
	v_fmac_f32_e32 v232, v121, v132
	v_fmac_f32_e32 v231, v121, v133
	v_fmac_f32_e32 v199, v117, v134
	v_fmac_f32_e32 v198, v117, v135
	v_fmac_f32_e32 v197, v117, v136
	v_fmac_f32_e32 v196, v117, v137
	v_fmac_f32_e32 v195, v117, v138
	v_fmac_f32_e32 v194, v117, v139
	v_fmac_f32_e32 v191, v117, v140
	v_fmac_f32_e32 v190, v117, v141
	v_fmac_f32_e32 v227, v117, v130
	v_fmac_f32_e32 v226, v117, v131
	v_fmac_f32_e32 v225, v117, v132
	v_fmac_f32_e32 v220, v117, v133
	ds_read_b128 v[126:129], v1 offset:4096
	ds_read_b128 v[138:141], v161 offset:20480
	ds_read_b128 v[134:137], v168 offset:36864
	ds_read_b128 v[130:133], v163 offset:53248
	ds_read_b128 v[122:125], v1 offset:6144
	v_fmac_f32_e32 v211, v120, v154
	v_fmac_f32_e32 v210, v120, v155
	v_fmac_f32_e32 v209, v120, v156
	v_fmac_f32_e32 v208, v120, v157
	v_fmac_f32_e32 v188, v116, v154
	v_fmac_f32_e32 v185, v116, v155
	v_fmac_f32_e32 v184, v116, v156
	v_fmac_f32_e32 v182, v116, v157
	v_fmac_f32_e32 v211, v121, v236
	v_fmac_f32_e32 v210, v121, v237
	v_fmac_f32_e32 v209, v121, v238
	v_fmac_f32_e32 v208, v121, v239
	v_fmac_f32_e32 v188, v117, v236
	v_fmac_f32_e32 v185, v117, v237
	v_fmac_f32_e32 v184, v117, v238
	v_fmac_f32_e32 v182, v117, v239
	ds_read_b128 v[114:117], v161 offset:22528
	s_waitcnt lgkmcnt(3)
	v_fmac_f32_e32 v207, v102, v134
	v_fmac_f32_e32 v206, v102, v135
	v_fmac_f32_e32 v202, v102, v136
	v_fmac_f32_e32 v201, v102, v137
	v_fmac_f32_e32 v179, v110, v134
	v_fmac_f32_e32 v178, v110, v135
	v_fmac_f32_e32 v177, v110, v136
	v_fmac_f32_e32 v176, v110, v137
	v_fmac_f32_e32 v211, v106, v134
	v_fmac_f32_e32 v210, v106, v135
	v_fmac_f32_e32 v209, v106, v136
	v_fmac_f32_e32 v208, v106, v137
	v_fmac_f32_e32 v188, v98, v134
	v_fmac_f32_e32 v185, v98, v135
	v_fmac_f32_e32 v184, v98, v136
	v_fmac_f32_e32 v182, v98, v137
	ds_read_b128 v[134:137], v144 offset:5120
	v_fmac_f32_e32 v175, v102, v126
	v_fmac_f32_e32 v174, v102, v127
	v_fmac_f32_e32 v173, v102, v128
	v_fmac_f32_e32 v159, v102, v129
	v_fmac_f32_e32 v205, v102, v138
	v_fmac_f32_e32 v204, v102, v139
	v_fmac_f32_e32 v203, v102, v140
	v_fmac_f32_e32 v200, v102, v141
	ds_read_b128 v[118:121], v168 offset:38912
	v_fmac_f32_e32 v193, v110, v126
	v_fmac_f32_e32 v192, v110, v127
	v_fmac_f32_e32 v189, v110, v128
	v_fmac_f32_e32 v187, v110, v129
	v_fmac_f32_e32 v221, v106, v126
	v_fmac_f32_e32 v219, v106, v127
	v_fmac_f32_e32 v218, v106, v128
	v_fmac_f32_e32 v216, v106, v129
	v_fmac_f32_e32 v199, v98, v126
	v_fmac_f32_e32 v198, v98, v127
	v_fmac_f32_e32 v197, v98, v128
	v_fmac_f32_e32 v196, v98, v129
	ds_read_b128 v[126:129], v163 offset:55296
	s_waitcnt lgkmcnt(5)
	v_fmac_f32_e32 v234, v102, v130
	v_fmac_f32_e32 v230, v102, v131
	v_fmac_f32_e32 v229, v102, v132
	v_fmac_f32_e32 v228, v102, v133
	v_fmac_f32_e32 v186, v110, v138
	v_fmac_f32_e32 v183, v110, v139
	v_fmac_f32_e32 v181, v110, v140
	v_fmac_f32_e32 v180, v110, v141
	v_fmac_f32_e32 v224, v110, v130
	v_fmac_f32_e32 v223, v110, v131
	v_fmac_f32_e32 v222, v110, v132
	v_fmac_f32_e32 v217, v110, v133
	v_fmac_f32_e32 v215, v106, v138
	v_fmac_f32_e32 v214, v106, v139
	v_fmac_f32_e32 v213, v106, v140
	v_fmac_f32_e32 v212, v106, v141
	v_fmac_f32_e32 v235, v106, v130
	v_fmac_f32_e32 v233, v106, v131
	v_fmac_f32_e32 v232, v106, v132
	v_fmac_f32_e32 v231, v106, v133
	v_fmac_f32_e32 v195, v98, v138
	v_fmac_f32_e32 v194, v98, v139
	v_fmac_f32_e32 v191, v98, v140
	v_fmac_f32_e32 v190, v98, v141
	v_fmac_f32_e32 v227, v98, v130
	v_fmac_f32_e32 v226, v98, v131
	v_fmac_f32_e32 v225, v98, v132
	v_fmac_f32_e32 v220, v98, v133
	ds_read_b128 v[138:141], v145 offset:21504
	ds_read_b128 v[146:149], v169 offset:37888
	ds_read_b128 v[130:133], v144 offset:7168
	s_waitcnt lgkmcnt(5)
	v_fmac_f32_e32 v175, v103, v134
	v_fmac_f32_e32 v174, v103, v135
	v_fmac_f32_e32 v173, v103, v136
	v_fmac_f32_e32 v159, v103, v137
	v_fmac_f32_e32 v193, v111, v134
	v_fmac_f32_e32 v192, v111, v135
	v_fmac_f32_e32 v189, v111, v136
	v_fmac_f32_e32 v187, v111, v137
	v_fmac_f32_e32 v221, v107, v134
	v_fmac_f32_e32 v219, v107, v135
	v_fmac_f32_e32 v218, v107, v136
	v_fmac_f32_e32 v216, v107, v137
	v_fmac_f32_e32 v199, v99, v134
	v_fmac_f32_e32 v198, v99, v135
	v_fmac_f32_e32 v197, v99, v136
	v_fmac_f32_e32 v196, v99, v137
	ds_read_b128 v[150:153], v170 offset:54272
	ds_read_b128 v[134:137], v145 offset:23552
	s_waitcnt lgkmcnt(4)
	v_fmac_f32_e32 v205, v103, v138
	v_fmac_f32_e32 v204, v103, v139
	v_fmac_f32_e32 v203, v103, v140
	v_fmac_f32_e32 v200, v103, v141
	v_fmac_f32_e32 v186, v111, v138
	v_fmac_f32_e32 v183, v111, v139
	v_fmac_f32_e32 v181, v111, v140
	v_fmac_f32_e32 v180, v111, v141
	v_fmac_f32_e32 v215, v107, v138
	v_fmac_f32_e32 v214, v107, v139
	v_fmac_f32_e32 v213, v107, v140
	v_fmac_f32_e32 v212, v107, v141
	v_fmac_f32_e32 v195, v99, v138
	v_fmac_f32_e32 v194, v99, v139
	v_fmac_f32_e32 v191, v99, v140
	v_fmac_f32_e32 v190, v99, v141
	ds_read_b128 v[138:141], v169 offset:39936
	s_waitcnt lgkmcnt(4)
	v_fmac_f32_e32 v207, v103, v146
	v_fmac_f32_e32 v206, v103, v147
	v_fmac_f32_e32 v202, v103, v148
	v_fmac_f32_e32 v201, v103, v149
	v_fmac_f32_e32 v179, v111, v146
	v_fmac_f32_e32 v178, v111, v147
	v_fmac_f32_e32 v177, v111, v148
	v_fmac_f32_e32 v176, v111, v149
	v_fmac_f32_e32 v211, v107, v146
	v_fmac_f32_e32 v210, v107, v147
	v_fmac_f32_e32 v209, v107, v148
	v_fmac_f32_e32 v208, v107, v149
	v_fmac_f32_e32 v188, v99, v146
	v_fmac_f32_e32 v185, v99, v147
	v_fmac_f32_e32 v184, v99, v148
	v_fmac_f32_e32 v182, v99, v149
	ds_read_b128 v[146:149], v170 offset:56320
	s_waitcnt lgkmcnt(3)
	v_fmac_f32_e32 v227, v99, v150
	v_fmac_f32_e32 v226, v99, v151
	v_fmac_f32_e32 v225, v99, v152
	v_fmac_f32_e32 v220, v99, v153
	v_fmac_f32_e32 v234, v103, v150
	v_fmac_f32_e32 v230, v103, v151
	v_fmac_f32_e32 v229, v103, v152
	v_fmac_f32_e32 v228, v103, v153
	v_fmac_f32_e32 v224, v111, v150
	v_fmac_f32_e32 v223, v111, v151
	v_fmac_f32_e32 v222, v111, v152
	v_fmac_f32_e32 v217, v111, v153
	v_fmac_f32_e32 v235, v107, v150
	v_fmac_f32_e32 v233, v107, v151
	v_fmac_f32_e32 v232, v107, v152
	v_fmac_f32_e32 v231, v107, v153
	v_fmac_f32_e32 v199, v100, v122
	v_fmac_f32_e32 v198, v100, v123
	v_fmac_f32_e32 v197, v100, v124
	v_fmac_f32_e32 v196, v100, v125
	v_fmac_f32_e32 v195, v100, v114
	v_fmac_f32_e32 v194, v100, v115
	v_fmac_f32_e32 v191, v100, v116
	v_fmac_f32_e32 v190, v100, v117
	v_fmac_f32_e32 v188, v100, v118
	v_fmac_f32_e32 v185, v100, v119
	v_fmac_f32_e32 v184, v100, v120
	v_fmac_f32_e32 v182, v100, v121
	v_fmac_f32_e32 v227, v100, v126
	v_fmac_f32_e32 v226, v100, v127
	v_fmac_f32_e32 v225, v100, v128
	v_fmac_f32_e32 v220, v100, v129
	v_fmac_f32_e32 v175, v104, v122
	v_fmac_f32_e32 v174, v104, v123
	v_fmac_f32_e32 v173, v104, v124
	v_fmac_f32_e32 v159, v104, v125
	v_fmac_f32_e32 v193, v112, v122
	v_fmac_f32_e32 v192, v112, v123
	v_fmac_f32_e32 v189, v112, v124
	v_fmac_f32_e32 v187, v112, v125
	v_fmac_f32_e32 v221, v108, v122
	v_fmac_f32_e32 v219, v108, v123
	v_fmac_f32_e32 v218, v108, v124
	v_fmac_f32_e32 v216, v108, v125
	v_fmac_f32_e32 v205, v104, v114
	v_fmac_f32_e32 v204, v104, v115
	v_fmac_f32_e32 v203, v104, v116
	v_fmac_f32_e32 v200, v104, v117
	v_fmac_f32_e32 v207, v104, v118
	v_fmac_f32_e32 v206, v104, v119
	v_fmac_f32_e32 v202, v104, v120
	v_fmac_f32_e32 v201, v104, v121
	v_fmac_f32_e32 v234, v104, v126
	v_fmac_f32_e32 v230, v104, v127
	v_fmac_f32_e32 v229, v104, v128
	v_fmac_f32_e32 v228, v104, v129
	v_fmac_f32_e32 v186, v112, v114
	v_fmac_f32_e32 v183, v112, v115
	v_fmac_f32_e32 v181, v112, v116
	v_fmac_f32_e32 v180, v112, v117
	v_fmac_f32_e32 v179, v112, v118
	v_fmac_f32_e32 v178, v112, v119
	v_fmac_f32_e32 v177, v112, v120
	v_fmac_f32_e32 v176, v112, v121
	v_fmac_f32_e32 v224, v112, v126
	v_fmac_f32_e32 v223, v112, v127
	v_fmac_f32_e32 v222, v112, v128
	v_fmac_f32_e32 v217, v112, v129
	v_fmac_f32_e32 v215, v108, v114
	v_fmac_f32_e32 v214, v108, v115
	v_fmac_f32_e32 v213, v108, v116
	v_fmac_f32_e32 v212, v108, v117
	v_fmac_f32_e32 v211, v108, v118
	v_fmac_f32_e32 v210, v108, v119
	v_fmac_f32_e32 v209, v108, v120
	v_fmac_f32_e32 v208, v108, v121
	v_fmac_f32_e32 v235, v108, v126
	v_fmac_f32_e32 v233, v108, v127
	v_fmac_f32_e32 v232, v108, v128
	v_fmac_f32_e32 v231, v108, v129
	v_fmac_f32_e32 v199, v101, v130
	v_fmac_f32_e32 v198, v101, v131
	v_fmac_f32_e32 v197, v101, v132
	v_fmac_f32_e32 v196, v101, v133
	s_waitcnt lgkmcnt(2)
	v_fmac_f32_e32 v195, v101, v134
	v_fmac_f32_e32 v194, v101, v135
	v_fmac_f32_e32 v191, v101, v136
	v_fmac_f32_e32 v190, v101, v137
	s_waitcnt lgkmcnt(1)
	v_fmac_f32_e32 v188, v101, v138
	v_fmac_f32_e32 v185, v101, v139
	v_fmac_f32_e32 v184, v101, v140
	v_fmac_f32_e32 v182, v101, v141
	s_waitcnt lgkmcnt(0)
	v_fmac_f32_e32 v227, v101, v146
	v_fmac_f32_e32 v226, v101, v147
	v_fmac_f32_e32 v225, v101, v148
	v_fmac_f32_e32 v220, v101, v149
	ds_read_b128 v[126:129], v1 offset:8192
	ds_read_b128 v[122:125], v161 offset:24576
	ds_read_b128 v[118:121], v168 offset:40960
	ds_read_b128 v[114:117], v163 offset:57344
	ds_read_b128 v[98:101], v1 offset:10240
	v_fmac_f32_e32 v175, v105, v130
	v_fmac_f32_e32 v174, v105, v131
	v_fmac_f32_e32 v173, v105, v132
	v_fmac_f32_e32 v159, v105, v133
	v_fmac_f32_e32 v205, v105, v134
	v_fmac_f32_e32 v204, v105, v135
	v_fmac_f32_e32 v203, v105, v136
	v_fmac_f32_e32 v200, v105, v137
	v_fmac_f32_e32 v193, v113, v130
	v_fmac_f32_e32 v192, v113, v131
	v_fmac_f32_e32 v189, v113, v132
	v_fmac_f32_e32 v187, v113, v133
	v_fmac_f32_e32 v186, v113, v134
	v_fmac_f32_e32 v183, v113, v135
	v_fmac_f32_e32 v181, v113, v136
	v_fmac_f32_e32 v180, v113, v137
	v_fmac_f32_e32 v221, v109, v130
	v_fmac_f32_e32 v219, v109, v131
	v_fmac_f32_e32 v218, v109, v132
	v_fmac_f32_e32 v216, v109, v133
	v_fmac_f32_e32 v215, v109, v134
	v_fmac_f32_e32 v214, v109, v135
	v_fmac_f32_e32 v213, v109, v136
	v_fmac_f32_e32 v212, v109, v137
	v_fmac_f32_e32 v207, v105, v138
	v_fmac_f32_e32 v206, v105, v139
	v_fmac_f32_e32 v202, v105, v140
	v_fmac_f32_e32 v201, v105, v141
	v_fmac_f32_e32 v234, v105, v146
	v_fmac_f32_e32 v230, v105, v147
	v_fmac_f32_e32 v229, v105, v148
	v_fmac_f32_e32 v228, v105, v149
	v_fmac_f32_e32 v179, v113, v138
	v_fmac_f32_e32 v178, v113, v139
	v_fmac_f32_e32 v177, v113, v140
	v_fmac_f32_e32 v176, v113, v141
	v_fmac_f32_e32 v224, v113, v146
	v_fmac_f32_e32 v223, v113, v147
	v_fmac_f32_e32 v222, v113, v148
	v_fmac_f32_e32 v217, v113, v149
	v_fmac_f32_e32 v211, v109, v138
	v_fmac_f32_e32 v210, v109, v139
	v_fmac_f32_e32 v209, v109, v140
	v_fmac_f32_e32 v208, v109, v141
	v_fmac_f32_e32 v235, v109, v146
	v_fmac_f32_e32 v233, v109, v147
	v_fmac_f32_e32 v232, v109, v148
	v_fmac_f32_e32 v231, v109, v149
	s_waitcnt lgkmcnt(4)
	v_fmac_f32_e32 v175, v86, v126
	v_fmac_f32_e32 v174, v86, v127
	v_fmac_f32_e32 v173, v86, v128
	v_fmac_f32_e32 v159, v86, v129
	ds_read_b128 v[102:105], v161 offset:26624
	ds_read_b128 v[110:113], v163 offset:59392
	s_waitcnt lgkmcnt(5)
	v_fmac_f32_e32 v205, v86, v122
	v_fmac_f32_e32 v204, v86, v123
	v_fmac_f32_e32 v203, v86, v124
	v_fmac_f32_e32 v200, v86, v125
	ds_read_b128 v[106:109], v168 offset:43008
	v_fmac_f32_e32 v193, v94, v126
	v_fmac_f32_e32 v192, v94, v127
	v_fmac_f32_e32 v189, v94, v128
	v_fmac_f32_e32 v187, v94, v129
	v_fmac_f32_e32 v186, v94, v122
	v_fmac_f32_e32 v183, v94, v123
	v_fmac_f32_e32 v181, v94, v124
	v_fmac_f32_e32 v180, v94, v125
	v_fmac_f32_e32 v221, v90, v126
	v_fmac_f32_e32 v219, v90, v127
	v_fmac_f32_e32 v218, v90, v128
	v_fmac_f32_e32 v216, v90, v129
	v_fmac_f32_e32 v215, v90, v122
	v_fmac_f32_e32 v214, v90, v123
	v_fmac_f32_e32 v213, v90, v124
	v_fmac_f32_e32 v212, v90, v125
	v_fmac_f32_e32 v199, v70, v126
	v_fmac_f32_e32 v198, v70, v127
	v_fmac_f32_e32 v197, v70, v128
	v_fmac_f32_e32 v196, v70, v129
	v_fmac_f32_e32 v195, v70, v122
	v_fmac_f32_e32 v194, v70, v123
	v_fmac_f32_e32 v191, v70, v124
	v_fmac_f32_e32 v190, v70, v125
	ds_read_b128 v[126:129], v144 offset:9216
	ds_read_b128 v[130:133], v145 offset:25600
	ds_read_b128 v[134:137], v169 offset:41984
	ds_read_b128 v[138:141], v170 offset:58368
	ds_read_b128 v[122:125], v144 offset:11264
	s_waitcnt lgkmcnt(10)
	v_fmac_f32_e32 v207, v86, v118
	v_fmac_f32_e32 v206, v86, v119
	v_fmac_f32_e32 v202, v86, v120
	v_fmac_f32_e32 v201, v86, v121
	s_waitcnt lgkmcnt(9)
	v_fmac_f32_e32 v234, v86, v114
	v_fmac_f32_e32 v230, v86, v115
	v_fmac_f32_e32 v229, v86, v116
	v_fmac_f32_e32 v228, v86, v117
	v_fmac_f32_e32 v179, v94, v118
	v_fmac_f32_e32 v178, v94, v119
	v_fmac_f32_e32 v177, v94, v120
	v_fmac_f32_e32 v176, v94, v121
	v_fmac_f32_e32 v224, v94, v114
	v_fmac_f32_e32 v223, v94, v115
	v_fmac_f32_e32 v222, v94, v116
	v_fmac_f32_e32 v217, v94, v117
	v_fmac_f32_e32 v211, v90, v118
	v_fmac_f32_e32 v210, v90, v119
	v_fmac_f32_e32 v209, v90, v120
	v_fmac_f32_e32 v208, v90, v121
	v_fmac_f32_e32 v235, v90, v114
	v_fmac_f32_e32 v233, v90, v115
	v_fmac_f32_e32 v232, v90, v116
	v_fmac_f32_e32 v231, v90, v117
	v_fmac_f32_e32 v188, v70, v118
	v_fmac_f32_e32 v185, v70, v119
	v_fmac_f32_e32 v184, v70, v120
	v_fmac_f32_e32 v182, v70, v121
	v_fmac_f32_e32 v227, v70, v114
	v_fmac_f32_e32 v226, v70, v115
	v_fmac_f32_e32 v225, v70, v116
	v_fmac_f32_e32 v220, v70, v117
	s_waitcnt lgkmcnt(4)
	v_fmac_f32_e32 v175, v87, v126
	v_fmac_f32_e32 v174, v87, v127
	v_fmac_f32_e32 v173, v87, v128
	v_fmac_f32_e32 v159, v87, v129
	ds_read_b128 v[118:121], v145 offset:27648
	ds_read_b128 v[114:117], v169 offset:44032
	v_fmac_f32_e32 v193, v95, v126
	v_fmac_f32_e32 v192, v95, v127
	v_fmac_f32_e32 v189, v95, v128
	v_fmac_f32_e32 v187, v95, v129
	v_fmac_f32_e32 v221, v91, v126
	v_fmac_f32_e32 v219, v91, v127
	v_fmac_f32_e32 v218, v91, v128
	v_fmac_f32_e32 v216, v91, v129
	v_fmac_f32_e32 v199, v71, v126
	v_fmac_f32_e32 v198, v71, v127
	v_fmac_f32_e32 v197, v71, v128
	v_fmac_f32_e32 v196, v71, v129
	ds_read_b128 v[126:129], v170 offset:60416
	s_waitcnt lgkmcnt(6)
	v_fmac_f32_e32 v205, v87, v130
	v_fmac_f32_e32 v204, v87, v131
	v_fmac_f32_e32 v203, v87, v132
	v_fmac_f32_e32 v200, v87, v133
	s_waitcnt lgkmcnt(5)
	v_fmac_f32_e32 v207, v87, v134
	v_fmac_f32_e32 v206, v87, v135
	v_fmac_f32_e32 v202, v87, v136
	v_fmac_f32_e32 v201, v87, v137
	s_waitcnt lgkmcnt(4)
	v_fmac_f32_e32 v234, v87, v138
	v_fmac_f32_e32 v230, v87, v139
	v_fmac_f32_e32 v229, v87, v140
	v_fmac_f32_e32 v228, v87, v141
	v_fmac_f32_e32 v186, v95, v130
	v_fmac_f32_e32 v183, v95, v131
	v_fmac_f32_e32 v181, v95, v132
	v_fmac_f32_e32 v180, v95, v133
	v_fmac_f32_e32 v179, v95, v134
	v_fmac_f32_e32 v178, v95, v135
	v_fmac_f32_e32 v177, v95, v136
	v_fmac_f32_e32 v176, v95, v137
	v_fmac_f32_e32 v224, v95, v138
	v_fmac_f32_e32 v223, v95, v139
	v_fmac_f32_e32 v222, v95, v140
	v_fmac_f32_e32 v217, v95, v141
	v_fmac_f32_e32 v215, v91, v130
	v_fmac_f32_e32 v214, v91, v131
	v_fmac_f32_e32 v213, v91, v132
	v_fmac_f32_e32 v212, v91, v133
	v_fmac_f32_e32 v211, v91, v134
	v_fmac_f32_e32 v210, v91, v135
	v_fmac_f32_e32 v209, v91, v136
	v_fmac_f32_e32 v208, v91, v137
	v_fmac_f32_e32 v235, v91, v138
	v_fmac_f32_e32 v233, v91, v139
	v_fmac_f32_e32 v232, v91, v140
	v_fmac_f32_e32 v231, v91, v141
	v_fmac_f32_e32 v195, v71, v130
	v_fmac_f32_e32 v194, v71, v131
	v_fmac_f32_e32 v191, v71, v132
	v_fmac_f32_e32 v190, v71, v133
	v_fmac_f32_e32 v175, v88, v98
	v_fmac_f32_e32 v174, v88, v99
	v_fmac_f32_e32 v173, v88, v100
	v_fmac_f32_e32 v159, v88, v101
	v_fmac_f32_e32 v205, v88, v102
	v_fmac_f32_e32 v204, v88, v103
	v_fmac_f32_e32 v203, v88, v104
	v_fmac_f32_e32 v200, v88, v105
	v_fmac_f32_e32 v207, v88, v106
	v_fmac_f32_e32 v206, v88, v107
	v_fmac_f32_e32 v202, v88, v108
	v_fmac_f32_e32 v201, v88, v109
	v_fmac_f32_e32 v234, v88, v110
	v_fmac_f32_e32 v230, v88, v111
	v_fmac_f32_e32 v229, v88, v112
	v_fmac_f32_e32 v228, v88, v113
	v_fmac_f32_e32 v193, v96, v98
	v_fmac_f32_e32 v192, v96, v99
	v_fmac_f32_e32 v189, v96, v100
	v_fmac_f32_e32 v187, v96, v101
	v_fmac_f32_e32 v186, v96, v102
	v_fmac_f32_e32 v183, v96, v103
	v_fmac_f32_e32 v181, v96, v104
	v_fmac_f32_e32 v180, v96, v105
	v_fmac_f32_e32 v179, v96, v106
	v_fmac_f32_e32 v178, v96, v107
	v_fmac_f32_e32 v177, v96, v108
	v_fmac_f32_e32 v176, v96, v109
	v_fmac_f32_e32 v224, v96, v110
	v_fmac_f32_e32 v223, v96, v111
	v_fmac_f32_e32 v222, v96, v112
	v_fmac_f32_e32 v217, v96, v113
	v_fmac_f32_e32 v221, v92, v98
	v_fmac_f32_e32 v219, v92, v99
	v_fmac_f32_e32 v218, v92, v100
	v_fmac_f32_e32 v216, v92, v101
	v_fmac_f32_e32 v215, v92, v102
	v_fmac_f32_e32 v214, v92, v103
	v_fmac_f32_e32 v213, v92, v104
	v_fmac_f32_e32 v212, v92, v105
	v_fmac_f32_e32 v211, v92, v106
	v_fmac_f32_e32 v210, v92, v107
	v_fmac_f32_e32 v209, v92, v108
	v_fmac_f32_e32 v208, v92, v109
	v_fmac_f32_e32 v235, v92, v110
	v_fmac_f32_e32 v233, v92, v111
	v_fmac_f32_e32 v232, v92, v112
	v_fmac_f32_e32 v231, v92, v113
	v_fmac_f32_e32 v199, v72, v98
	v_fmac_f32_e32 v198, v72, v99
	v_fmac_f32_e32 v197, v72, v100
	v_fmac_f32_e32 v196, v72, v101
	v_fmac_f32_e32 v195, v72, v102
	v_fmac_f32_e32 v194, v72, v103
	v_fmac_f32_e32 v191, v72, v104
	v_fmac_f32_e32 v190, v72, v105
	s_waitcnt lgkmcnt(3)
	v_fmac_f32_e32 v175, v89, v122
	v_fmac_f32_e32 v174, v89, v123
	v_fmac_f32_e32 v173, v89, v124
	v_fmac_f32_e32 v159, v89, v125
	s_waitcnt lgkmcnt(2)
	v_fmac_f32_e32 v205, v89, v118
	v_fmac_f32_e32 v204, v89, v119
	v_fmac_f32_e32 v203, v89, v120
	v_fmac_f32_e32 v200, v89, v121
	s_waitcnt lgkmcnt(1)
	v_fmac_f32_e32 v207, v89, v114
	v_fmac_f32_e32 v206, v89, v115
	v_fmac_f32_e32 v202, v89, v116
	v_fmac_f32_e32 v201, v89, v117
	s_waitcnt lgkmcnt(0)
	v_fmac_f32_e32 v234, v89, v126
	v_fmac_f32_e32 v230, v89, v127
	v_fmac_f32_e32 v229, v89, v128
	v_fmac_f32_e32 v228, v89, v129
	v_fmac_f32_e32 v193, v97, v122
	v_fmac_f32_e32 v192, v97, v123
	v_fmac_f32_e32 v189, v97, v124
	v_fmac_f32_e32 v187, v97, v125
	v_fmac_f32_e32 v186, v97, v118
	v_fmac_f32_e32 v183, v97, v119
	v_fmac_f32_e32 v181, v97, v120
	v_fmac_f32_e32 v180, v97, v121
	v_fmac_f32_e32 v179, v97, v114
	v_fmac_f32_e32 v178, v97, v115
	v_fmac_f32_e32 v177, v97, v116
	v_fmac_f32_e32 v176, v97, v117
	v_fmac_f32_e32 v224, v97, v126
	v_fmac_f32_e32 v223, v97, v127
	v_fmac_f32_e32 v222, v97, v128
	v_fmac_f32_e32 v217, v97, v129
	v_fmac_f32_e32 v221, v93, v122
	v_fmac_f32_e32 v219, v93, v123
	v_fmac_f32_e32 v218, v93, v124
	v_fmac_f32_e32 v216, v93, v125
	v_fmac_f32_e32 v215, v93, v118
	v_fmac_f32_e32 v214, v93, v119
	v_fmac_f32_e32 v213, v93, v120
	v_fmac_f32_e32 v212, v93, v121
	v_fmac_f32_e32 v211, v93, v114
	v_fmac_f32_e32 v210, v93, v115
	v_fmac_f32_e32 v209, v93, v116
	v_fmac_f32_e32 v208, v93, v117
	v_fmac_f32_e32 v235, v93, v126
	v_fmac_f32_e32 v233, v93, v127
	v_fmac_f32_e32 v232, v93, v128
	v_fmac_f32_e32 v231, v93, v129
	ds_read_b128 v[98:101], v1 offset:12288
	ds_read_b128 v[94:97], v161 offset:28672
	ds_read_b128 v[90:93], v168 offset:45056
	ds_read_b128 v[86:89], v163 offset:61440
	ds_read_b128 v[102:105], v1 offset:14336
	v_fmac_f32_e32 v188, v71, v134
	v_fmac_f32_e32 v185, v71, v135
	v_fmac_f32_e32 v184, v71, v136
	v_fmac_f32_e32 v182, v71, v137
	v_fmac_f32_e32 v227, v71, v138
	v_fmac_f32_e32 v226, v71, v139
	v_fmac_f32_e32 v225, v71, v140
	v_fmac_f32_e32 v220, v71, v141
	v_fmac_f32_e32 v188, v72, v106
	v_fmac_f32_e32 v185, v72, v107
	v_fmac_f32_e32 v184, v72, v108
	v_fmac_f32_e32 v182, v72, v109
	v_fmac_f32_e32 v227, v72, v110
	v_fmac_f32_e32 v226, v72, v111
	v_fmac_f32_e32 v225, v72, v112
	v_fmac_f32_e32 v220, v72, v113
	v_fmac_f32_e32 v199, v73, v122
	v_fmac_f32_e32 v198, v73, v123
	v_fmac_f32_e32 v197, v73, v124
	v_fmac_f32_e32 v196, v73, v125
	v_fmac_f32_e32 v195, v73, v118
	v_fmac_f32_e32 v194, v73, v119
	v_fmac_f32_e32 v191, v73, v120
	v_fmac_f32_e32 v190, v73, v121
	v_fmac_f32_e32 v188, v73, v114
	v_fmac_f32_e32 v185, v73, v115
	v_fmac_f32_e32 v184, v73, v116
	v_fmac_f32_e32 v182, v73, v117
	v_fmac_f32_e32 v227, v73, v126
	v_fmac_f32_e32 v226, v73, v127
	v_fmac_f32_e32 v225, v73, v128
	v_fmac_f32_e32 v220, v73, v129
	s_waitcnt lgkmcnt(4)
	v_fmac_f32_e32 v175, v74, v98
	v_fmac_f32_e32 v174, v74, v99
	v_fmac_f32_e32 v173, v74, v100
	v_fmac_f32_e32 v159, v74, v101
	ds_read_b128 v[106:109], v161 offset:30720
	ds_read_b128 v[114:117], v163 offset:63488
	s_waitcnt lgkmcnt(5)
	v_fmac_f32_e32 v205, v74, v94
	v_fmac_f32_e32 v204, v74, v95
	v_fmac_f32_e32 v203, v74, v96
	v_fmac_f32_e32 v200, v74, v97
	ds_read_b128 v[110:113], v168 offset:47104
	s_waitcnt lgkmcnt(5)
	v_fmac_f32_e32 v207, v74, v90
	v_fmac_f32_e32 v206, v74, v91
	v_fmac_f32_e32 v202, v74, v92
	v_fmac_f32_e32 v201, v74, v93
	s_waitcnt lgkmcnt(4)
	v_fmac_f32_e32 v234, v74, v86
	v_fmac_f32_e32 v230, v74, v87
	v_fmac_f32_e32 v229, v74, v88
	v_fmac_f32_e32 v228, v74, v89
	v_fmac_f32_e32 v193, v82, v98
	v_fmac_f32_e32 v192, v82, v99
	v_fmac_f32_e32 v189, v82, v100
	v_fmac_f32_e32 v187, v82, v101
	v_fmac_f32_e32 v186, v82, v94
	v_fmac_f32_e32 v183, v82, v95
	v_fmac_f32_e32 v181, v82, v96
	v_fmac_f32_e32 v180, v82, v97
	v_fmac_f32_e32 v179, v82, v90
	v_fmac_f32_e32 v178, v82, v91
	v_fmac_f32_e32 v177, v82, v92
	v_fmac_f32_e32 v176, v82, v93
	v_fmac_f32_e32 v224, v82, v86
	v_fmac_f32_e32 v223, v82, v87
	v_fmac_f32_e32 v222, v82, v88
	v_fmac_f32_e32 v217, v82, v89
	v_fmac_f32_e32 v221, v78, v98
	v_fmac_f32_e32 v219, v78, v99
	v_fmac_f32_e32 v218, v78, v100
	v_fmac_f32_e32 v216, v78, v101
	v_fmac_f32_e32 v215, v78, v94
	v_fmac_f32_e32 v214, v78, v95
	v_fmac_f32_e32 v213, v78, v96
	v_fmac_f32_e32 v212, v78, v97
	v_fmac_f32_e32 v211, v78, v90
	v_fmac_f32_e32 v210, v78, v91
	v_fmac_f32_e32 v209, v78, v92
	v_fmac_f32_e32 v208, v78, v93
	v_fmac_f32_e32 v235, v78, v86
	v_fmac_f32_e32 v233, v78, v87
	v_fmac_f32_e32 v232, v78, v88
	v_fmac_f32_e32 v231, v78, v89
	v_fmac_f32_e32 v199, v66, v98
	v_fmac_f32_e32 v198, v66, v99
	v_fmac_f32_e32 v197, v66, v100
	v_fmac_f32_e32 v196, v66, v101
	v_fmac_f32_e32 v195, v66, v94
	v_fmac_f32_e32 v194, v66, v95
	v_fmac_f32_e32 v191, v66, v96
	v_fmac_f32_e32 v190, v66, v97
	v_fmac_f32_e32 v188, v66, v90
	v_fmac_f32_e32 v185, v66, v91
	v_fmac_f32_e32 v184, v66, v92
	v_fmac_f32_e32 v182, v66, v93
	v_fmac_f32_e32 v227, v66, v86
	v_fmac_f32_e32 v226, v66, v87
	v_fmac_f32_e32 v225, v66, v88
	v_fmac_f32_e32 v220, v66, v89
	ds_read_b128 v[90:93], v144 offset:13312
	ds_read_b128 v[94:97], v145 offset:29696
	ds_read_b128 v[98:101], v169 offset:46080
	ds_read_b128 v[118:121], v170 offset:62464
	ds_read_b128 v[86:89], v144 offset:15360
	ds_read_b128 v[122:125], v145 offset:31744
	ds_read_b128 v[126:129], v169 offset:48128
	ds_read_b128 v[130:133], v170 offset:64512
	s_waitcnt lgkmcnt(7)
	v_fmac_f32_e32 v175, v75, v90
	v_fmac_f32_e32 v174, v75, v91
	v_fmac_f32_e32 v173, v75, v92
	v_fmac_f32_e32 v159, v75, v93
	s_waitcnt lgkmcnt(6)
	v_fmac_f32_e32 v205, v75, v94
	v_fmac_f32_e32 v204, v75, v95
	v_fmac_f32_e32 v203, v75, v96
	v_fmac_f32_e32 v200, v75, v97
	s_waitcnt lgkmcnt(5)
	v_fmac_f32_e32 v207, v75, v98
	v_fmac_f32_e32 v206, v75, v99
	v_fmac_f32_e32 v202, v75, v100
	v_fmac_f32_e32 v201, v75, v101
	s_waitcnt lgkmcnt(4)
	v_fmac_f32_e32 v234, v75, v118
	v_fmac_f32_e32 v230, v75, v119
	v_fmac_f32_e32 v229, v75, v120
	v_fmac_f32_e32 v228, v75, v121
	v_mbcnt_lo_u32_b32 v75, -1, 0
	v_fmac_f32_e32 v175, v76, v102
	v_fmac_f32_e32 v174, v76, v103
	v_fmac_f32_e32 v173, v76, v104
	v_fmac_f32_e32 v159, v76, v105
	v_fmac_f32_e32 v205, v76, v106
	v_fmac_f32_e32 v204, v76, v107
	v_fmac_f32_e32 v203, v76, v108
	v_fmac_f32_e32 v200, v76, v109
	v_fmac_f32_e32 v207, v76, v110
	v_fmac_f32_e32 v206, v76, v111
	v_fmac_f32_e32 v202, v76, v112
	v_fmac_f32_e32 v201, v76, v113
	v_fmac_f32_e32 v234, v76, v114
	v_fmac_f32_e32 v230, v76, v115
	v_fmac_f32_e32 v229, v76, v116
	v_fmac_f32_e32 v228, v76, v117
	v_mbcnt_hi_u32_b32 v75, -1, v75
	s_waitcnt lgkmcnt(3)
	v_fmac_f32_e32 v175, v77, v86
	v_fmac_f32_e32 v174, v77, v87
	v_fmac_f32_e32 v173, v77, v88
	v_fmac_f32_e32 v159, v77, v89
	s_waitcnt lgkmcnt(2)
	v_fmac_f32_e32 v205, v77, v122
	v_fmac_f32_e32 v204, v77, v123
	v_fmac_f32_e32 v203, v77, v124
	v_fmac_f32_e32 v200, v77, v125
	s_waitcnt lgkmcnt(1)
	v_fmac_f32_e32 v207, v77, v126
	v_fmac_f32_e32 v206, v77, v127
	v_fmac_f32_e32 v202, v77, v128
	v_fmac_f32_e32 v201, v77, v129
	s_waitcnt lgkmcnt(0)
	v_fmac_f32_e32 v234, v77, v130
	v_fmac_f32_e32 v230, v77, v131
	v_fmac_f32_e32 v229, v77, v132
	v_fmac_f32_e32 v228, v77, v133
	v_and_b32_e32 v77, 64, v75
	v_fmac_f32_e32 v221, v79, v90
	v_xor_b32_e32 v76, 32, v75
	v_add_u32_e32 v77, 64, v77
	v_fmac_f32_e32 v224, v83, v118
	v_fmac_f32_e32 v219, v79, v91
	v_fmac_f32_e32 v235, v79, v118
	v_fmac_f32_e32 v227, v67, v118
	v_fmac_f32_e32 v221, v80, v102
	v_and_b32_e32 v74, 32, v0
	v_cmp_lt_i32_e32 vcc, v76, v77
	v_fmac_f32_e32 v218, v79, v92
	v_fmac_f32_e32 v224, v84, v114
	v_fmac_f32_e32 v219, v80, v103
	v_fmac_f32_e32 v235, v80, v114
	v_fmac_f32_e32 v227, v68, v114
	v_fmac_f32_e32 v221, v81, v86
	v_cndmask_b32_e32 v76, v75, v76, vcc
	v_cmp_eq_u32_e64 s[16:17], 0, v74
	v_fmac_f32_e32 v218, v80, v104
	v_fmac_f32_e32 v224, v85, v130
	v_fmac_f32_e32 v219, v81, v87
	v_fmac_f32_e32 v235, v81, v130
	v_fmac_f32_e32 v227, v69, v130
	v_lshlrev_b32_e32 v130, 2, v76
	v_fmac_f32_e32 v218, v81, v88
	v_fmac_f32_e32 v216, v79, v93
	v_fmac_f32_e32 v215, v79, v94
	v_fmac_f32_e32 v214, v79, v95
	v_fmac_f32_e32 v213, v79, v96
	v_fmac_f32_e32 v212, v79, v97
	v_fmac_f32_e32 v211, v79, v98
	v_fmac_f32_e32 v210, v79, v99
	v_fmac_f32_e32 v209, v79, v100
	v_fmac_f32_e32 v208, v79, v101
	v_fmac_f32_e32 v233, v79, v119
	v_fmac_f32_e32 v232, v79, v120
	v_fmac_f32_e32 v231, v79, v121
	v_permlane32_swap_b32_e32 v175, v221
	v_add_f32_e32 v74, v175, v221
	v_fmac_f32_e32 v216, v80, v105
	s_waitcnt lgkmcnt(0)
	v_permlane32_swap_b32_e32 v174, v219
	v_add_f32_e32 v76, v174, v219
	v_fmac_f32_e32 v215, v80, v106
	v_fmac_f32_e32 v216, v81, v89
	s_waitcnt lgkmcnt(0)
	v_permlane32_swap_b32_e32 v173, v218
	v_add_f32_e32 v78, v173, v218
	v_fmac_f32_e32 v214, v80, v107
	v_fmac_f32_e32 v213, v80, v108
	v_fmac_f32_e32 v212, v80, v109
	v_fmac_f32_e32 v211, v80, v110
	v_fmac_f32_e32 v210, v80, v111
	v_fmac_f32_e32 v209, v80, v112
	v_fmac_f32_e32 v208, v80, v113
	v_fmac_f32_e32 v233, v80, v115
	v_fmac_f32_e32 v232, v80, v116
	v_fmac_f32_e32 v231, v80, v117
	v_fmac_f32_e32 v215, v81, v122
	s_waitcnt lgkmcnt(0)
	v_fmac_f32_e32 v214, v81, v123
	v_fmac_f32_e32 v213, v81, v124
	v_fmac_f32_e32 v212, v81, v125
	v_fmac_f32_e32 v211, v81, v126
	v_fmac_f32_e32 v210, v81, v127
	v_fmac_f32_e32 v209, v81, v128
	v_fmac_f32_e32 v208, v81, v129
	v_fmac_f32_e32 v233, v81, v131
	v_fmac_f32_e32 v232, v81, v132
	v_fmac_f32_e32 v231, v81, v133
	v_permlane32_swap_b32_e32 v159, v216
	v_add_f32_e32 v79, v159, v216
	s_waitcnt lgkmcnt(0)
	v_permlane32_swap_b32_e32 v205, v215
	v_add_f32_e32 v80, v205, v215
	s_waitcnt lgkmcnt(0)
	v_permlane32_swap_b32_e32 v204, v214
	v_add_f32_e32 v81, v204, v214
	v_fmac_f32_e32 v193, v83, v90
	v_fmac_f32_e32 v192, v83, v91
	v_fmac_f32_e32 v189, v83, v92
	v_fmac_f32_e32 v187, v83, v93
	v_fmac_f32_e32 v186, v83, v94
	v_fmac_f32_e32 v183, v83, v95
	v_fmac_f32_e32 v181, v83, v96
	v_fmac_f32_e32 v180, v83, v97
	v_fmac_f32_e32 v179, v83, v98
	v_fmac_f32_e32 v178, v83, v99
	v_fmac_f32_e32 v177, v83, v100
	v_fmac_f32_e32 v176, v83, v101
	v_fmac_f32_e32 v223, v83, v119
	v_fmac_f32_e32 v222, v83, v120
	v_fmac_f32_e32 v217, v83, v121
	s_waitcnt lgkmcnt(0)
	v_fmac_f32_e32 v193, v84, v102
	v_fmac_f32_e32 v192, v84, v103
	v_fmac_f32_e32 v189, v84, v104
	v_fmac_f32_e32 v187, v84, v105
	v_fmac_f32_e32 v186, v84, v106
	v_fmac_f32_e32 v183, v84, v107
	v_fmac_f32_e32 v181, v84, v108
	v_fmac_f32_e32 v180, v84, v109
	v_fmac_f32_e32 v179, v84, v110
	v_fmac_f32_e32 v178, v84, v111
	v_fmac_f32_e32 v177, v84, v112
	v_fmac_f32_e32 v176, v84, v113
	v_fmac_f32_e32 v223, v84, v115
	v_fmac_f32_e32 v222, v84, v116
	v_fmac_f32_e32 v217, v84, v117
	v_fmac_f32_e32 v193, v85, v86
	v_fmac_f32_e32 v192, v85, v87
	v_fmac_f32_e32 v189, v85, v88
	v_fmac_f32_e32 v187, v85, v89
	v_fmac_f32_e32 v186, v85, v122
	v_fmac_f32_e32 v183, v85, v123
	v_fmac_f32_e32 v181, v85, v124
	v_fmac_f32_e32 v180, v85, v125
	v_fmac_f32_e32 v179, v85, v126
	v_fmac_f32_e32 v178, v85, v127
	v_fmac_f32_e32 v177, v85, v128
	v_fmac_f32_e32 v176, v85, v129
	v_fmac_f32_e32 v223, v85, v131
	v_fmac_f32_e32 v222, v85, v132
	v_fmac_f32_e32 v217, v85, v133
	v_permlane32_swap_b32_e32 v203, v213
	v_add_f32_e32 v82, v203, v213
	s_waitcnt lgkmcnt(0)
	v_permlane32_swap_b32_e32 v200, v212
	v_add_f32_e32 v83, v200, v212
	v_fmac_f32_e32 v198, v67, v91
	s_waitcnt lgkmcnt(0)
	v_permlane32_swap_b32_e32 v207, v211
	v_add_f32_e32 v84, v207, v211
	v_fmac_f32_e32 v197, v67, v92
	v_fmac_f32_e32 v198, v68, v103
	s_waitcnt lgkmcnt(0)
	v_fmac_f32_e32 v197, v68, v104
	v_fmac_f32_e32 v198, v69, v87
	v_fmac_f32_e32 v197, v69, v88
	v_fmac_f32_e32 v199, v67, v90
	v_fmac_f32_e32 v199, v68, v102
	v_fmac_f32_e32 v199, v69, v86
	v_permlane32_swap_b32_e32 v206, v210
	v_add_f32_e32 v85, v206, v210
	s_waitcnt lgkmcnt(0)
	v_permlane32_swap_b32_e32 v202, v209
	v_add_f32_e32 v86, v202, v209
	s_waitcnt lgkmcnt(0)
	v_permlane32_swap_b32_e32 v201, v208
	v_add_f32_e32 v87, v201, v208
	s_waitcnt lgkmcnt(0)
	v_fmac_f32_e32 v196, v67, v93
	v_fmac_f32_e32 v196, v68, v105
	v_fmac_f32_e32 v196, v69, v89
	v_permlane32_swap_b32_e32 v234, v235
	v_add_f32_e32 v88, v234, v235
	s_waitcnt lgkmcnt(0)
	v_permlane32_swap_b32_e32 v230, v233
	v_add_f32_e32 v89, v230, v233
	s_waitcnt lgkmcnt(0)
	v_permlane32_swap_b32_e32 v229, v232
	v_add_f32_e32 v90, v229, v232
	s_waitcnt lgkmcnt(0)
	v_fmac_f32_e32 v195, v67, v94
	v_permlane32_swap_b32_e32 v228, v231
	v_add_f32_e32 v91, v228, v231
	s_waitcnt lgkmcnt(0)
	v_permlane32_swap_b32_e32 v193, v199
	v_add_f32_e32 v92, v193, v199
	s_waitcnt lgkmcnt(0)
	v_permlane32_swap_b32_e32 v192, v198
	v_add_f32_e32 v93, v192, v198
	v_fmac_f32_e32 v195, v68, v106
	s_waitcnt lgkmcnt(0)
	v_fmac_f32_e32 v191, v67, v96
	v_fmac_f32_e32 v195, v69, v122
	v_fmac_f32_e32 v190, v67, v97
	v_fmac_f32_e32 v194, v67, v95
	v_permlane32_swap_b32_e32 v189, v197
	v_add_f32_e32 v94, v189, v197
	v_fmac_f32_e32 v194, v68, v107
	s_waitcnt lgkmcnt(0)
	v_permlane32_swap_b32_e32 v187, v196
	v_add_f32_e32 v95, v187, v196
	v_fmac_f32_e32 v191, v68, v108
	v_fmac_f32_e32 v194, v69, v123
	s_waitcnt lgkmcnt(0)
	v_permlane32_swap_b32_e32 v186, v195
	v_add_f32_e32 v96, v186, v195
	v_fmac_f32_e32 v190, v68, v109
	v_fmac_f32_e32 v191, v69, v124
	s_waitcnt lgkmcnt(0)
	v_fmac_f32_e32 v185, v67, v99
	v_fmac_f32_e32 v190, v69, v125
	v_fmac_f32_e32 v184, v67, v100
	v_fmac_f32_e32 v188, v67, v98
	v_fmac_f32_e32 v188, v68, v110
	v_xor_b32_e32 v110, 16, v75
	v_fmac_f32_e32 v226, v67, v119
	v_permlane32_swap_b32_e32 v183, v194
	v_add_f32_e32 v97, v183, v194
	v_and_b32_e32 v109, 16, v0
	v_cmp_lt_i32_e32 vcc, v110, v77
	v_fmac_f32_e32 v226, v68, v115
	s_waitcnt lgkmcnt(0)
	v_permlane32_swap_b32_e32 v181, v191
	v_add_f32_e32 v98, v181, v191
	v_cndmask_b32_e32 v110, v75, v110, vcc
	v_cmp_eq_u32_e64 s[4:5], 0, v109
	v_fmac_f32_e32 v185, v68, v111
	v_fmac_f32_e32 v226, v69, v131
	v_fmac_f32_e32 v188, v69, v126
	s_waitcnt lgkmcnt(0)
	v_permlane32_swap_b32_e32 v180, v190
	v_add_f32_e32 v99, v180, v190
	v_lshlrev_b32_e32 v131, 2, v110
	v_permlane16_swap_b32_e32 v74, v92
	v_add_f32_e32 v74, v74, v92
	v_permlane16_swap_b32_e32 v76, v93
	v_add_f32_e32 v76, v76, v93
	v_fmac_f32_e32 v184, v68, v112
	v_fmac_f32_e32 v185, v69, v127
	s_waitcnt lgkmcnt(0)
	v_fmac_f32_e32 v184, v69, v128
	v_permlane16_swap_b32_e32 v78, v94
	v_add_f32_e32 v78, v78, v94
	v_fmac_f32_e32 v182, v67, v101
	v_permlane32_swap_b32_e32 v179, v188
	v_add_f32_e32 v100, v179, v188
	s_waitcnt lgkmcnt(0)
	v_fmac_f32_e32 v182, v68, v113
	s_waitcnt lgkmcnt(0)
	v_permlane32_swap_b32_e32 v178, v185
	v_add_f32_e32 v101, v178, v185
	s_waitcnt lgkmcnt(0)
	v_fmac_f32_e32 v182, v69, v129
	s_waitcnt lgkmcnt(0)
	v_permlane32_swap_b32_e32 v177, v184
	v_add_f32_e32 v102, v177, v184
	s_waitcnt lgkmcnt(0)
	v_permlane16_swap_b32_e32 v81, v97
	v_add_f32_e32 v81, v81, v97
	v_permlane16_swap_b32_e32 v80, v96
	v_add_f32_e32 v80, v80, v96
	s_waitcnt lgkmcnt(0)
	s_waitcnt lgkmcnt(0)
	v_fmac_f32_e32 v225, v67, v120
	v_permlane32_swap_b32_e32 v176, v182
	v_add_f32_e32 v103, v176, v182
	v_fmac_f32_e32 v225, v68, v116
	s_waitcnt lgkmcnt(0)
	v_permlane32_swap_b32_e32 v224, v227
	v_add_f32_e32 v104, v224, v227
	v_fmac_f32_e32 v225, v69, v132
	s_waitcnt lgkmcnt(0)
	v_permlane32_swap_b32_e32 v223, v226
	v_add_f32_e32 v105, v223, v226
	s_waitcnt lgkmcnt(0)
	v_permlane16_swap_b32_e32 v84, v100
	v_add_f32_e32 v84, v84, v100
	v_permlane16_swap_b32_e32 v83, v99
	v_add_f32_e32 v83, v83, v99
	s_waitcnt lgkmcnt(0)
	s_waitcnt lgkmcnt(0)
	v_permlane32_swap_b32_e32 v222, v225
	v_add_f32_e32 v106, v222, v225
	v_fmac_f32_e32 v220, v67, v121
	s_waitcnt lgkmcnt(0)
	v_permlane16_swap_b32_e32 v87, v103
	v_add_f32_e32 v87, v87, v103
	v_fmac_f32_e32 v220, v68, v117
	v_permlane16_swap_b32_e32 v86, v102
	v_add_f32_e32 v86, v86, v102
	s_waitcnt lgkmcnt(0)
	v_fmac_f32_e32 v220, v69, v133
	s_waitcnt lgkmcnt(0)
	v_permlane16_swap_b32_e32 v82, v98
	v_add_f32_e32 v82, v82, v98
	s_waitcnt lgkmcnt(0)
	v_permlane16_swap_b32_e32 v90, v106
	v_add_f32_e32 v90, v90, v106
	v_permlane16_swap_b32_e32 v89, v105
	v_add_f32_e32 v89, v89, v105
	s_waitcnt lgkmcnt(0)
	v_xor_b32_e32 v93, 8, v75
	v_permlane32_swap_b32_e32 v217, v220
	v_add_f32_e32 v107, v217, v220
	s_waitcnt lgkmcnt(0)
	v_and_b32_e32 v92, 8, v0
	v_cmp_lt_i32_e32 vcc, v93, v77
	s_waitcnt lgkmcnt(0)
	s_waitcnt lgkmcnt(0)
	v_cndmask_b32_e32 v93, v75, v93, vcc
	v_cmp_eq_u32_e64 s[8:9], 0, v92
	v_lshlrev_b32_e32 v133, 2, v93
	v_permlane16_swap_b32_e32 v85, v101
	v_add_f32_e32 v85, v85, v101
	v_add_f32_dpp v74, v74, v74 row_ror:8 row_mask:0xf bank_mask:0xf
	v_add_f32_dpp v84, v84, v84 row_ror:8 row_mask:0xf bank_mask:0xf
	v_cndmask_b32_e64 v74, v84, v74, s[8:9]
	s_waitcnt lgkmcnt(0)
	v_permlane16_swap_b32_e32 v79, v95
	v_add_f32_e32 v79, v79, v95
	s_waitcnt lgkmcnt(0)
	s_waitcnt lgkmcnt(0)
	v_permlane16_swap_b32_e32 v88, v104
	v_add_f32_e32 v88, v88, v104
	s_waitcnt lgkmcnt(0)
	v_add_f32_dpp v76, v76, v76 row_ror:8 row_mask:0xf bank_mask:0xf
	v_add_f32_dpp v85, v85, v85 row_ror:8 row_mask:0xf bank_mask:0xf
	v_cndmask_b32_e64 v76, v85, v76, s[8:9]
	v_add_f32_dpp v78, v78, v78 row_ror:8 row_mask:0xf bank_mask:0xf
	v_add_f32_dpp v86, v86, v86 row_ror:8 row_mask:0xf bank_mask:0xf
	v_cndmask_b32_e64 v78, v86, v78, s[8:9]
	v_add_f32_dpp v79, v79, v79 row_ror:8 row_mask:0xf bank_mask:0xf
	v_add_f32_dpp v87, v87, v87 row_ror:8 row_mask:0xf bank_mask:0xf
	v_cndmask_b32_e64 v79, v87, v79, s[8:9]
	s_waitcnt lgkmcnt(0)
	v_permlane16_swap_b32_e32 v91, v107
	v_add_f32_e32 v91, v91, v107
	s_waitcnt lgkmcnt(0)
	v_add_f32_dpp v80, v80, v80 row_ror:8 row_mask:0xf bank_mask:0xf
	v_add_f32_dpp v88, v88, v88 row_ror:8 row_mask:0xf bank_mask:0xf
	v_cndmask_b32_e64 v80, v88, v80, s[8:9]
	s_waitcnt lgkmcnt(0)
	v_add_f32_dpp v81, v81, v81 row_ror:8 row_mask:0xf bank_mask:0xf
	v_add_f32_dpp v89, v89, v89 row_ror:8 row_mask:0xf bank_mask:0xf
	v_cndmask_b32_e64 v81, v89, v81, s[8:9]
	v_xor_b32_e32 v87, 4, v75
	s_waitcnt lgkmcnt(0)
	v_add_f32_dpp v82, v82, v82 row_ror:8 row_mask:0xf bank_mask:0xf
	v_add_f32_dpp v90, v90, v90 row_ror:8 row_mask:0xf bank_mask:0xf
	v_cndmask_b32_e64 v82, v90, v82, s[8:9]
	v_and_b32_e32 v86, 4, v0
	v_cmp_lt_i32_e32 vcc, v87, v77
	s_waitcnt lgkmcnt(0)
	s_waitcnt lgkmcnt(0)
	v_cndmask_b32_e32 v87, v75, v87, vcc
	v_cmp_eq_u32_e64 s[10:11], 0, v86
	s_waitcnt lgkmcnt(0)
	v_lshlrev_b32_e32 v134, 2, v87
	v_cndmask_b32_e64 v86, v74, v80, s[10:11]
	v_cndmask_b32_e64 v74, v80, v74, s[10:11]
	v_cndmask_b32_e64 v80, v76, v81, s[10:11]
	v_cndmask_b32_e64 v76, v81, v76, s[10:11]
	v_cndmask_b32_e64 v81, v78, v82, s[10:11]
	v_add_f32_dpp v83, v83, v83 row_ror:8 row_mask:0xf bank_mask:0xf
	v_add_f32_dpp v91, v91, v91 row_ror:8 row_mask:0xf bank_mask:0xf
	v_cndmask_b32_e64 v83, v91, v83, s[8:9]
	ds_bpermute_b32 v81, v134, v81
	s_waitcnt lgkmcnt(0)
	ds_bpermute_b32 v80, v134, v80
	ds_bpermute_b32 v86, v134, v86
	v_cndmask_b32_e64 v84, v79, v83, s[10:11]
	ds_bpermute_b32 v84, v134, v84
	v_cndmask_b32_e64 v78, v82, v78, s[10:11]
	s_waitcnt lgkmcnt(0)
	v_add_f32_e32 v78, v78, v81
	v_xor_b32_e32 v81, 2, v75
	s_waitcnt lgkmcnt(0)
	v_add_f32_e32 v76, v76, v80
	v_and_b32_e32 v80, 2, v0
	v_cmp_lt_i32_e32 vcc, v81, v77
	s_waitcnt lgkmcnt(0)
	v_add_f32_e32 v74, v74, v86
	v_cndmask_b32_e64 v79, v83, v79, s[10:11]
	v_cndmask_b32_e32 v81, v75, v81, vcc
	v_cmp_eq_u32_e64 s[14:15], 0, v80
	s_waitcnt lgkmcnt(0)
	v_add_f32_e32 v79, v79, v84
	v_lshlrev_b32_e32 v135, 2, v81
	v_cndmask_b32_e64 v80, v74, v78, s[14:15]
	ds_bpermute_b32 v80, v135, v80
	v_cndmask_b32_e64 v81, v76, v79, s[14:15]
	ds_bpermute_b32 v81, v135, v81
	v_cvt_pk_f16_f32 v73, v72, v73
	v_cndmask_b32_e64 v72, v78, v74, s[14:15]
	s_waitcnt lgkmcnt(0)
	v_add_f32_e32 v74, v72, v80
	v_cndmask_b32_e64 v72, v79, v76, s[14:15]
	s_waitcnt lgkmcnt(0)
	v_add_f32_e32 v76, v72, v81
	v_xor_b32_e32 v72, 1, v75
	v_and_b32_e32 v132, 1, v0
	v_cmp_lt_i32_e32 vcc, v72, v77
	v_cmp_eq_u32_e64 s[6:7], 0, v132
	v_and_b32_e32 v139, 15, v0
	v_cndmask_b32_e32 v72, v75, v72, vcc
	v_lshlrev_b32_e32 v136, 2, v72
	v_cvt_pk_f16_f32 v72, v70, v71
	global_store_dwordx2 v[142:143], v[72:73], off offset:1024 sc1
	v_cvt_pk_f16_f32 v73, v68, v69
	v_add_f32_dpp v74, v74, v74 quad_perm:[1,0,3,2] row_mask:0xf bank_mask:0xf
	v_add_f32_dpp v76, v76, v76 quad_perm:[1,0,3,2] row_mask:0xf bank_mask:0xf
	v_cndmask_b32_e64 v68, v76, v74, s[6:7]
	s_waitcnt lgkmcnt(0)
	ds_bpermute_b32 v69, v136, v68
	ds_bpermute_b32 v71, v136, v139
	v_cvt_pk_f16_f32 v72, v66, v67
	global_store_dwordx2 v[142:143], v[72:73], off offset:1536 sc1
	s_waitcnt lgkmcnt(1)
	v_cmp_lt_f32_e64 s[18:19], v68, v69
	v_cmp_nlt_f32_e32 vcc, v68, v69
	s_and_saveexec_b64 s[22:23], vcc
	s_cbranch_execz .LBB1_7
	v_cmp_eq_f32_e32 vcc, v68, v69
	s_waitcnt lgkmcnt(0)
	v_cmp_lt_i32_e64 s[12:13], v71, v139
	s_and_b64 s[12:13], s[12:13], vcc
	s_andn2_b64 s[18:19], s[18:19], exec
	s_and_b64 s[12:13], s[12:13], exec
	s_or_b64 s[18:19], s[18:19], s[12:13]

.LBB1_9:
	s_or_b64 exec, exec, s[12:13]
	ds_bpermute_b32 v69, v135, v67
	s_waitcnt lgkmcnt(0)
	ds_bpermute_b32 v71, v135, v70
	s_waitcnt lgkmcnt(0)
	v_cmp_lt_f32_e64 s[18:19], v66, v69
	v_cmp_nlt_f32_e32 vcc, v66, v69
	s_and_saveexec_b64 s[22:23], vcc
	s_cbranch_execz .LBB1_11
	v_cmp_eq_f32_e32 vcc, v66, v69
	s_waitcnt lgkmcnt(0)
	v_cmp_lt_i32_e64 s[12:13], v71, v70
	s_and_b64 s[12:13], vcc, s[12:13]
	s_andn2_b64 s[18:19], s[18:19], exec
	s_and_b64 s[12:13], s[12:13], exec
	s_or_b64 s[18:19], s[18:19], s[12:13]

.LBB1_13:
	s_or_b64 exec, exec, s[12:13]
	ds_bpermute_b32 v69, v134, v67
	s_waitcnt lgkmcnt(0)
	ds_bpermute_b32 v71, v134, v70
	s_waitcnt lgkmcnt(0)
	v_cmp_lt_f32_e64 s[18:19], v66, v69
	v_cmp_nlt_f32_e32 vcc, v66, v69
	s_and_saveexec_b64 s[22:23], vcc
	s_cbranch_execz .LBB1_15
	v_cmp_eq_f32_e32 vcc, v66, v69
	s_waitcnt lgkmcnt(0)
	v_cmp_lt_i32_e64 s[12:13], v71, v70
	s_and_b64 s[12:13], vcc, s[12:13]
	s_andn2_b64 s[18:19], s[18:19], exec
	s_and_b64 s[12:13], s[12:13], exec
	s_or_b64 s[18:19], s[18:19], s[12:13]

.LBB1_17:
	s_or_b64 exec, exec, s[12:13]
	v_mov_b32_dpp v67, v67 row_ror:8 row_mask:0xf bank_mask:0xf
	v_mov_b32_dpp v69, v70 row_ror:8 row_mask:0xf bank_mask:0xf
	s_waitcnt lgkmcnt(0)
	v_cmp_lt_f32_e64 s[18:19], v66, v67
	v_cmp_nlt_f32_e32 vcc, v66, v67
	s_and_saveexec_b64 s[22:23], vcc
	s_cbranch_execz .LBB1_19
	v_cmp_eq_f32_e32 vcc, v66, v67
	s_waitcnt lgkmcnt(0)
	v_cmp_lt_i32_e64 s[12:13], v69, v70
	s_and_b64 s[12:13], vcc, s[12:13]
	s_andn2_b64 s[18:19], s[18:19], exec
	s_and_b64 s[12:13], s[12:13], exec
	s_or_b64 s[18:19], s[18:19], s[12:13]

.LBB1_21:
	s_or_b64 exec, exec, s[12:13]
	v_mov_b32_e32 v67, 0xff61b1e6
	v_cmp_eq_u32_e32 vcc, v139, v70
	v_mov_b32_dpp v72, v139 quad_perm:[1,0,3,2] row_mask:0xf bank_mask:0xf
	s_nop 0
	v_cndmask_b32_e32 v67, v68, v67, vcc
	s_waitcnt lgkmcnt(0)
	s_nop 0
	v_mov_b32_dpp v69, v67 quad_perm:[1,0,3,2] row_mask:0xf bank_mask:0xf
	s_waitcnt lgkmcnt(0)
	v_cmp_lt_f32_e64 s[22:23], v67, v69
	v_cmp_nlt_f32_e64 s[12:13], v67, v69
	s_and_saveexec_b64 s[24:25], s[12:13]
	v_cmp_eq_f32_e64 s[12:13], v67, v69
	v_cmp_lt_i32_e64 s[18:19], v72, v139
	s_and_b64 s[12:13], s[12:13], s[18:19]
	s_andn2_b64 s[18:19], s[22:23], exec
	s_and_b64 s[12:13], s[12:13], exec
	s_or_b64 s[22:23], s[18:19], s[12:13]
	s_or_b64 exec, exec, s[24:25]
	v_mov_b32_e32 v71, v139
	s_and_saveexec_b64 s[12:13], s[22:23]
	v_mov_b32_e32 v67, v69
	v_mov_b32_e32 v71, v72
	s_or_b64 exec, exec, s[12:13]
	ds_bpermute_b32 v69, v135, v67
	ds_bpermute_b32 v72, v135, v71
	s_waitcnt lgkmcnt(0)
	v_cmp_lt_f32_e64 s[22:23], v67, v69
	v_cmp_nlt_f32_e64 s[12:13], v67, v69
	s_and_saveexec_b64 s[24:25], s[12:13]
	s_cbranch_execz .LBB1_27
	v_cmp_eq_f32_e64 s[12:13], v67, v69
	s_waitcnt lgkmcnt(0)
	v_cmp_lt_i32_e64 s[18:19], v72, v71
	s_and_b64 s[12:13], s[12:13], s[18:19]
	s_andn2_b64 s[18:19], s[22:23], exec
	s_and_b64 s[12:13], s[12:13], exec
	s_or_b64 s[22:23], s[18:19], s[12:13]

.LBB1_29:
	s_or_b64 exec, exec, s[12:13]
	ds_bpermute_b32 v69, v134, v67
	s_waitcnt lgkmcnt(0)
	ds_bpermute_b32 v72, v134, v71
	s_waitcnt lgkmcnt(0)
	v_cmp_lt_f32_e64 s[22:23], v67, v69
	v_cmp_nlt_f32_e64 s[12:13], v67, v69
	s_and_saveexec_b64 s[24:25], s[12:13]
	s_cbranch_execz .LBB1_31
	v_cmp_eq_f32_e64 s[12:13], v67, v69
	s_waitcnt lgkmcnt(0)
	v_cmp_lt_i32_e64 s[18:19], v72, v71
	s_and_b64 s[12:13], s[12:13], s[18:19]
	s_andn2_b64 s[18:19], s[22:23], exec
	s_and_b64 s[12:13], s[12:13], exec
	s_or_b64 s[22:23], s[18:19], s[12:13]

.LBB1_33:
	s_or_b64 exec, exec, s[12:13]
	v_mov_b32_dpp v69, v67 row_ror:8 row_mask:0xf bank_mask:0xf
	s_waitcnt lgkmcnt(0)
	v_mov_b32_dpp v72, v71 row_ror:8 row_mask:0xf bank_mask:0xf
	s_waitcnt lgkmcnt(0)
	v_cmp_lt_f32_e64 s[22:23], v67, v69
	v_cmp_nlt_f32_e64 s[12:13], v67, v69
	s_and_saveexec_b64 s[24:25], s[12:13]
	s_cbranch_execz .LBB1_35
	v_cmp_eq_f32_e64 s[12:13], v67, v69
	s_waitcnt lgkmcnt(0)
	v_cmp_lt_i32_e64 s[18:19], v72, v71
	s_and_b64 s[12:13], s[12:13], s[18:19]
	s_andn2_b64 s[18:19], s[22:23], exec
	s_and_b64 s[12:13], s[12:13], exec
	s_or_b64 s[22:23], s[18:19], s[12:13]

.LBB1_37:
	s_or_b64 exec, exec, s[12:13]
	s_waitcnt lgkmcnt(0)
	v_sub_f32_e32 v72, v68, v66
	v_mul_f32_e32 v72, 0x3fb8aa3b, v72
	v_exp_f32_e32 v72, v72
	v_cmp_eq_u32_e64 s[12:13], v139, v71
	v_mov_b32_e32 v69, 0xff61b1e6
	s_or_b64 vcc, vcc, s[12:13]
	v_mov_b32_dpp v73, v72 quad_perm:[1,0,3,2] row_mask:0xf bank_mask:0xf
	v_cndmask_b32_e32 v68, v68, v69, vcc
	s_nop 1
	v_mov_b32_dpp v69, v68 quad_perm:[1,0,3,2] row_mask:0xf bank_mask:0xf
	v_max_f32_e32 v68, v68, v68
	v_sub_f32_e32 v66, v67, v66
	s_waitcnt lgkmcnt(0)
	v_add_f32_e32 v72, v72, v73
	ds_bpermute_b32 v73, v135, v72
	s_waitcnt lgkmcnt(0)
	v_max_f32_e32 v69, v69, v69
	v_max_f32_e32 v68, v68, v69
	ds_bpermute_b32 v69, v135, v68
	v_mul_f32_e32 v66, 0x3fb8aa3b, v66
	s_waitcnt lgkmcnt(0)
	v_add_f32_e32 v72, v72, v73
	ds_bpermute_b32 v73, v134, v72
	v_exp_f32_e32 v66, v66
	s_waitcnt lgkmcnt(0)
	v_max_f32_e32 v69, v69, v69
	v_max_f32_e32 v68, v68, v69
	ds_bpermute_b32 v69, v134, v68
	s_waitcnt lgkmcnt(0)
	v_add_f32_e32 v72, v72, v73
	s_nop 1
	v_mov_b32_dpp v73, v72 row_ror:8 row_mask:0xf bank_mask:0xf
	s_load_dwordx2 s[22:23], s[0:1], 0x38
	s_mov_b32 s18, 0x38d1b717
	s_waitcnt lgkmcnt(0)
	v_max_f32_e32 v69, v69, v69
	v_max_f32_e32 v68, v68, v69
	s_nop 1
	v_mov_b32_dpp v69, v68 row_ror:8 row_mask:0xf bank_mask:0xf
	v_add_f32_e32 v72, v72, v73
	v_div_scale_f32 v73, s[12:13], v72, v72, v66
	v_rcp_f32_e32 v74, v73
	s_waitcnt lgkmcnt(0)
	v_max_f32_e32 v69, v69, v69
	v_max_f32_e32 v68, v68, v69
	v_lshlrev_b32_e32 v140, 2, v172
	v_fma_f32 v69, -v73, v74, 1.0
	v_fmac_f32_e32 v74, v69, v74
	v_div_scale_f32 v69, vcc, v66, v72, v66
	v_mul_f32_e32 v75, v69, v74
	v_fma_f32 v76, -v73, v75, v69
	v_fmac_f32_e32 v75, v76, v74
	v_fma_f32 v69, -v73, v75, v69
	v_div_scale_f32 v73, s[12:13], v72, v72, 1.0
	v_rcp_f32_e32 v76, v73
	v_div_fmas_f32 v69, v69, v74, v75
	v_div_fixup_f32 v77, v69, v72, v66
	v_cmp_eq_u32_e64 s[12:13], 0, v139
	v_fma_f32 v66, -v73, v76, 1.0
	v_fmac_f32_e32 v76, v66, v76
	v_div_scale_f32 v66, vcc, 1.0, v72, 1.0
	v_mul_f32_e32 v69, v66, v76
	v_fma_f32 v74, -v73, v69, v66
	v_fmac_f32_e32 v69, v74, v76
	v_fma_f32 v66, -v73, v69, v66
	v_div_fmas_f32 v66, v66, v76, v69
	v_div_fixup_f32 v76, v66, v72, 1.0
	v_sub_f32_e32 v66, v67, v68
	v_cmp_gt_f32_e32 vcc, s18, v66
	s_and_b64 vcc, s[12:13], vcc
	v_bfe_u32 v138, v0, 2, 4
	v_cndmask_b32_e64 v66, 0, 1, vcc
	v_cmp_ne_u32_e64 s[24:25], 0, v66
	v_lshrrev_b32_e32 v137, 4, v172
	s_cbranch_vccz .LBB1_76
	v_mov_b32_e32 v73, 0
	v_mov_b32_e32 v159, v73
	v_lshl_add_u64 v[66:67], s[20:21], 0, v[158:159]
	s_mov_b32 s30, 0x652b82fe
	s_mov_b32 s34, 0xfefa39ef
	s_mov_b32 s36, 0x3b39803f
	s_mov_b32 s38, 0x6a5dcb37
	s_mov_b32 s40, 0
	s_mov_b32 s42, 0
	v_bfe_u32 v141, v0, 2, 4
	v_add_u32_e32 v142, 0x8000, v168
	v_add_u32_e32 v143, 0x4400, v145
	v_add_u32_e32 v146, 0x8400, v169
	v_add_u32_e32 v147, 0xc400, v170
	v_lshl_add_u64 v[74:75], v[66:67], 0, 8
	s_mov_b64 s[26:27], 0x400
	s_mov_b32 s31, 0x3ff71547
	s_mov_b32 s35, 0xbfe62e42
	s_mov_b32 s37, 0xbc7abc9e
	s_mov_b32 s39, 0x3e5ade15
	s_mov_b32 s41, 0x40900000
	s_mov_b32 s43, 0xc090cc00
	v_mov_b32_e32 v148, 0xfe37e43c
	v_mov_b32_e32 v149, 0x8800759c
	v_mov_b32_e32 v78, 0xfca7ab0c
	v_mov_b32_e32 v79, 0x3e928af3
	v_mov_b32_e32 v80, 0x623fde64
	v_mov_b32_e32 v81, 0x3ec71dee
	v_mov_b32_e32 v82, 0x7c89e6b0
	v_mov_b32_e32 v83, 0x3efa0199
	v_mov_b32_e32 v84, 0x14761f6e
	v_mov_b32_e32 v85, 0x3f2a01a0
	v_mov_b32_e32 v86, 0x1852b7b0
	v_mov_b32_e32 v87, 0x3f56c16c
	v_mov_b32_e32 v88, 0x11122322
	v_mov_b32_e32 v89, 0x3f811111
	v_mov_b32_e32 v90, 0x555502a1
	v_mov_b32_e32 v91, 0x3fa55555
	v_mov_b32_e32 v92, 0x55555511
	v_mov_b32_e32 v93, 0x3fc55555
	v_mov_b32_e32 v94, 11
	v_mov_b32_e32 v95, 0x3fe00000
	v_mov_b32_e32 v150, 0x7ff00000
	s_branch .LBB1_40

.LBB1_79:
	s_or_b64 exec, exec, s[18:19]
	v_or_b32_e32 v102, 4, v171
	v_add_lshl_u32 v66, v102, s3, 11
	v_mov_b32_e32 v67, 0
	v_lshl_add_u64 v[70:71], s[28:29], 0, v[66:67]
	v_lshlrev_b32_e32 v66, 1, v140
	v_cvt_pk_f16_f32 v69, v64, v65
	v_cvt_pk_f16_f32 v68, v62, v63
	v_lshl_add_u64 v[66:67], v[70:71], 0, v[66:67]
	global_store_dwordx2 v[66:67], v[68:69], off sc1
	v_cvt_pk_f16_f32 v69, v48, v49
	v_cvt_pk_f16_f32 v68, v46, v47
	global_store_dwordx2 v[66:67], v[68:69], off offset:512 sc1
	v_cvt_pk_f16_f32 v69, v32, v33
	v_cvt_pk_f16_f32 v68, v30, v31
	global_store_dwordx2 v[66:67], v[68:69], off offset:1024 sc1
	v_cvt_pk_f16_f32 v69, v20, v21
	v_cvt_pk_f16_f32 v68, v18, v19
	global_store_dwordx2 v[66:67], v[68:69], off offset:1536 sc1
	v_cvt_pk_f16_f32 v69, v52, v53
	v_cvt_pk_f16_f32 v68, v50, v51
	global_store_dwordx2 v[66:67], v[68:69], off offset:2048 sc1
	v_cvt_pk_f16_f32 v69, v36, v37
	v_cvt_pk_f16_f32 v68, v34, v35
	global_store_dwordx2 v[66:67], v[68:69], off offset:2560 sc1
	v_cvt_pk_f16_f32 v69, v28, v29
	v_cvt_pk_f16_f32 v68, v26, v27
	s_movk_i32 s18, 0x1000
	global_store_dwordx2 v[66:67], v[68:69], off offset:3072 sc1
	v_cvt_pk_f16_f32 v69, v16, v17
	v_cvt_pk_f16_f32 v68, v14, v15
	v_add_co_u32_e32 v98, vcc, s18, v66
	global_store_dwordx2 v[66:67], v[68:69], off offset:3584 sc1
	s_nop 0
	v_addc_co_u32_e32 v99, vcc, 0, v67, vcc
	v_cvt_pk_f16_f32 v67, v44, v45
	v_cvt_pk_f16_f32 v66, v42, v43
	global_store_dwordx2 v[98:99], v[66:67], off offset:512 sc1
	v_cvt_pk_f16_f32 v67, v24, v25
	v_cvt_pk_f16_f32 v66, v22, v23
	global_store_dwordx2 v[98:99], v[66:67], off offset:1024 sc1
	v_cvt_pk_f16_f32 v67, v12, v13
	v_cvt_pk_f16_f32 v66, v10, v11
	v_cvt_pk_f16_f32 v69, v60, v61
	v_cvt_pk_f16_f32 v68, v58, v59
	global_store_dwordx2 v[98:99], v[66:67], off offset:1536 sc1
	v_cvt_pk_f16_f32 v67, v56, v57
	v_cvt_pk_f16_f32 v66, v54, v55
	global_store_dwordx2 v[98:99], v[68:69], off sc1
	global_store_dwordx2 v[98:99], v[66:67], off offset:2048 sc1
	ds_read_b128 v[94:97], v1
	ds_read_b128 v[90:93], v161 offset:16384
	ds_read_b128 v[86:89], v168 offset:32768
	ds_read_b128 v[82:85], v163 offset:49152
	ds_read_b128 v[66:69], v1 offset:2048
	ds_read_b128 v[70:73], v161 offset:18432
	ds_read_b128 v[78:81], v163 offset:51200
	ds_read_b128 v[74:77], v168 offset:34816
	ds_read_b128 v[174:177], v144 offset:1024
	ds_read_b128 v[178:181], v145 offset:17408
	ds_read_b128 v[182:185], v169 offset:33792
	ds_read_b128 v[186:189], v170 offset:50176
	ds_read_b128 v[190:193], v144 offset:3072
	ds_read_b128 v[194:197], v145 offset:19456
	ds_read_b128 v[198:201], v169 offset:35840
	ds_read_b128 v[202:205], v170 offset:52224
	s_waitcnt lgkmcnt(0)
	v_fma_f32 v159, v62, v94, 0
	v_fma_f32 v154, v62, v95, 0
	v_fma_f32 v153, v62, v96, 0
	v_fma_f32 v152, v62, v97, 0
	v_fma_f32 v148, v62, v90, 0
	v_fma_f32 v147, v62, v91, 0
	v_fma_f32 v146, v62, v92, 0
	v_fma_f32 v129, v62, v93, 0
	v_fma_f32 v140, v62, v86, 0
	v_fma_f32 v128, v62, v87, 0
	v_fma_f32 v124, v62, v88, 0
	v_fma_f32 v123, v62, v89, 0
	v_fma_f32 v122, v62, v82, 0
	v_fma_f32 v121, v62, v83, 0
	v_fma_f32 v120, v62, v84, 0
	v_fma_f32 v119, v62, v85, 0
	v_fma_f32 v118, v50, v94, 0
	v_fma_f32 v117, v50, v95, 0
	v_fma_f32 v116, v50, v96, 0
	v_fma_f32 v115, v50, v97, 0
	v_fma_f32 v114, v50, v90, 0
	v_fma_f32 v113, v50, v91, 0
	v_fma_f32 v112, v50, v92, 0
	v_fma_f32 v111, v50, v93, 0
	v_fma_f32 v110, v50, v86, 0
	v_fma_f32 v109, v50, v87, 0
	v_fma_f32 v108, v50, v88, 0
	v_fma_f32 v107, v50, v89, 0
	v_fma_f32 v106, v50, v82, 0
	v_fma_f32 v105, v50, v83, 0
	v_fma_f32 v104, v50, v84, 0
	v_fma_f32 v103, v50, v85, 0
	v_fma_f32 v173, v58, v94, 0
	v_fma_f32 v172, v58, v95, 0
	v_fma_f32 v171, v58, v96, 0
	v_fma_f32 v167, v58, v97, 0
	v_fma_f32 v166, v58, v90, 0
	v_fma_f32 v165, v58, v91, 0
	v_fma_f32 v164, v58, v92, 0
	v_fma_f32 v157, v58, v93, 0
	v_fma_f32 v156, v58, v86, 0
	v_fma_f32 v155, v58, v87, 0
	v_fma_f32 v151, v58, v88, 0
	v_fma_f32 v150, v58, v89, 0
	v_fma_f32 v149, v58, v82, 0
	v_fma_f32 v143, v58, v83, 0
	v_fma_f32 v142, v58, v84, 0
	v_fma_f32 v141, v58, v85, 0
	v_fma_f32 v127, v54, v94, 0
	v_fma_f32 v126, v54, v95, 0
	v_fma_f32 v125, v54, v96, 0
	v_fma_f32 v97, v54, v97, 0
	v_fma_f32 v96, v54, v90, 0
	v_fma_f32 v95, v54, v91, 0
	v_fma_f32 v94, v54, v92, 0
	v_fma_f32 v93, v54, v93, 0
	v_fma_f32 v92, v54, v86, 0
	v_fma_f32 v91, v54, v87, 0
	v_fma_f32 v90, v54, v88, 0
	v_fma_f32 v88, v54, v89, 0
	v_fma_f32 v87, v54, v82, 0
	v_fma_f32 v86, v54, v83, 0
	v_fma_f32 v83, v54, v84, 0
	v_fma_f32 v82, v54, v85, 0
	v_fmac_f32_e32 v159, v63, v174
	v_fmac_f32_e32 v154, v63, v175
	v_fmac_f32_e32 v153, v63, v176
	v_fmac_f32_e32 v152, v63, v177
	v_fmac_f32_e32 v148, v63, v178
	v_fmac_f32_e32 v147, v63, v179
	v_fmac_f32_e32 v146, v63, v180
	v_fmac_f32_e32 v129, v63, v181
	v_fmac_f32_e32 v140, v63, v182
	v_fmac_f32_e32 v128, v63, v183
	v_fmac_f32_e32 v124, v63, v184
	v_fmac_f32_e32 v123, v63, v185
	v_fmac_f32_e32 v122, v63, v186
	v_fmac_f32_e32 v121, v63, v187
	v_fmac_f32_e32 v120, v63, v188
	v_fmac_f32_e32 v119, v63, v189
	v_fmac_f32_e32 v118, v51, v174
	v_fmac_f32_e32 v117, v51, v175
	v_fmac_f32_e32 v116, v51, v176
	v_fmac_f32_e32 v115, v51, v177
	v_fmac_f32_e32 v114, v51, v178
	v_fmac_f32_e32 v113, v51, v179
	v_fmac_f32_e32 v112, v51, v180
	v_fmac_f32_e32 v111, v51, v181
	v_fmac_f32_e32 v110, v51, v182
	v_fmac_f32_e32 v109, v51, v183
	v_fmac_f32_e32 v108, v51, v184
	v_fmac_f32_e32 v107, v51, v185
	v_fmac_f32_e32 v106, v51, v186
	v_fmac_f32_e32 v105, v51, v187
	v_fmac_f32_e32 v104, v51, v188
	v_fmac_f32_e32 v103, v51, v189
	v_fmac_f32_e32 v173, v59, v174
	v_fmac_f32_e32 v172, v59, v175
	v_fmac_f32_e32 v171, v59, v176
	v_fmac_f32_e32 v167, v59, v177
	v_fmac_f32_e32 v166, v59, v178
	v_fmac_f32_e32 v165, v59, v179
	v_fmac_f32_e32 v164, v59, v180
	v_fmac_f32_e32 v157, v59, v181
	v_fmac_f32_e32 v156, v59, v182
	v_fmac_f32_e32 v155, v59, v183
	v_fmac_f32_e32 v151, v59, v184
	v_fmac_f32_e32 v150, v59, v185
	v_fmac_f32_e32 v149, v59, v186
	v_fmac_f32_e32 v143, v59, v187
	v_fmac_f32_e32 v142, v59, v188
	v_fmac_f32_e32 v141, v59, v189
	v_fmac_f32_e32 v127, v55, v174
	v_fmac_f32_e32 v126, v55, v175
	v_fmac_f32_e32 v125, v55, v176
	v_fmac_f32_e32 v97, v55, v177
	v_fmac_f32_e32 v96, v55, v178
	v_fmac_f32_e32 v95, v55, v179
	v_fmac_f32_e32 v94, v55, v180
	v_fmac_f32_e32 v93, v55, v181
	v_fmac_f32_e32 v92, v55, v182
	v_fmac_f32_e32 v91, v55, v183
	v_fmac_f32_e32 v90, v55, v184
	v_fmac_f32_e32 v88, v55, v185
	v_fmac_f32_e32 v87, v55, v186
	v_fmac_f32_e32 v86, v55, v187
	v_fmac_f32_e32 v83, v55, v188
	v_fmac_f32_e32 v82, v55, v189
	v_fmac_f32_e32 v159, v64, v66
	v_fmac_f32_e32 v154, v64, v67
	v_fmac_f32_e32 v153, v64, v68
	v_fmac_f32_e32 v152, v64, v69
	v_fmac_f32_e32 v148, v64, v70
	v_fmac_f32_e32 v147, v64, v71
	v_fmac_f32_e32 v146, v64, v72
	v_fmac_f32_e32 v129, v64, v73
	v_fmac_f32_e32 v140, v64, v74
	v_fmac_f32_e32 v128, v64, v75
	v_fmac_f32_e32 v124, v64, v76
	v_fmac_f32_e32 v123, v64, v77
	v_fmac_f32_e32 v122, v64, v78
	v_fmac_f32_e32 v121, v64, v79
	v_fmac_f32_e32 v120, v64, v80
	v_fmac_f32_e32 v119, v64, v81
	v_fmac_f32_e32 v118, v52, v66
	v_fmac_f32_e32 v117, v52, v67
	v_fmac_f32_e32 v116, v52, v68
	v_fmac_f32_e32 v115, v52, v69
	v_fmac_f32_e32 v114, v52, v70
	v_fmac_f32_e32 v113, v52, v71
	v_fmac_f32_e32 v112, v52, v72
	v_fmac_f32_e32 v111, v52, v73
	v_fmac_f32_e32 v110, v52, v74
	v_fmac_f32_e32 v109, v52, v75
	v_fmac_f32_e32 v108, v52, v76
	v_fmac_f32_e32 v107, v52, v77
	v_fmac_f32_e32 v106, v52, v78
	v_fmac_f32_e32 v105, v52, v79
	v_fmac_f32_e32 v104, v52, v80
	v_fmac_f32_e32 v103, v52, v81
	v_fmac_f32_e32 v173, v60, v66
	v_fmac_f32_e32 v172, v60, v67
	v_fmac_f32_e32 v171, v60, v68
	v_fmac_f32_e32 v167, v60, v69
	v_fmac_f32_e32 v166, v60, v70
	v_fmac_f32_e32 v165, v60, v71
	v_fmac_f32_e32 v164, v60, v72
	v_fmac_f32_e32 v157, v60, v73
	v_fmac_f32_e32 v156, v60, v74
	v_fmac_f32_e32 v155, v60, v75
	v_fmac_f32_e32 v151, v60, v76
	v_fmac_f32_e32 v150, v60, v77
	v_fmac_f32_e32 v149, v60, v78
	v_fmac_f32_e32 v143, v60, v79
	v_fmac_f32_e32 v142, v60, v80
	v_fmac_f32_e32 v141, v60, v81
	v_fmac_f32_e32 v127, v56, v66
	v_fmac_f32_e32 v126, v56, v67
	v_fmac_f32_e32 v125, v56, v68
	v_fmac_f32_e32 v97, v56, v69
	v_fmac_f32_e32 v96, v56, v70
	v_fmac_f32_e32 v95, v56, v71
	v_fmac_f32_e32 v94, v56, v72
	v_fmac_f32_e32 v93, v56, v73
	v_fmac_f32_e32 v92, v56, v74
	v_fmac_f32_e32 v91, v56, v75
	v_fmac_f32_e32 v90, v56, v76
	v_fmac_f32_e32 v88, v56, v77
	v_fmac_f32_e32 v87, v56, v78
	v_fmac_f32_e32 v86, v56, v79
	v_fmac_f32_e32 v83, v56, v80
	v_fmac_f32_e32 v82, v56, v81
	v_fmac_f32_e32 v159, v65, v190
	v_fmac_f32_e32 v154, v65, v191
	v_fmac_f32_e32 v153, v65, v192
	v_fmac_f32_e32 v152, v65, v193
	v_fmac_f32_e32 v148, v65, v194
	v_fmac_f32_e32 v147, v65, v195
	v_fmac_f32_e32 v146, v65, v196
	v_fmac_f32_e32 v129, v65, v197
	v_fmac_f32_e32 v140, v65, v198
	v_fmac_f32_e32 v128, v65, v199
	v_fmac_f32_e32 v124, v65, v200
	v_fmac_f32_e32 v123, v65, v201
	v_fmac_f32_e32 v122, v65, v202
	v_fmac_f32_e32 v121, v65, v203
	v_fmac_f32_e32 v120, v65, v204
	v_fmac_f32_e32 v119, v65, v205
	v_fmac_f32_e32 v118, v53, v190
	v_fmac_f32_e32 v117, v53, v191
	v_fmac_f32_e32 v116, v53, v192
	v_fmac_f32_e32 v115, v53, v193
	v_fmac_f32_e32 v114, v53, v194
	v_fmac_f32_e32 v113, v53, v195
	v_fmac_f32_e32 v112, v53, v196
	v_fmac_f32_e32 v111, v53, v197
	v_fmac_f32_e32 v110, v53, v198
	v_fmac_f32_e32 v109, v53, v199
	v_fmac_f32_e32 v108, v53, v200
	v_fmac_f32_e32 v107, v53, v201
	v_fmac_f32_e32 v106, v53, v202
	v_fmac_f32_e32 v105, v53, v203
	v_fmac_f32_e32 v104, v53, v204
	v_fmac_f32_e32 v103, v53, v205
	v_fmac_f32_e32 v173, v61, v190
	v_fmac_f32_e32 v172, v61, v191
	v_fmac_f32_e32 v171, v61, v192
	v_fmac_f32_e32 v167, v61, v193
	v_fmac_f32_e32 v166, v61, v194
	v_fmac_f32_e32 v165, v61, v195
	v_fmac_f32_e32 v164, v61, v196
	v_fmac_f32_e32 v157, v61, v197
	v_fmac_f32_e32 v156, v61, v198
	v_fmac_f32_e32 v155, v61, v199
	v_fmac_f32_e32 v151, v61, v200
	v_fmac_f32_e32 v150, v61, v201
	v_fmac_f32_e32 v149, v61, v202
	v_fmac_f32_e32 v143, v61, v203
	v_fmac_f32_e32 v142, v61, v204
	v_fmac_f32_e32 v141, v61, v205
	v_fmac_f32_e32 v127, v57, v190
	v_fmac_f32_e32 v126, v57, v191
	v_fmac_f32_e32 v125, v57, v192
	v_fmac_f32_e32 v97, v57, v193
	v_fmac_f32_e32 v96, v57, v194
	v_fmac_f32_e32 v95, v57, v195
	v_fmac_f32_e32 v94, v57, v196
	v_fmac_f32_e32 v93, v57, v197
	v_fmac_f32_e32 v92, v57, v198
	v_fmac_f32_e32 v91, v57, v199
	v_fmac_f32_e32 v90, v57, v200
	v_fmac_f32_e32 v88, v57, v201
	v_fmac_f32_e32 v87, v57, v202
	v_fmac_f32_e32 v86, v57, v203
	v_fmac_f32_e32 v83, v57, v204
	v_fmac_f32_e32 v82, v57, v205
	ds_read_b128 v[62:65], v1 offset:4096
	ds_read_b128 v[58:61], v161 offset:20480
	ds_read_b128 v[54:57], v168 offset:36864
	ds_read_b128 v[50:53], v163 offset:53248
	ds_read_b128 v[66:69], v1 offset:6144
	s_waitcnt lgkmcnt(4)
	v_fmac_f32_e32 v159, v46, v62
	v_fmac_f32_e32 v154, v46, v63
	v_fmac_f32_e32 v153, v46, v64
	v_fmac_f32_e32 v152, v46, v65
	ds_read_b128 v[70:73], v161 offset:22528
	ds_read_b128 v[78:81], v163 offset:55296
	s_waitcnt lgkmcnt(5)
	v_fmac_f32_e32 v148, v46, v58
	v_fmac_f32_e32 v147, v46, v59
	v_fmac_f32_e32 v146, v46, v60
	v_fmac_f32_e32 v129, v46, v61
	ds_read_b128 v[74:77], v168 offset:38912
	s_waitcnt lgkmcnt(5)
	v_fmac_f32_e32 v140, v46, v54
	v_fmac_f32_e32 v128, v46, v55
	v_fmac_f32_e32 v124, v46, v56
	v_fmac_f32_e32 v123, v46, v57
	s_waitcnt lgkmcnt(4)
	v_fmac_f32_e32 v122, v46, v50
	v_fmac_f32_e32 v121, v46, v51
	v_fmac_f32_e32 v120, v46, v52
	v_fmac_f32_e32 v119, v46, v53
	v_fmac_f32_e32 v118, v34, v62
	v_fmac_f32_e32 v117, v34, v63
	v_fmac_f32_e32 v116, v34, v64
	v_fmac_f32_e32 v115, v34, v65
	v_fmac_f32_e32 v114, v34, v58
	v_fmac_f32_e32 v113, v34, v59
	v_fmac_f32_e32 v112, v34, v60
	v_fmac_f32_e32 v111, v34, v61
	v_fmac_f32_e32 v110, v34, v54
	v_fmac_f32_e32 v109, v34, v55
	v_fmac_f32_e32 v108, v34, v56
	v_fmac_f32_e32 v107, v34, v57
	v_fmac_f32_e32 v106, v34, v50
	v_fmac_f32_e32 v105, v34, v51
	v_fmac_f32_e32 v104, v34, v52
	v_fmac_f32_e32 v103, v34, v53
	v_fmac_f32_e32 v173, v42, v62
	v_fmac_f32_e32 v172, v42, v63
	v_fmac_f32_e32 v171, v42, v64
	v_fmac_f32_e32 v167, v42, v65
	v_fmac_f32_e32 v166, v42, v58
	v_fmac_f32_e32 v165, v42, v59
	v_fmac_f32_e32 v164, v42, v60
	v_fmac_f32_e32 v157, v42, v61
	v_fmac_f32_e32 v156, v42, v54
	v_fmac_f32_e32 v155, v42, v55
	v_fmac_f32_e32 v151, v42, v56
	v_fmac_f32_e32 v150, v42, v57
	v_fmac_f32_e32 v149, v42, v50
	v_fmac_f32_e32 v143, v42, v51
	v_fmac_f32_e32 v142, v42, v52
	v_fmac_f32_e32 v141, v42, v53
	v_fmac_f32_e32 v127, v38, v62
	v_fmac_f32_e32 v126, v38, v63
	v_fmac_f32_e32 v125, v38, v64
	v_fmac_f32_e32 v97, v38, v65
	v_fmac_f32_e32 v96, v38, v58
	v_fmac_f32_e32 v95, v38, v59
	v_fmac_f32_e32 v94, v38, v60
	v_fmac_f32_e32 v93, v38, v61
	v_fmac_f32_e32 v92, v38, v54
	v_fmac_f32_e32 v91, v38, v55
	v_fmac_f32_e32 v90, v38, v56
	v_fmac_f32_e32 v88, v38, v57
	v_fmac_f32_e32 v87, v38, v50
	v_fmac_f32_e32 v86, v38, v51
	v_fmac_f32_e32 v83, v38, v52
	v_fmac_f32_e32 v82, v38, v53
	ds_read_b128 v[50:53], v144 offset:5120
	ds_read_b128 v[54:57], v145 offset:21504
	ds_read_b128 v[58:61], v169 offset:37888
	ds_read_b128 v[62:65], v170 offset:54272
	ds_read_b128 v[174:177], v144 offset:7168
	ds_read_b128 v[178:181], v145 offset:23552
	ds_read_b128 v[182:185], v169 offset:39936
	ds_read_b128 v[186:189], v170 offset:56320
	s_waitcnt lgkmcnt(7)
	v_fmac_f32_e32 v159, v47, v50
	v_fmac_f32_e32 v154, v47, v51
	v_fmac_f32_e32 v153, v47, v52
	v_fmac_f32_e32 v152, v47, v53
	s_waitcnt lgkmcnt(6)
	v_fmac_f32_e32 v148, v47, v54
	v_fmac_f32_e32 v147, v47, v55
	v_fmac_f32_e32 v146, v47, v56
	v_fmac_f32_e32 v129, v47, v57
	s_waitcnt lgkmcnt(5)
	v_fmac_f32_e32 v140, v47, v58
	v_fmac_f32_e32 v128, v47, v59
	v_fmac_f32_e32 v124, v47, v60
	v_fmac_f32_e32 v123, v47, v61
	s_waitcnt lgkmcnt(4)
	v_fmac_f32_e32 v122, v47, v62
	v_fmac_f32_e32 v121, v47, v63
	v_fmac_f32_e32 v120, v47, v64
	v_fmac_f32_e32 v119, v47, v65
	v_fmac_f32_e32 v118, v35, v50
	v_fmac_f32_e32 v117, v35, v51
	v_fmac_f32_e32 v116, v35, v52
	v_fmac_f32_e32 v115, v35, v53
	v_fmac_f32_e32 v114, v35, v54
	v_fmac_f32_e32 v113, v35, v55
	v_fmac_f32_e32 v112, v35, v56
	v_fmac_f32_e32 v111, v35, v57
	v_fmac_f32_e32 v110, v35, v58
	v_fmac_f32_e32 v109, v35, v59
	v_fmac_f32_e32 v108, v35, v60
	v_fmac_f32_e32 v107, v35, v61
	v_fmac_f32_e32 v106, v35, v62
	v_fmac_f32_e32 v105, v35, v63
	v_fmac_f32_e32 v104, v35, v64
	v_fmac_f32_e32 v103, v35, v65
	v_fmac_f32_e32 v173, v43, v50
	v_fmac_f32_e32 v172, v43, v51
	v_fmac_f32_e32 v171, v43, v52
	v_fmac_f32_e32 v167, v43, v53
	v_fmac_f32_e32 v166, v43, v54
	v_fmac_f32_e32 v165, v43, v55
	v_fmac_f32_e32 v164, v43, v56
	v_fmac_f32_e32 v157, v43, v57
	v_fmac_f32_e32 v156, v43, v58
	v_fmac_f32_e32 v155, v43, v59
	v_fmac_f32_e32 v151, v43, v60
	v_fmac_f32_e32 v150, v43, v61
	v_fmac_f32_e32 v149, v43, v62
	v_fmac_f32_e32 v143, v43, v63
	v_fmac_f32_e32 v142, v43, v64
	v_fmac_f32_e32 v141, v43, v65
	v_fmac_f32_e32 v127, v39, v50
	v_fmac_f32_e32 v126, v39, v51
	v_fmac_f32_e32 v125, v39, v52
	v_fmac_f32_e32 v97, v39, v53
	v_fmac_f32_e32 v96, v39, v54
	v_fmac_f32_e32 v95, v39, v55
	v_fmac_f32_e32 v94, v39, v56
	v_fmac_f32_e32 v93, v39, v57
	v_fmac_f32_e32 v92, v39, v58
	v_fmac_f32_e32 v91, v39, v59
	v_fmac_f32_e32 v90, v39, v60
	v_fmac_f32_e32 v88, v39, v61
	v_fmac_f32_e32 v87, v39, v62
	v_fmac_f32_e32 v86, v39, v63
	v_fmac_f32_e32 v83, v39, v64
	v_fmac_f32_e32 v82, v39, v65
	v_fmac_f32_e32 v159, v48, v66
	v_fmac_f32_e32 v154, v48, v67
	v_fmac_f32_e32 v153, v48, v68
	v_fmac_f32_e32 v152, v48, v69
	v_fmac_f32_e32 v148, v48, v70
	v_fmac_f32_e32 v147, v48, v71
	v_fmac_f32_e32 v146, v48, v72
	v_fmac_f32_e32 v129, v48, v73
	v_fmac_f32_e32 v140, v48, v74
	v_fmac_f32_e32 v128, v48, v75
	v_fmac_f32_e32 v124, v48, v76
	v_fmac_f32_e32 v123, v48, v77
	v_fmac_f32_e32 v122, v48, v78
	v_fmac_f32_e32 v121, v48, v79
	v_fmac_f32_e32 v120, v48, v80
	v_fmac_f32_e32 v119, v48, v81
	v_fmac_f32_e32 v118, v36, v66
	v_fmac_f32_e32 v117, v36, v67
	v_fmac_f32_e32 v116, v36, v68
	v_fmac_f32_e32 v115, v36, v69
	v_fmac_f32_e32 v114, v36, v70
	v_fmac_f32_e32 v113, v36, v71
	v_fmac_f32_e32 v112, v36, v72
	v_fmac_f32_e32 v111, v36, v73
	v_fmac_f32_e32 v110, v36, v74
	v_fmac_f32_e32 v109, v36, v75
	v_fmac_f32_e32 v108, v36, v76
	v_fmac_f32_e32 v107, v36, v77
	v_fmac_f32_e32 v106, v36, v78
	v_fmac_f32_e32 v105, v36, v79
	v_fmac_f32_e32 v104, v36, v80
	v_fmac_f32_e32 v103, v36, v81
	v_fmac_f32_e32 v173, v44, v66
	v_fmac_f32_e32 v172, v44, v67
	v_fmac_f32_e32 v171, v44, v68
	v_fmac_f32_e32 v167, v44, v69
	v_fmac_f32_e32 v166, v44, v70
	v_fmac_f32_e32 v165, v44, v71
	v_fmac_f32_e32 v164, v44, v72
	v_fmac_f32_e32 v157, v44, v73
	v_fmac_f32_e32 v156, v44, v74
	v_fmac_f32_e32 v155, v44, v75
	v_fmac_f32_e32 v151, v44, v76
	v_fmac_f32_e32 v150, v44, v77
	v_fmac_f32_e32 v149, v44, v78
	v_fmac_f32_e32 v143, v44, v79
	v_fmac_f32_e32 v142, v44, v80
	v_fmac_f32_e32 v141, v44, v81
	v_fmac_f32_e32 v127, v40, v66
	v_fmac_f32_e32 v126, v40, v67
	v_fmac_f32_e32 v125, v40, v68
	v_fmac_f32_e32 v97, v40, v69
	v_fmac_f32_e32 v96, v40, v70
	v_fmac_f32_e32 v95, v40, v71
	v_fmac_f32_e32 v94, v40, v72
	v_fmac_f32_e32 v93, v40, v73
	v_fmac_f32_e32 v92, v40, v74
	v_fmac_f32_e32 v91, v40, v75
	v_fmac_f32_e32 v90, v40, v76
	v_fmac_f32_e32 v88, v40, v77
	v_fmac_f32_e32 v87, v40, v78
	v_fmac_f32_e32 v86, v40, v79
	v_fmac_f32_e32 v83, v40, v80
	v_fmac_f32_e32 v82, v40, v81
	v_cvt_pk_f16_f32 v101, v40, v41
	v_cvt_pk_f16_f32 v100, v38, v39
	s_waitcnt lgkmcnt(3)
	v_fmac_f32_e32 v159, v49, v174
	v_fmac_f32_e32 v154, v49, v175
	v_fmac_f32_e32 v153, v49, v176
	v_fmac_f32_e32 v152, v49, v177
	s_waitcnt lgkmcnt(2)
	v_fmac_f32_e32 v148, v49, v178
	v_fmac_f32_e32 v147, v49, v179
	v_fmac_f32_e32 v146, v49, v180
	v_fmac_f32_e32 v129, v49, v181
	s_waitcnt lgkmcnt(1)
	v_fmac_f32_e32 v140, v49, v182
	v_fmac_f32_e32 v128, v49, v183
	v_fmac_f32_e32 v124, v49, v184
	v_fmac_f32_e32 v123, v49, v185
	s_waitcnt lgkmcnt(0)
	v_fmac_f32_e32 v122, v49, v186
	v_fmac_f32_e32 v121, v49, v187
	v_fmac_f32_e32 v120, v49, v188
	v_fmac_f32_e32 v119, v49, v189
	v_fmac_f32_e32 v118, v37, v174
	v_fmac_f32_e32 v117, v37, v175
	v_fmac_f32_e32 v116, v37, v176
	v_fmac_f32_e32 v115, v37, v177
	v_fmac_f32_e32 v114, v37, v178
	v_fmac_f32_e32 v113, v37, v179
	v_fmac_f32_e32 v112, v37, v180
	v_fmac_f32_e32 v111, v37, v181
	v_fmac_f32_e32 v110, v37, v182
	v_fmac_f32_e32 v109, v37, v183
	v_fmac_f32_e32 v108, v37, v184
	v_fmac_f32_e32 v107, v37, v185
	v_fmac_f32_e32 v106, v37, v186
	v_fmac_f32_e32 v105, v37, v187
	v_fmac_f32_e32 v104, v37, v188
	v_fmac_f32_e32 v103, v37, v189
	v_fmac_f32_e32 v173, v45, v174
	v_fmac_f32_e32 v172, v45, v175
	v_fmac_f32_e32 v171, v45, v176
	v_fmac_f32_e32 v167, v45, v177
	v_fmac_f32_e32 v166, v45, v178
	v_fmac_f32_e32 v165, v45, v179
	v_fmac_f32_e32 v164, v45, v180
	v_fmac_f32_e32 v157, v45, v181
	v_fmac_f32_e32 v156, v45, v182
	v_fmac_f32_e32 v155, v45, v183
	v_fmac_f32_e32 v151, v45, v184
	v_fmac_f32_e32 v150, v45, v185
	v_fmac_f32_e32 v149, v45, v186
	v_fmac_f32_e32 v143, v45, v187
	v_fmac_f32_e32 v142, v45, v188
	v_fmac_f32_e32 v141, v45, v189
	v_fmac_f32_e32 v127, v41, v174
	v_fmac_f32_e32 v126, v41, v175
	v_fmac_f32_e32 v125, v41, v176
	v_fmac_f32_e32 v97, v41, v177
	v_fmac_f32_e32 v96, v41, v178
	v_fmac_f32_e32 v95, v41, v179
	v_fmac_f32_e32 v94, v41, v180
	v_fmac_f32_e32 v93, v41, v181
	v_fmac_f32_e32 v92, v41, v182
	v_fmac_f32_e32 v91, v41, v183
	v_fmac_f32_e32 v90, v41, v184
	v_fmac_f32_e32 v88, v41, v185
	v_fmac_f32_e32 v87, v41, v186
	v_fmac_f32_e32 v86, v41, v187
	v_fmac_f32_e32 v83, v41, v188
	v_fmac_f32_e32 v82, v41, v189
	ds_read_b128 v[46:49], v1 offset:8192
	ds_read_b128 v[42:45], v161 offset:24576
	ds_read_b128 v[38:41], v168 offset:40960
	ds_read_b128 v[34:37], v163 offset:57344
	ds_read_b128 v[50:53], v1 offset:10240
	s_waitcnt lgkmcnt(4)
	v_fmac_f32_e32 v159, v30, v46
	v_fmac_f32_e32 v154, v30, v47
	v_fmac_f32_e32 v153, v30, v48
	v_fmac_f32_e32 v152, v30, v49
	ds_read_b128 v[54:57], v161 offset:26624
	ds_read_b128 v[62:65], v163 offset:59392
	s_waitcnt lgkmcnt(5)
	v_fmac_f32_e32 v148, v30, v42
	v_fmac_f32_e32 v147, v30, v43
	v_fmac_f32_e32 v146, v30, v44
	v_fmac_f32_e32 v129, v30, v45
	ds_read_b128 v[58:61], v168 offset:43008
	s_waitcnt lgkmcnt(5)
	v_fmac_f32_e32 v140, v30, v38
	v_fmac_f32_e32 v128, v30, v39
	v_fmac_f32_e32 v124, v30, v40
	v_fmac_f32_e32 v123, v30, v41
	s_waitcnt lgkmcnt(4)
	v_fmac_f32_e32 v122, v30, v34
	v_fmac_f32_e32 v121, v30, v35
	v_fmac_f32_e32 v120, v30, v36
	v_fmac_f32_e32 v119, v30, v37
	v_fmac_f32_e32 v118, v26, v46
	v_fmac_f32_e32 v117, v26, v47
	v_fmac_f32_e32 v116, v26, v48
	v_fmac_f32_e32 v115, v26, v49
	v_fmac_f32_e32 v114, v26, v42
	v_fmac_f32_e32 v113, v26, v43
	v_fmac_f32_e32 v112, v26, v44
	v_fmac_f32_e32 v111, v26, v45
	v_fmac_f32_e32 v110, v26, v38
	v_fmac_f32_e32 v109, v26, v39
	v_fmac_f32_e32 v108, v26, v40
	v_fmac_f32_e32 v107, v26, v41
	v_fmac_f32_e32 v106, v26, v34
	v_fmac_f32_e32 v105, v26, v35
	v_fmac_f32_e32 v104, v26, v36
	v_fmac_f32_e32 v103, v26, v37
	v_fmac_f32_e32 v173, v22, v46
	v_fmac_f32_e32 v172, v22, v47
	v_fmac_f32_e32 v171, v22, v48
	v_fmac_f32_e32 v167, v22, v49
	v_fmac_f32_e32 v166, v22, v42
	v_fmac_f32_e32 v165, v22, v43
	v_fmac_f32_e32 v164, v22, v44
	v_fmac_f32_e32 v157, v22, v45
	v_fmac_f32_e32 v156, v22, v38
	v_fmac_f32_e32 v155, v22, v39
	v_fmac_f32_e32 v151, v22, v40
	v_fmac_f32_e32 v150, v22, v41
	v_fmac_f32_e32 v149, v22, v34
	v_fmac_f32_e32 v143, v22, v35
	v_fmac_f32_e32 v142, v22, v36
	v_fmac_f32_e32 v141, v22, v37
	v_fmac_f32_e32 v127, v6, v46
	v_fmac_f32_e32 v126, v6, v47
	v_fmac_f32_e32 v125, v6, v48
	v_fmac_f32_e32 v97, v6, v49
	v_fmac_f32_e32 v96, v6, v42
	v_fmac_f32_e32 v95, v6, v43
	v_fmac_f32_e32 v94, v6, v44
	v_fmac_f32_e32 v93, v6, v45
	v_fmac_f32_e32 v92, v6, v38
	v_fmac_f32_e32 v91, v6, v39
	v_fmac_f32_e32 v90, v6, v40
	v_fmac_f32_e32 v88, v6, v41
	v_fmac_f32_e32 v87, v6, v34
	v_fmac_f32_e32 v86, v6, v35
	v_fmac_f32_e32 v83, v6, v36
	v_fmac_f32_e32 v82, v6, v37
	ds_read_b128 v[34:37], v144 offset:9216
	ds_read_b128 v[38:41], v145 offset:25600
	ds_read_b128 v[42:45], v169 offset:41984
	ds_read_b128 v[46:49], v170 offset:58368
	ds_read_b128 v[66:69], v144 offset:11264
	ds_read_b128 v[70:73], v145 offset:27648
	ds_read_b128 v[74:77], v169 offset:44032
	ds_read_b128 v[78:81], v170 offset:60416
	s_waitcnt lgkmcnt(7)
	v_fmac_f32_e32 v159, v31, v34
	v_fmac_f32_e32 v154, v31, v35
	v_fmac_f32_e32 v153, v31, v36
	v_fmac_f32_e32 v152, v31, v37
	s_waitcnt lgkmcnt(6)
	v_fmac_f32_e32 v148, v31, v38
	v_fmac_f32_e32 v147, v31, v39
	v_fmac_f32_e32 v146, v31, v40
	v_fmac_f32_e32 v129, v31, v41
	s_waitcnt lgkmcnt(5)
	v_fmac_f32_e32 v140, v31, v42
	v_fmac_f32_e32 v128, v31, v43
	v_fmac_f32_e32 v124, v31, v44
	v_fmac_f32_e32 v123, v31, v45
	s_waitcnt lgkmcnt(4)
	v_fmac_f32_e32 v122, v31, v46
	v_fmac_f32_e32 v121, v31, v47
	v_fmac_f32_e32 v120, v31, v48
	v_fmac_f32_e32 v119, v31, v49
	v_fmac_f32_e32 v118, v27, v34
	v_fmac_f32_e32 v117, v27, v35
	v_fmac_f32_e32 v116, v27, v36
	v_fmac_f32_e32 v115, v27, v37
	v_fmac_f32_e32 v114, v27, v38
	v_fmac_f32_e32 v113, v27, v39
	v_fmac_f32_e32 v112, v27, v40
	v_fmac_f32_e32 v111, v27, v41
	v_fmac_f32_e32 v110, v27, v42
	v_fmac_f32_e32 v109, v27, v43
	v_fmac_f32_e32 v108, v27, v44
	v_fmac_f32_e32 v107, v27, v45
	v_fmac_f32_e32 v106, v27, v46
	v_fmac_f32_e32 v105, v27, v47
	v_fmac_f32_e32 v104, v27, v48
	v_fmac_f32_e32 v103, v27, v49
	v_fmac_f32_e32 v173, v23, v34
	v_fmac_f32_e32 v172, v23, v35
	v_fmac_f32_e32 v171, v23, v36
	v_fmac_f32_e32 v167, v23, v37
	v_fmac_f32_e32 v166, v23, v38
	v_fmac_f32_e32 v165, v23, v39
	v_fmac_f32_e32 v164, v23, v40
	v_fmac_f32_e32 v157, v23, v41
	v_fmac_f32_e32 v156, v23, v42
	v_fmac_f32_e32 v155, v23, v43
	v_fmac_f32_e32 v151, v23, v44
	v_fmac_f32_e32 v150, v23, v45
	v_fmac_f32_e32 v149, v23, v46
	v_fmac_f32_e32 v143, v23, v47
	v_fmac_f32_e32 v142, v23, v48
	v_fmac_f32_e32 v141, v23, v49
	v_fmac_f32_e32 v159, v32, v50
	v_fmac_f32_e32 v154, v32, v51
	v_fmac_f32_e32 v153, v32, v52
	v_fmac_f32_e32 v152, v32, v53
	v_fmac_f32_e32 v148, v32, v54
	v_fmac_f32_e32 v147, v32, v55
	v_fmac_f32_e32 v146, v32, v56
	v_fmac_f32_e32 v129, v32, v57
	v_fmac_f32_e32 v140, v32, v58
	v_fmac_f32_e32 v128, v32, v59
	v_fmac_f32_e32 v124, v32, v60
	v_fmac_f32_e32 v123, v32, v61
	v_fmac_f32_e32 v122, v32, v62
	v_fmac_f32_e32 v121, v32, v63
	v_fmac_f32_e32 v120, v32, v64
	v_fmac_f32_e32 v119, v32, v65
	v_fmac_f32_e32 v118, v28, v50
	v_fmac_f32_e32 v117, v28, v51
	v_fmac_f32_e32 v116, v28, v52
	v_fmac_f32_e32 v115, v28, v53
	v_fmac_f32_e32 v114, v28, v54
	v_fmac_f32_e32 v113, v28, v55
	v_fmac_f32_e32 v112, v28, v56
	v_fmac_f32_e32 v111, v28, v57
	v_fmac_f32_e32 v110, v28, v58
	v_fmac_f32_e32 v109, v28, v59
	v_fmac_f32_e32 v108, v28, v60
	v_fmac_f32_e32 v107, v28, v61
	v_fmac_f32_e32 v106, v28, v62
	v_fmac_f32_e32 v105, v28, v63
	v_fmac_f32_e32 v104, v28, v64
	v_fmac_f32_e32 v103, v28, v65
	v_fmac_f32_e32 v173, v24, v50
	v_fmac_f32_e32 v172, v24, v51
	v_fmac_f32_e32 v171, v24, v52
	v_fmac_f32_e32 v167, v24, v53
	v_fmac_f32_e32 v166, v24, v54
	v_fmac_f32_e32 v165, v24, v55
	v_fmac_f32_e32 v164, v24, v56
	v_fmac_f32_e32 v157, v24, v57
	v_fmac_f32_e32 v156, v24, v58
	v_fmac_f32_e32 v155, v24, v59
	v_fmac_f32_e32 v151, v24, v60
	v_fmac_f32_e32 v150, v24, v61
	v_fmac_f32_e32 v149, v24, v62
	v_fmac_f32_e32 v143, v24, v63
	v_fmac_f32_e32 v142, v24, v64
	v_fmac_f32_e32 v141, v24, v65
	v_fmac_f32_e32 v127, v7, v34
	v_fmac_f32_e32 v126, v7, v35
	v_fmac_f32_e32 v125, v7, v36
	v_fmac_f32_e32 v97, v7, v37
	v_fmac_f32_e32 v96, v7, v38
	v_fmac_f32_e32 v95, v7, v39
	v_fmac_f32_e32 v94, v7, v40
	v_fmac_f32_e32 v93, v7, v41
	s_waitcnt lgkmcnt(3)
	v_fmac_f32_e32 v159, v33, v66
	v_fmac_f32_e32 v154, v33, v67
	v_fmac_f32_e32 v153, v33, v68
	v_fmac_f32_e32 v152, v33, v69
	s_waitcnt lgkmcnt(2)
	v_fmac_f32_e32 v148, v33, v70
	v_fmac_f32_e32 v147, v33, v71
	v_fmac_f32_e32 v146, v33, v72
	v_fmac_f32_e32 v129, v33, v73
	s_waitcnt lgkmcnt(1)
	v_fmac_f32_e32 v140, v33, v74
	v_fmac_f32_e32 v128, v33, v75
	v_fmac_f32_e32 v124, v33, v76
	v_fmac_f32_e32 v123, v33, v77
	s_waitcnt lgkmcnt(0)
	v_fmac_f32_e32 v122, v33, v78
	v_fmac_f32_e32 v121, v33, v79
	v_fmac_f32_e32 v120, v33, v80
	v_fmac_f32_e32 v119, v33, v81
	v_fmac_f32_e32 v118, v29, v66
	v_fmac_f32_e32 v117, v29, v67
	v_fmac_f32_e32 v116, v29, v68
	v_fmac_f32_e32 v115, v29, v69
	v_fmac_f32_e32 v114, v29, v70
	v_fmac_f32_e32 v113, v29, v71
	v_fmac_f32_e32 v112, v29, v72
	v_fmac_f32_e32 v111, v29, v73
	v_fmac_f32_e32 v110, v29, v74
	v_fmac_f32_e32 v109, v29, v75
	v_fmac_f32_e32 v108, v29, v76
	v_fmac_f32_e32 v107, v29, v77
	v_fmac_f32_e32 v106, v29, v78
	v_fmac_f32_e32 v105, v29, v79
	v_fmac_f32_e32 v104, v29, v80
	v_fmac_f32_e32 v103, v29, v81
	v_fmac_f32_e32 v173, v25, v66
	v_fmac_f32_e32 v172, v25, v67
	v_fmac_f32_e32 v171, v25, v68
	v_fmac_f32_e32 v167, v25, v69
	v_fmac_f32_e32 v166, v25, v70
	v_fmac_f32_e32 v165, v25, v71
	v_fmac_f32_e32 v164, v25, v72
	v_fmac_f32_e32 v157, v25, v73
	v_fmac_f32_e32 v156, v25, v74
	v_fmac_f32_e32 v155, v25, v75
	v_fmac_f32_e32 v151, v25, v76
	v_fmac_f32_e32 v150, v25, v77
	v_fmac_f32_e32 v149, v25, v78
	v_fmac_f32_e32 v143, v25, v79
	v_fmac_f32_e32 v142, v25, v80
	v_fmac_f32_e32 v141, v25, v81
	ds_read_b128 v[34:37], v1 offset:12288
	ds_read_b128 v[30:33], v161 offset:28672
	ds_read_b128 v[26:29], v168 offset:45056
	ds_read_b128 v[22:25], v163 offset:61440
	ds_read_b128 v[38:41], v1 offset:14336
	v_fmac_f32_e32 v92, v7, v42
	v_fmac_f32_e32 v91, v7, v43
	v_fmac_f32_e32 v90, v7, v44
	v_fmac_f32_e32 v88, v7, v45
	v_fmac_f32_e32 v87, v7, v46
	v_fmac_f32_e32 v86, v7, v47
	v_fmac_f32_e32 v83, v7, v48
	v_fmac_f32_e32 v82, v7, v49
	v_fmac_f32_e32 v127, v8, v50
	v_fmac_f32_e32 v126, v8, v51
	v_fmac_f32_e32 v125, v8, v52
	v_fmac_f32_e32 v97, v8, v53
	v_fmac_f32_e32 v96, v8, v54
	v_fmac_f32_e32 v95, v8, v55
	v_fmac_f32_e32 v94, v8, v56
	v_fmac_f32_e32 v93, v8, v57
	v_fmac_f32_e32 v92, v8, v58
	v_fmac_f32_e32 v91, v8, v59
	v_fmac_f32_e32 v90, v8, v60
	v_fmac_f32_e32 v88, v8, v61
	v_fmac_f32_e32 v87, v8, v62
	v_fmac_f32_e32 v86, v8, v63
	v_fmac_f32_e32 v83, v8, v64
	v_fmac_f32_e32 v82, v8, v65
	v_fmac_f32_e32 v127, v9, v66
	v_fmac_f32_e32 v126, v9, v67
	v_fmac_f32_e32 v125, v9, v68
	v_fmac_f32_e32 v97, v9, v69
	v_fmac_f32_e32 v96, v9, v70
	v_fmac_f32_e32 v95, v9, v71
	v_fmac_f32_e32 v94, v9, v72
	v_fmac_f32_e32 v93, v9, v73
	v_fmac_f32_e32 v92, v9, v74
	v_fmac_f32_e32 v91, v9, v75
	v_fmac_f32_e32 v90, v9, v76
	v_fmac_f32_e32 v88, v9, v77
	v_fmac_f32_e32 v87, v9, v78
	v_fmac_f32_e32 v86, v9, v79
	v_fmac_f32_e32 v83, v9, v80
	v_fmac_f32_e32 v82, v9, v81
	s_waitcnt lgkmcnt(4)
	v_fmac_f32_e32 v159, v18, v34
	v_fmac_f32_e32 v154, v18, v35
	v_fmac_f32_e32 v153, v18, v36
	v_fmac_f32_e32 v152, v18, v37
	ds_read_b128 v[42:45], v161 offset:30720
	ds_read_b128 v[50:53], v163 offset:63488
	s_waitcnt lgkmcnt(5)
	v_fmac_f32_e32 v148, v18, v30
	v_fmac_f32_e32 v147, v18, v31
	v_fmac_f32_e32 v146, v18, v32
	v_fmac_f32_e32 v129, v18, v33
	ds_read_b128 v[46:49], v168 offset:47104
	s_waitcnt lgkmcnt(5)
	v_fmac_f32_e32 v140, v18, v26
	v_fmac_f32_e32 v128, v18, v27
	v_fmac_f32_e32 v124, v18, v28
	v_fmac_f32_e32 v123, v18, v29
	s_waitcnt lgkmcnt(4)
	v_fmac_f32_e32 v122, v18, v22
	v_fmac_f32_e32 v121, v18, v23
	v_fmac_f32_e32 v120, v18, v24
	v_fmac_f32_e32 v119, v18, v25
	v_fmac_f32_e32 v118, v14, v34
	v_fmac_f32_e32 v117, v14, v35
	v_fmac_f32_e32 v116, v14, v36
	v_fmac_f32_e32 v115, v14, v37
	v_fmac_f32_e32 v114, v14, v30
	v_fmac_f32_e32 v113, v14, v31
	v_fmac_f32_e32 v112, v14, v32
	v_fmac_f32_e32 v111, v14, v33
	v_fmac_f32_e32 v110, v14, v26
	v_fmac_f32_e32 v109, v14, v27
	v_fmac_f32_e32 v108, v14, v28
	v_fmac_f32_e32 v107, v14, v29
	v_fmac_f32_e32 v106, v14, v22
	v_fmac_f32_e32 v105, v14, v23
	v_fmac_f32_e32 v104, v14, v24
	v_fmac_f32_e32 v103, v14, v25
	v_fmac_f32_e32 v173, v10, v34
	v_fmac_f32_e32 v172, v10, v35
	v_fmac_f32_e32 v171, v10, v36
	v_fmac_f32_e32 v167, v10, v37
	v_fmac_f32_e32 v166, v10, v30
	v_fmac_f32_e32 v165, v10, v31
	v_fmac_f32_e32 v164, v10, v32
	v_fmac_f32_e32 v157, v10, v33
	v_fmac_f32_e32 v156, v10, v26
	v_fmac_f32_e32 v155, v10, v27
	v_fmac_f32_e32 v151, v10, v28
	v_fmac_f32_e32 v150, v10, v29
	v_fmac_f32_e32 v149, v10, v22
	v_fmac_f32_e32 v143, v10, v23
	v_fmac_f32_e32 v142, v10, v24
	v_fmac_f32_e32 v141, v10, v25
	v_fmac_f32_e32 v127, v2, v34
	v_fmac_f32_e32 v126, v2, v35
	v_fmac_f32_e32 v125, v2, v36
	v_fmac_f32_e32 v97, v2, v37
	v_fmac_f32_e32 v96, v2, v30
	v_fmac_f32_e32 v95, v2, v31
	v_fmac_f32_e32 v94, v2, v32
	v_fmac_f32_e32 v93, v2, v33
	v_fmac_f32_e32 v92, v2, v26
	v_fmac_f32_e32 v91, v2, v27
	v_fmac_f32_e32 v90, v2, v28
	v_fmac_f32_e32 v88, v2, v29
	v_fmac_f32_e32 v87, v2, v22
	v_fmac_f32_e32 v86, v2, v23
	v_fmac_f32_e32 v83, v2, v24
	v_fmac_f32_e32 v82, v2, v25
	ds_read_b128 v[26:29], v144 offset:13312
	ds_read_b128 v[30:33], v145 offset:29696
	ds_read_b128 v[34:37], v169 offset:46080
	ds_read_b128 v[54:57], v170 offset:62464
	ds_read_b128 v[22:25], v144 offset:15360
	s_waitcnt lgkmcnt(4)
	v_fmac_f32_e32 v159, v19, v26
	ds_read_b128 v[58:61], v145 offset:31744
	ds_read_b128 v[62:65], v169 offset:48128
	ds_read_b128 v[66:69], v170 offset:64512
	v_fmac_f32_e32 v173, v11, v26
	v_fmac_f32_e32 v154, v19, v27
	v_fmac_f32_e32 v172, v11, v27
	v_fmac_f32_e32 v159, v20, v38
	v_fmac_f32_e32 v173, v12, v38
	v_fmac_f32_e32 v153, v19, v28
	v_fmac_f32_e32 v171, v11, v28
	v_fmac_f32_e32 v154, v20, v39
	v_fmac_f32_e32 v172, v12, v39
	s_waitcnt lgkmcnt(3)
	v_fmac_f32_e32 v159, v21, v22
	v_fmac_f32_e32 v173, v13, v22
	v_fmac_f32_e32 v167, v11, v29
	v_fmac_f32_e32 v166, v11, v30
	v_fmac_f32_e32 v165, v11, v31
	v_fmac_f32_e32 v164, v11, v32
	v_fmac_f32_e32 v157, v11, v33
	v_fmac_f32_e32 v156, v11, v34
	v_fmac_f32_e32 v155, v11, v35
	v_fmac_f32_e32 v151, v11, v36
	v_fmac_f32_e32 v150, v11, v37
	v_fmac_f32_e32 v149, v11, v54
	v_fmac_f32_e32 v143, v11, v55
	v_fmac_f32_e32 v142, v11, v56
	v_fmac_f32_e32 v141, v11, v57
	v_fmac_f32_e32 v153, v20, v40
	v_fmac_f32_e32 v171, v12, v40
	v_fmac_f32_e32 v154, v21, v23
	v_fmac_f32_e32 v172, v13, v23
	v_fmac_f32_e32 v167, v12, v41
	v_fmac_f32_e32 v166, v12, v42
	v_fmac_f32_e32 v165, v12, v43
	v_fmac_f32_e32 v164, v12, v44
	v_fmac_f32_e32 v157, v12, v45
	v_fmac_f32_e32 v156, v12, v46
	v_fmac_f32_e32 v155, v12, v47
	v_fmac_f32_e32 v151, v12, v48
	v_fmac_f32_e32 v150, v12, v49
	v_fmac_f32_e32 v149, v12, v50
	v_fmac_f32_e32 v143, v12, v51
	v_fmac_f32_e32 v142, v12, v52
	v_fmac_f32_e32 v141, v12, v53
	v_fmac_f32_e32 v153, v21, v24
	v_fmac_f32_e32 v171, v13, v24
	v_fmac_f32_e32 v167, v13, v25
	s_waitcnt lgkmcnt(0)
	v_fmac_f32_e32 v166, v13, v58
	v_fmac_f32_e32 v165, v13, v59
	v_fmac_f32_e32 v164, v13, v60
	v_fmac_f32_e32 v157, v13, v61
	s_waitcnt lgkmcnt(0)
	v_fmac_f32_e32 v156, v13, v62
	v_fmac_f32_e32 v155, v13, v63
	v_fmac_f32_e32 v151, v13, v64
	v_fmac_f32_e32 v150, v13, v65
	s_waitcnt lgkmcnt(0)
	v_fmac_f32_e32 v149, v13, v66
	v_fmac_f32_e32 v143, v13, v67
	v_fmac_f32_e32 v142, v13, v68
	v_fmac_f32_e32 v141, v13, v69
	v_fmac_f32_e32 v152, v19, v29
	v_permlane32_swap_b32_e32 v159, v173
	v_add_f32_e32 v10, v159, v173
	v_fmac_f32_e32 v148, v19, v30
	v_fmac_f32_e32 v152, v20, v41
	s_waitcnt lgkmcnt(0)
	v_permlane32_swap_b32_e32 v154, v172
	v_add_f32_e32 v11, v154, v172
	v_fmac_f32_e32 v147, v19, v31
	v_fmac_f32_e32 v148, v20, v42
	v_fmac_f32_e32 v152, v21, v25
	s_waitcnt lgkmcnt(0)
	v_permlane32_swap_b32_e32 v153, v171
	v_add_f32_e32 v12, v153, v171
	v_fmac_f32_e32 v147, v20, v43
	v_fmac_f32_e32 v148, v21, v58
	s_waitcnt lgkmcnt(0)
	v_fmac_f32_e32 v118, v15, v26
	v_fmac_f32_e32 v117, v15, v27
	v_fmac_f32_e32 v116, v15, v28
	v_fmac_f32_e32 v115, v15, v29
	v_fmac_f32_e32 v114, v15, v30
	v_fmac_f32_e32 v113, v15, v31
	v_fmac_f32_e32 v112, v15, v32
	v_fmac_f32_e32 v111, v15, v33
	v_fmac_f32_e32 v110, v15, v34
	v_fmac_f32_e32 v109, v15, v35
	v_fmac_f32_e32 v108, v15, v36
	v_fmac_f32_e32 v107, v15, v37
	v_fmac_f32_e32 v106, v15, v54
	v_fmac_f32_e32 v105, v15, v55
	v_fmac_f32_e32 v104, v15, v56
	v_fmac_f32_e32 v103, v15, v57
	v_fmac_f32_e32 v147, v21, v59
	v_fmac_f32_e32 v118, v16, v38
	v_fmac_f32_e32 v117, v16, v39
	v_fmac_f32_e32 v116, v16, v40
	v_fmac_f32_e32 v115, v16, v41
	v_fmac_f32_e32 v114, v16, v42
	v_fmac_f32_e32 v113, v16, v43
	v_fmac_f32_e32 v112, v16, v44
	v_fmac_f32_e32 v111, v16, v45
	v_fmac_f32_e32 v110, v16, v46
	v_fmac_f32_e32 v109, v16, v47
	v_fmac_f32_e32 v108, v16, v48
	v_fmac_f32_e32 v107, v16, v49
	v_fmac_f32_e32 v106, v16, v50
	v_fmac_f32_e32 v105, v16, v51
	v_fmac_f32_e32 v104, v16, v52
	v_fmac_f32_e32 v103, v16, v53
	v_fmac_f32_e32 v146, v19, v32
	v_permlane32_swap_b32_e32 v152, v167
	v_add_f32_e32 v13, v152, v167
	v_fmac_f32_e32 v129, v19, v33
	v_fmac_f32_e32 v146, v20, v44
	s_waitcnt lgkmcnt(0)
	v_permlane32_swap_b32_e32 v148, v166
	v_add_f32_e32 v14, v148, v166
	v_fmac_f32_e32 v140, v19, v34
	v_fmac_f32_e32 v129, v20, v45
	v_fmac_f32_e32 v146, v21, v60
	s_waitcnt lgkmcnt(0)
	v_permlane32_swap_b32_e32 v147, v165
	v_add_f32_e32 v15, v147, v165
	v_fmac_f32_e32 v140, v20, v46
	v_fmac_f32_e32 v129, v21, v61
	s_waitcnt lgkmcnt(0)
	v_fmac_f32_e32 v140, v21, v62
	v_fmac_f32_e32 v128, v19, v35
	v_fmac_f32_e32 v124, v19, v36
	v_fmac_f32_e32 v123, v19, v37
	v_fmac_f32_e32 v122, v19, v54
	v_fmac_f32_e32 v121, v19, v55
	v_fmac_f32_e32 v120, v19, v56
	v_fmac_f32_e32 v119, v19, v57
	v_fmac_f32_e32 v118, v17, v22
	v_fmac_f32_e32 v117, v17, v23
	v_fmac_f32_e32 v116, v17, v24
	v_fmac_f32_e32 v115, v17, v25
	v_fmac_f32_e32 v114, v17, v58
	v_fmac_f32_e32 v113, v17, v59
	v_fmac_f32_e32 v112, v17, v60
	v_fmac_f32_e32 v111, v17, v61
	v_fmac_f32_e32 v110, v17, v62
	v_fmac_f32_e32 v109, v17, v63
	v_fmac_f32_e32 v108, v17, v64
	v_fmac_f32_e32 v107, v17, v65
	v_fmac_f32_e32 v106, v17, v66
	v_fmac_f32_e32 v105, v17, v67
	v_fmac_f32_e32 v104, v17, v68
	v_fmac_f32_e32 v103, v17, v69
	v_permlane32_swap_b32_e32 v146, v164
	v_add_f32_e32 v16, v146, v164
	v_fmac_f32_e32 v128, v20, v47
	s_waitcnt lgkmcnt(0)
	v_permlane32_swap_b32_e32 v129, v157
	v_add_f32_e32 v17, v129, v157
	v_fmac_f32_e32 v124, v20, v48
	v_fmac_f32_e32 v128, v21, v63
	s_waitcnt lgkmcnt(0)
	v_permlane32_swap_b32_e32 v140, v156
	v_add_f32_e32 v18, v140, v156
	v_fmac_f32_e32 v127, v3, v26
	v_fmac_f32_e32 v123, v20, v49
	v_fmac_f32_e32 v122, v20, v50
	v_fmac_f32_e32 v121, v20, v51
	v_fmac_f32_e32 v120, v20, v52
	v_fmac_f32_e32 v119, v20, v53
	v_fmac_f32_e32 v124, v21, v64
	s_waitcnt lgkmcnt(0)
	v_fmac_f32_e32 v127, v4, v38
	v_fmac_f32_e32 v123, v21, v65
	v_fmac_f32_e32 v122, v21, v66
	v_fmac_f32_e32 v121, v21, v67
	v_fmac_f32_e32 v120, v21, v68
	v_fmac_f32_e32 v119, v21, v69
	v_fmac_f32_e32 v127, v5, v22
	v_permlane32_swap_b32_e32 v128, v155
	v_add_f32_e32 v19, v128, v155
	s_waitcnt lgkmcnt(0)
	v_permlane32_swap_b32_e32 v124, v151
	v_add_f32_e32 v20, v124, v151
	v_fmac_f32_e32 v125, v3, v28
	s_waitcnt lgkmcnt(0)
	v_permlane32_swap_b32_e32 v123, v150
	v_add_f32_e32 v21, v123, v150
	v_fmac_f32_e32 v97, v3, v29
	v_fmac_f32_e32 v125, v4, v40
	s_waitcnt lgkmcnt(0)
	v_fmac_f32_e32 v97, v4, v41
	v_fmac_f32_e32 v125, v5, v24
	v_fmac_f32_e32 v97, v5, v25
	v_fmac_f32_e32 v126, v3, v27
	v_fmac_f32_e32 v126, v4, v39
	v_fmac_f32_e32 v126, v5, v23
	v_permlane32_swap_b32_e32 v122, v149
	v_add_f32_e32 v22, v122, v149
	s_waitcnt lgkmcnt(0)
	v_permlane32_swap_b32_e32 v121, v143
	v_add_f32_e32 v23, v121, v143
	s_waitcnt lgkmcnt(0)
	v_permlane32_swap_b32_e32 v120, v142
	v_add_f32_e32 v24, v120, v142
	s_waitcnt lgkmcnt(0)
	v_permlane32_swap_b32_e32 v119, v141
	v_add_f32_e32 v25, v119, v141
	s_waitcnt lgkmcnt(0)
	v_permlane32_swap_b32_e32 v118, v127
	v_add_f32_e32 v26, v118, v127
	v_fmac_f32_e32 v96, v3, v30
	s_waitcnt lgkmcnt(0)
	v_permlane32_swap_b32_e32 v117, v126
	v_add_f32_e32 v27, v117, v126
	v_fmac_f32_e32 v96, v4, v42
	s_waitcnt lgkmcnt(0)
	v_fmac_f32_e32 v96, v5, v58
	v_fmac_f32_e32 v95, v3, v31
	v_permlane32_swap_b32_e32 v116, v125
	v_add_f32_e32 v28, v116, v125
	v_fmac_f32_e32 v94, v3, v32
	v_fmac_f32_e32 v95, v4, v43
	s_waitcnt lgkmcnt(0)
	v_permlane32_swap_b32_e32 v115, v97
	v_add_f32_e32 v29, v115, v97
	v_fmac_f32_e32 v93, v3, v33
	v_fmac_f32_e32 v94, v4, v44
	v_fmac_f32_e32 v95, v5, v59
	s_waitcnt lgkmcnt(0)
	v_permlane32_swap_b32_e32 v114, v96
	v_add_f32_e32 v30, v114, v96
	v_fmac_f32_e32 v93, v4, v45
	v_fmac_f32_e32 v94, v5, v60
	s_waitcnt lgkmcnt(0)
	v_fmac_f32_e32 v93, v5, v61
	v_fmac_f32_e32 v92, v3, v34
	v_permlane16_swap_b32_e32 v10, v26
	v_add_f32_e32 v10, v10, v26
	v_permlane32_swap_b32_e32 v113, v95
	v_add_f32_e32 v31, v113, v95
	v_fmac_f32_e32 v91, v3, v35
	v_fmac_f32_e32 v92, v4, v46
	s_waitcnt lgkmcnt(0)
	v_permlane32_swap_b32_e32 v112, v94
	v_add_f32_e32 v32, v112, v94
	v_fmac_f32_e32 v90, v3, v36
	v_fmac_f32_e32 v91, v4, v47
	v_fmac_f32_e32 v92, v5, v62
	s_waitcnt lgkmcnt(0)
	v_permlane32_swap_b32_e32 v111, v93
	v_add_f32_e32 v33, v111, v93
	v_permlane16_swap_b32_e32 v11, v27
	v_add_f32_e32 v11, v11, v27
	v_fmac_f32_e32 v90, v4, v48
	v_fmac_f32_e32 v91, v5, v63
	s_waitcnt lgkmcnt(0)
	s_waitcnt lgkmcnt(0)
	v_fmac_f32_e32 v90, v5, v64
	v_fmac_f32_e32 v88, v3, v37
	v_permlane32_swap_b32_e32 v110, v92
	v_add_f32_e32 v34, v110, v92
	v_permlane16_swap_b32_e32 v14, v30
	v_add_f32_e32 v14, v14, v30
	v_fmac_f32_e32 v87, v3, v54
	v_fmac_f32_e32 v88, v4, v49
	s_waitcnt lgkmcnt(0)
	v_permlane32_swap_b32_e32 v109, v91
	v_add_f32_e32 v35, v109, v91
	s_waitcnt lgkmcnt(0)
	v_fmac_f32_e32 v86, v3, v55
	v_fmac_f32_e32 v87, v4, v50
	v_fmac_f32_e32 v88, v5, v65
	s_waitcnt lgkmcnt(0)
	v_permlane32_swap_b32_e32 v108, v90
	v_add_f32_e32 v36, v108, v90
	v_fmac_f32_e32 v86, v4, v51
	v_fmac_f32_e32 v87, v5, v66
	s_waitcnt lgkmcnt(0)
	v_fmac_f32_e32 v86, v5, v67
	v_permlane16_swap_b32_e32 v12, v28
	v_add_f32_e32 v12, v12, v28
	s_waitcnt lgkmcnt(0)
	v_permlane16_swap_b32_e32 v17, v33
	v_add_f32_e32 v17, v17, v33
	s_waitcnt lgkmcnt(0)
	v_fmac_f32_e32 v83, v3, v56
	v_permlane32_swap_b32_e32 v107, v88
	v_add_f32_e32 v37, v107, v88
	v_fmac_f32_e32 v82, v3, v57
	v_fmac_f32_e32 v83, v4, v52
	s_waitcnt lgkmcnt(0)
	v_permlane32_swap_b32_e32 v106, v87
	v_add_f32_e32 v38, v106, v87
	v_fmac_f32_e32 v82, v4, v53
	v_fmac_f32_e32 v83, v5, v68
	s_waitcnt lgkmcnt(0)
	v_permlane32_swap_b32_e32 v105, v86
	v_add_f32_e32 v39, v105, v86
	v_fmac_f32_e32 v82, v5, v69
	s_waitcnt lgkmcnt(0)
	v_permlane16_swap_b32_e32 v15, v31
	v_add_f32_e32 v15, v15, v31
	v_permlane16_swap_b32_e32 v16, v32
	v_add_f32_e32 v16, v16, v32
	s_waitcnt lgkmcnt(0)
	s_waitcnt lgkmcnt(0)
	v_permlane16_swap_b32_e32 v20, v36
	v_add_f32_e32 v20, v20, v36
	s_waitcnt lgkmcnt(0)
	v_permlane32_swap_b32_e32 v104, v83
	v_add_f32_e32 v40, v104, v83
	s_waitcnt lgkmcnt(0)
	v_permlane32_swap_b32_e32 v103, v82
	v_add_f32_e32 v41, v103, v82
	v_permlane16_swap_b32_e32 v18, v34
	v_add_f32_e32 v18, v18, v34
	v_permlane16_swap_b32_e32 v19, v35
	v_add_f32_e32 v19, v19, v35
	s_waitcnt lgkmcnt(0)
	s_waitcnt lgkmcnt(0)
	s_waitcnt lgkmcnt(0)
	s_waitcnt lgkmcnt(0)
	v_permlane16_swap_b32_e32 v23, v39
	v_add_f32_e32 v23, v23, v39
	s_waitcnt lgkmcnt(0)
	v_add_f32_dpp v10, v10, v10 row_ror:8 row_mask:0xf bank_mask:0xf
	v_add_f32_dpp v18, v18, v18 row_ror:8 row_mask:0xf bank_mask:0xf
	v_cndmask_b32_e64 v10, v18, v10, s[8:9]
	v_permlane16_swap_b32_e32 v13, v29
	v_add_f32_e32 v13, v13, v29
	v_permlane16_swap_b32_e32 v21, v37
	v_add_f32_e32 v21, v21, v37
	v_permlane16_swap_b32_e32 v22, v38
	v_add_f32_e32 v22, v22, v38
	s_waitcnt lgkmcnt(0)
	s_waitcnt lgkmcnt(0)
	s_waitcnt lgkmcnt(0)
	s_waitcnt lgkmcnt(0)
	v_add_f32_dpp v11, v11, v11 row_ror:8 row_mask:0xf bank_mask:0xf
	v_add_f32_dpp v19, v19, v19 row_ror:8 row_mask:0xf bank_mask:0xf
	v_cndmask_b32_e64 v11, v19, v11, s[8:9]
	v_permlane16_swap_b32_e32 v24, v40
	v_add_f32_e32 v24, v24, v40
	v_permlane16_swap_b32_e32 v25, v41
	v_add_f32_e32 v25, v25, v41
	s_waitcnt lgkmcnt(0)
	s_waitcnt lgkmcnt(0)
	v_add_f32_dpp v13, v13, v13 row_ror:8 row_mask:0xf bank_mask:0xf
	v_add_f32_dpp v21, v21, v21 row_ror:8 row_mask:0xf bank_mask:0xf
	v_cndmask_b32_e64 v13, v21, v13, s[8:9]
	v_add_f32_dpp v14, v14, v14 row_ror:8 row_mask:0xf bank_mask:0xf
	v_add_f32_dpp v22, v22, v22 row_ror:8 row_mask:0xf bank_mask:0xf
	v_cndmask_b32_e64 v14, v22, v14, s[8:9]
	v_add_f32_dpp v12, v12, v12 row_ror:8 row_mask:0xf bank_mask:0xf
	v_add_f32_dpp v20, v20, v20 row_ror:8 row_mask:0xf bank_mask:0xf
	v_cndmask_b32_e64 v12, v20, v12, s[8:9]
	s_waitcnt lgkmcnt(0)
	s_waitcnt lgkmcnt(0)
	v_add_f32_dpp v15, v15, v15 row_ror:8 row_mask:0xf bank_mask:0xf
	v_add_f32_dpp v23, v23, v23 row_ror:8 row_mask:0xf bank_mask:0xf
	v_cndmask_b32_e64 v15, v23, v15, s[8:9]
	v_add_f32_dpp v16, v16, v16 row_ror:8 row_mask:0xf bank_mask:0xf
	v_add_f32_dpp v24, v24, v24 row_ror:8 row_mask:0xf bank_mask:0xf
	v_cndmask_b32_e64 v16, v24, v16, s[8:9]
	v_add_f32_dpp v17, v17, v17 row_ror:8 row_mask:0xf bank_mask:0xf
	v_add_f32_dpp v25, v25, v25 row_ror:8 row_mask:0xf bank_mask:0xf
	v_cndmask_b32_e64 v17, v25, v17, s[8:9]
	s_waitcnt lgkmcnt(0)
	s_waitcnt lgkmcnt(0)
	s_waitcnt lgkmcnt(0)
	s_waitcnt lgkmcnt(0)
	s_waitcnt lgkmcnt(0)
	v_cndmask_b32_e64 v20, v10, v14, s[10:11]
	v_cndmask_b32_e64 v10, v14, v10, s[10:11]
	v_cndmask_b32_e64 v14, v11, v15, s[10:11]
	v_cndmask_b32_e64 v11, v15, v11, s[10:11]
	v_cndmask_b32_e64 v15, v12, v16, s[10:11]
	v_cndmask_b32_e64 v18, v13, v17, s[10:11]
	ds_bpermute_b32 v20, v134, v20
	ds_bpermute_b32 v14, v134, v14
	ds_bpermute_b32 v15, v134, v15
	ds_bpermute_b32 v18, v134, v18
	v_cndmask_b32_e64 v12, v16, v12, s[10:11]
	v_cndmask_b32_e64 v13, v17, v13, s[10:11]
	s_waitcnt lgkmcnt(0)
	v_add_f32_e32 v10, v10, v20
	s_waitcnt lgkmcnt(0)
	v_add_f32_e32 v11, v11, v14
	s_waitcnt lgkmcnt(0)
	v_add_f32_e32 v12, v12, v15
	s_waitcnt lgkmcnt(0)
	v_add_f32_e32 v13, v13, v18
	v_add_f32_dpp v10, v10, v10 quad_perm:[2,3,0,1] row_mask:0xf bank_mask:0xf
	v_add_f32_dpp v12, v12, v12 quad_perm:[2,3,0,1] row_mask:0xf bank_mask:0xf
	v_cndmask_b32_e64 v10, v12, v10, s[14:15]
	v_add_f32_dpp v11, v11, v11 quad_perm:[2,3,0,1] row_mask:0xf bank_mask:0xf
	v_add_f32_dpp v13, v13, v13 quad_perm:[2,3,0,1] row_mask:0xf bank_mask:0xf
	v_cndmask_b32_e64 v11, v13, v11, s[14:15]
	v_cvt_pk_f16_f32 v9, v8, v9
	s_waitcnt lgkmcnt(0)
	s_waitcnt lgkmcnt(0)
	v_cvt_pk_f16_f32 v8, v6, v7
	v_add_f32_dpp v10, v10, v10 quad_perm:[1,0,3,2] row_mask:0xf bank_mask:0xf
	v_add_f32_dpp v11, v11, v11 quad_perm:[1,0,3,2] row_mask:0xf bank_mask:0xf
	v_cndmask_b32_e64 v6, v11, v10, s[6:7]
	global_store_dwordx2 v[98:99], v[8:9], off offset:3072 sc1
	v_cvt_pk_f16_f32 v9, v4, v5
	s_waitcnt lgkmcnt(0)
	ds_bpermute_b32 v7, v136, v6
	ds_bpermute_b32 v5, v136, v139
	v_cvt_pk_f16_f32 v8, v2, v3
	global_store_dwordx2 v[98:99], v[100:101], off offset:2560 sc1
	global_store_dwordx2 v[98:99], v[8:9], off offset:3584 sc1
	s_waitcnt lgkmcnt(1)
	v_cmp_lt_f32_e64 s[18:19], v6, v7
	v_cmp_nlt_f32_e32 vcc, v6, v7
	s_and_saveexec_b64 s[28:29], vcc
	s_cbranch_execz .LBB1_81
	v_cmp_eq_f32_e32 vcc, v6, v7
	s_waitcnt lgkmcnt(0)
	v_cmp_lt_i32_e64 s[14:15], v5, v139
	s_and_b64 s[14:15], s[14:15], vcc
	s_andn2_b64 s[18:19], s[18:19], exec
	s_and_b64 s[14:15], s[14:15], exec
	s_or_b64 s[18:19], s[18:19], s[14:15]

.LBB1_83:
	s_or_b64 exec, exec, s[14:15]
	s_waitcnt lgkmcnt(0)
	v_mov_b32_dpp v5, v3 quad_perm:[2,3,0,1] row_mask:0xf bank_mask:0xf
	v_mov_b32_dpp v7, v2 quad_perm:[2,3,0,1] row_mask:0xf bank_mask:0xf
	s_waitcnt lgkmcnt(0)
	v_cmp_lt_f32_e64 s[18:19], v4, v5
	v_cmp_nlt_f32_e32 vcc, v4, v5
	s_and_saveexec_b64 s[28:29], vcc
	s_cbranch_execz .LBB1_85
	v_cmp_eq_f32_e32 vcc, v4, v5
	s_waitcnt lgkmcnt(0)
	v_cmp_lt_i32_e64 s[14:15], v7, v2
	s_and_b64 s[14:15], vcc, s[14:15]
	s_andn2_b64 s[18:19], s[18:19], exec
	s_and_b64 s[14:15], s[14:15], exec
	s_or_b64 s[18:19], s[18:19], s[14:15]

.LBB1_87:
	s_or_b64 exec, exec, s[14:15]
	ds_bpermute_b32 v5, v134, v3
	s_waitcnt lgkmcnt(0)
	ds_bpermute_b32 v7, v134, v2
	s_waitcnt lgkmcnt(0)
	v_cmp_lt_f32_e64 s[18:19], v4, v5
	v_cmp_nlt_f32_e32 vcc, v4, v5
	s_and_saveexec_b64 s[28:29], vcc
	s_cbranch_execz .LBB1_89
	v_cmp_eq_f32_e32 vcc, v4, v5
	s_waitcnt lgkmcnt(0)
	v_cmp_lt_i32_e64 s[14:15], v7, v2
	s_and_b64 s[14:15], vcc, s[14:15]
	s_andn2_b64 s[18:19], s[18:19], exec
	s_and_b64 s[14:15], s[14:15], exec
	s_or_b64 s[18:19], s[18:19], s[14:15]

.LBB1_91:
	s_or_b64 exec, exec, s[14:15]
	v_mov_b32_dpp v3, v3 row_ror:8 row_mask:0xf bank_mask:0xf
	v_mov_b32_dpp v5, v2 row_ror:8 row_mask:0xf bank_mask:0xf
	s_waitcnt lgkmcnt(0)
	v_cmp_lt_f32_e64 s[18:19], v4, v3
	v_cmp_nlt_f32_e32 vcc, v4, v3
	s_and_saveexec_b64 s[28:29], vcc
	s_cbranch_execz .LBB1_93
	v_cmp_eq_f32_e32 vcc, v4, v3
	s_waitcnt lgkmcnt(0)
	v_cmp_lt_i32_e64 s[14:15], v5, v2
	s_and_b64 s[14:15], vcc, s[14:15]
	s_andn2_b64 s[18:19], s[18:19], exec
	s_and_b64 s[14:15], s[14:15], exec
	s_or_b64 s[18:19], s[18:19], s[14:15]

.LBB1_95:
	s_or_b64 exec, exec, s[14:15]
	v_mov_b32_e32 v3, 0xff61b1e6
	v_cmp_eq_u32_e32 vcc, v139, v2
	v_mov_b32_dpp v8, v139 quad_perm:[1,0,3,2] row_mask:0xf bank_mask:0xf
	s_waitcnt lgkmcnt(0)
	v_cndmask_b32_e32 v5, v6, v3, vcc
	s_nop 1
	v_mov_b32_dpp v7, v5 quad_perm:[1,0,3,2] row_mask:0xf bank_mask:0xf
	s_waitcnt lgkmcnt(0)
	v_cmp_lt_f32_e64 s[28:29], v5, v7
	v_cmp_nlt_f32_e64 s[14:15], v5, v7
	s_and_saveexec_b64 s[30:31], s[14:15]
	v_cmp_eq_f32_e64 s[14:15], v5, v7
	v_cmp_lt_i32_e64 s[18:19], v8, v139
	s_and_b64 s[14:15], s[14:15], s[18:19]
	s_andn2_b64 s[18:19], s[28:29], exec
	s_and_b64 s[14:15], s[14:15], exec
	s_or_b64 s[28:29], s[18:19], s[14:15]
	s_or_b64 exec, exec, s[30:31]
	v_mov_b32_e32 v3, v139
	s_and_saveexec_b64 s[14:15], s[28:29]
	v_mov_b32_e32 v5, v7
	v_mov_b32_e32 v3, v8
	s_or_b64 exec, exec, s[14:15]
	v_mov_b32_dpp v7, v5 quad_perm:[2,3,0,1] row_mask:0xf bank_mask:0xf
	v_mov_b32_dpp v8, v3 quad_perm:[2,3,0,1] row_mask:0xf bank_mask:0xf
	s_waitcnt lgkmcnt(0)
	v_cmp_lt_f32_e64 s[28:29], v5, v7
	v_cmp_nlt_f32_e64 s[14:15], v5, v7
	s_and_saveexec_b64 s[30:31], s[14:15]
	s_cbranch_execz .LBB1_101
	v_cmp_eq_f32_e64 s[14:15], v5, v7
	s_waitcnt lgkmcnt(0)
	v_cmp_lt_i32_e64 s[18:19], v8, v3
	s_and_b64 s[14:15], s[14:15], s[18:19]
	s_andn2_b64 s[18:19], s[28:29], exec
	s_and_b64 s[14:15], s[14:15], exec
	s_or_b64 s[28:29], s[18:19], s[14:15]

.LBB1_103:
	s_or_b64 exec, exec, s[14:15]
	ds_bpermute_b32 v7, v134, v5
	s_waitcnt lgkmcnt(0)
	ds_bpermute_b32 v8, v134, v3
	s_waitcnt lgkmcnt(0)
	v_cmp_lt_f32_e64 s[28:29], v5, v7
	v_cmp_nlt_f32_e64 s[14:15], v5, v7
	s_and_saveexec_b64 s[30:31], s[14:15]
	s_cbranch_execz .LBB1_105
	v_cmp_eq_f32_e64 s[14:15], v5, v7
	s_waitcnt lgkmcnt(0)
	v_cmp_lt_i32_e64 s[18:19], v8, v3
	s_and_b64 s[14:15], s[14:15], s[18:19]
	s_andn2_b64 s[18:19], s[28:29], exec
	s_and_b64 s[14:15], s[14:15], exec
	s_or_b64 s[28:29], s[18:19], s[14:15]

.LBB1_107:
	s_or_b64 exec, exec, s[14:15]
	v_mov_b32_dpp v7, v5 row_ror:8 row_mask:0xf bank_mask:0xf
	s_waitcnt lgkmcnt(0)
	v_mov_b32_dpp v8, v3 row_ror:8 row_mask:0xf bank_mask:0xf
	s_waitcnt lgkmcnt(0)
	v_cmp_lt_f32_e64 s[28:29], v5, v7
	v_cmp_nlt_f32_e64 s[14:15], v5, v7
	s_and_saveexec_b64 s[30:31], s[14:15]
	s_cbranch_execz .LBB1_109
	v_cmp_eq_f32_e64 s[14:15], v5, v7
	s_waitcnt lgkmcnt(0)
	v_cmp_lt_i32_e64 s[18:19], v8, v3
	s_and_b64 s[14:15], s[14:15], s[18:19]
	s_andn2_b64 s[18:19], s[28:29], exec
	s_and_b64 s[14:15], s[14:15], exec
	s_or_b64 s[28:29], s[18:19], s[14:15]

.LBB1_111:
	s_or_b64 exec, exec, s[14:15]
	s_waitcnt lgkmcnt(0)
	v_sub_f32_e32 v8, v6, v4
	v_mul_f32_e32 v8, 0x3fb8aa3b, v8
	v_exp_f32_e32 v8, v8
	v_cmp_eq_u32_e64 s[14:15], v139, v3
	v_mov_b32_e32 v7, 0xff61b1e6
	s_or_b64 vcc, vcc, s[14:15]
	v_mov_b32_dpp v9, v8 quad_perm:[1,0,3,2] row_mask:0xf bank_mask:0xf
	v_cndmask_b32_e32 v6, v6, v7, vcc
	s_nop 1
	v_mov_b32_dpp v7, v6 quad_perm:[1,0,3,2] row_mask:0xf bank_mask:0xf
	v_max_f32_e32 v6, v6, v6
	v_sub_f32_e32 v4, v5, v4
	s_waitcnt lgkmcnt(0)
	v_add_f32_e32 v8, v8, v9
	s_nop 1
	v_mov_b32_dpp v9, v8 quad_perm:[2,3,0,1] row_mask:0xf bank_mask:0xf
	s_waitcnt lgkmcnt(0)
	v_max_f32_e32 v7, v7, v7
	v_max_f32_e32 v6, v6, v7
	s_nop 1
	v_mov_b32_dpp v7, v6 quad_perm:[2,3,0,1] row_mask:0xf bank_mask:0xf
	v_mul_f32_e32 v4, 0x3fb8aa3b, v4
	s_waitcnt lgkmcnt(0)
	v_add_f32_e32 v8, v8, v9
	ds_bpermute_b32 v9, v134, v8
	v_exp_f32_e32 v4, v4
	s_waitcnt lgkmcnt(0)
	v_max_f32_e32 v7, v7, v7
	v_max_f32_e32 v6, v6, v7
	ds_bpermute_b32 v7, v134, v6
	s_waitcnt lgkmcnt(0)
	v_add_f32_e32 v8, v8, v9
	s_nop 1
	v_mov_b32_dpp v9, v8 row_ror:8 row_mask:0xf bank_mask:0xf
	s_waitcnt lgkmcnt(0)
	v_max_f32_e32 v7, v7, v7
	v_max_f32_e32 v6, v6, v7
	s_nop 1
	v_mov_b32_dpp v7, v6 row_ror:8 row_mask:0xf bank_mask:0xf
	s_waitcnt lgkmcnt(0)
	v_add_f32_e32 v8, v8, v9
	v_div_scale_f32 v9, s[14:15], v8, v8, v4
	v_rcp_f32_e32 v10, v9
	s_waitcnt lgkmcnt(0)
	v_max_f32_e32 v7, v7, v7
	v_max_f32_e32 v11, v6, v7
	v_fma_f32 v6, -v9, v10, 1.0
	v_fmac_f32_e32 v10, v6, v10
	v_div_scale_f32 v6, vcc, v4, v8, v4
	v_mul_f32_e32 v7, v6, v10
	v_fma_f32 v12, -v9, v7, v6
	v_fmac_f32_e32 v7, v12, v10
	v_fma_f32 v6, -v9, v7, v6
	v_div_scale_f32 v9, s[14:15], v8, v8, 1.0
	v_rcp_f32_e32 v12, v9
	v_div_fmas_f32 v6, v6, v10, v7
	v_div_fixup_f32 v7, v6, v8, v4
	s_mov_b32 s14, 0x38d1b717
	v_fma_f32 v4, -v9, v12, 1.0
	v_fmac_f32_e32 v12, v4, v12
	v_div_scale_f32 v4, vcc, 1.0, v8, 1.0
	v_mul_f32_e32 v6, v4, v12
	v_fma_f32 v10, -v9, v6, v4
	v_fmac_f32_e32 v6, v10, v12
	v_fma_f32 v4, -v9, v6, v4
	v_div_fmas_f32 v4, v4, v12, v6
	v_div_fixup_f32 v6, v4, v8, 1.0
	v_sub_f32_e32 v4, v5, v11
	v_cmp_gt_f32_e32 vcc, s14, v4
	s_and_b64 s[14:15], s[12:13], vcc
	v_cndmask_b32_e64 v4, 0, 1, s[14:15]
	v_cmp_ne_u32_e64 s[14:15], 0, v4
	s_mov_b64 vcc, s[14:15]
	s_cbranch_vccz .LBB1_150
	v_mov_b32_e32 v159, 0
	v_lshl_add_u64 v[4:5], s[20:21], 0, v[158:159]
	s_mov_b32 s28, 0x652b82fe
	s_mov_b32 s30, 0xfefa39ef
	s_mov_b32 s34, 0x3b39803f
	s_mov_b32 s36, 0x6a5dcb37
	s_mov_b32 s38, 0
	s_mov_b32 s40, 0
	v_add_u32_e32 v60, 0x8000, v168
	v_add_u32_e32 v61, 0x4400, v145
	v_add_u32_e32 v62, 0x8400, v169
	v_add_u32_e32 v63, 0xc400, v170
	v_lshl_add_u64 v[4:5], v[4:5], 0, 8
	v_add_u32_e32 v64, 4, v162
	s_mov_b64 s[20:21], 0x400
	s_mov_b32 s29, 0x3ff71547
	s_mov_b32 s31, 0xbfe62e42
	s_mov_b32 s35, 0xbc7abc9e
	s_mov_b32 s37, 0x3e5ade15
	s_mov_b32 s39, 0x40900000
	s_mov_b32 s41, 0xc090cc00
	v_mov_b32_e32 v65, 0xfe37e43c
	v_mov_b32_e32 v66, 0x8800759c
	v_mov_b32_e32 v8, 0xfca7ab0c
	v_mov_b32_e32 v9, 0x3e928af3
	v_mov_b32_e32 v10, 0x623fde64
	v_mov_b32_e32 v11, 0x3ec71dee
	v_mov_b32_e32 v12, 0x7c89e6b0
	v_mov_b32_e32 v13, 0x3efa0199
	v_mov_b32_e32 v14, 0x14761f6e
	v_mov_b32_e32 v15, 0x3f2a01a0
	v_mov_b32_e32 v16, 0x1852b7b0
	v_mov_b32_e32 v17, 0x3f56c16c
	v_mov_b32_e32 v18, 0x11122322
	v_mov_b32_e32 v19, 0x3f811111
	v_mov_b32_e32 v20, 0x555502a1
	v_mov_b32_e32 v21, 0x3fa55555
	v_mov_b32_e32 v22, 0x55555511
	v_mov_b32_e32 v23, 0x3fc55555
	v_mov_b32_e32 v24, 11
	v_mov_b32_e32 v25, 0x3fe00000
	v_mov_b32_e32 v67, 0x7ff00000
	s_branch .LBB1_114

.LBB2_114:
	s_setprio 0
	v_and_b32_e32 v0, 16, v0
	v_lshlrev_b32_e32 v1, 2, v191
	s_lshl_b32 s0, s34, 5
	v_add_u32_e32 v70, 12, v1
	v_cmp_eq_u32_e32 vcc, 0, v0
	s_add_i32 s0, s0, s33
	s_mov_b32 s1, 0x3f3504f3
	v_cndmask_b32_e32 v0, v70, v1, vcc
	v_or_b32_e32 v0, s0, v0
	v_ashrrev_i32_e32 v1, 31, v0
	v_lshl_add_u64 v[78:79], v[0:1], 1, s[4:5]
	v_mul_f32_e64 v1, |v74|, s1
	s_mov_b32 s3, 0x3ea7ba05
	v_fma_f32 v0, v1, s3, 1.0
	v_mul_f32_e64 v1, v1, -v1
	v_mul_f32_e32 v1, 0x3fb8aa3b, v1
	v_mul_f32_e64 v71, |v75|, s1
	v_exp_f32_e32 v70, v1
	v_fma_f32 v1, v71, s3, 1.0
	v_rcp_f32_e32 v0, v0
	v_rcp_f32_e32 v1, v1
	s_mov_b32 s8, 0xbfba00e3
	s_mov_b32 s0, 0x3f87dc22
	v_mov_b64_e32 v[80:81], s[8:9]
	v_pk_fma_f32 v[72:73], v[0:1], s[0:1], v[80:81] op_sel_hi:[1,0,0]
	v_mul_f32_e64 v71, v71, -v71
	s_mov_b32 s2, 0x3fb5f0e3
	v_mul_f32_e32 v71, 0x3fb8aa3b, v71
	v_pk_fma_f32 v[72:73], v[72:73], v[0:1], s[2:3] op_sel_hi:[1,1,0]
	s_mov_b32 s4, 0xbe91a98e
	v_exp_f32_e32 v71, v71
	v_pk_fma_f32 v[72:73], v[72:73], v[0:1], s[4:5] op_sel_hi:[1,1,0]
	s_mov_b32 s6, 0x3e827906
	v_pk_fma_f32 v[72:73], v[72:73], v[0:1], s[6:7] op_sel_hi:[1,1,0]
	v_cmp_le_f32_e32 vcc, 0, v75
	v_pk_mul_f32 v[0:1], v[0:1], v[72:73]
	s_nop 0
	v_pk_mul_f32 v[0:1], v[0:1], 0.5 op_sel_hi:[1,0]
	s_nop 0
	v_pk_mul_f32 v[72:73], v[70:71], v[0:1]
	v_pk_fma_f32 v[0:1], v[70:71], v[0:1], 1.0 op_sel_hi:[1,1,0] neg_lo:[1,0,0] neg_hi:[1,0,0]
	v_mul_f32_e64 v71, |v76|, s1
	v_cndmask_b32_e32 v1, v73, v1, vcc
	v_cmp_le_f32_e32 vcc, 0, v74
	v_mul_f32_e64 v73, |v77|, s1
	s_nop 0
	v_cndmask_b32_e32 v0, v72, v0, vcc
	v_pk_mul_f32 v[0:1], v[74:75], v[0:1]
	v_cmp_le_f32_e32 vcc, 0, v77
	s_waitcnt vmcnt(0)
	v_pk_mul_f32 v[0:1], v[220:221], v[0:1] op_sel_hi:[0,1]
	v_cvt_pk_f16_f32 v70, v0, v1
	v_fma_f32 v0, v71, s3, 1.0
	v_fma_f32 v1, v73, s3, 1.0
	v_rcp_f32_e32 v0, v0
	v_rcp_f32_e32 v1, v1
	v_mul_f32_e64 v71, v71, -v71
	v_mul_f32_e32 v71, 0x3fb8aa3b, v71
	v_exp_f32_e32 v72, v71
	v_pk_fma_f32 v[74:75], v[0:1], s[0:1], v[80:81] op_sel_hi:[1,0,0]
	v_mul_f32_e64 v71, v73, -v73
	v_mul_f32_e32 v71, 0x3fb8aa3b, v71
	v_pk_fma_f32 v[74:75], v[74:75], v[0:1], s[2:3] op_sel_hi:[1,1,0]
	v_exp_f32_e32 v73, v71
	v_pk_fma_f32 v[74:75], v[74:75], v[0:1], s[4:5] op_sel_hi:[1,1,0]
	s_nop 0
	v_pk_fma_f32 v[74:75], v[74:75], v[0:1], s[6:7] op_sel_hi:[1,1,0]
	s_nop 0
	v_pk_mul_f32 v[0:1], v[0:1], v[74:75]
	s_nop 0
	v_pk_mul_f32 v[0:1], v[0:1], 0.5 op_sel_hi:[1,0]
	s_nop 0
	v_pk_mul_f32 v[74:75], v[72:73], v[0:1]
	v_pk_fma_f32 v[0:1], v[72:73], v[0:1], 1.0 op_sel_hi:[1,1,0] neg_lo:[1,0,0] neg_hi:[1,0,0]
	v_mul_f32_e64 v72, |v66|, s1
	v_cndmask_b32_e32 v1, v75, v1, vcc
	v_cmp_le_f32_e32 vcc, 0, v76
	v_mul_f32_e64 v73, |v67|, s1
	s_nop 0
	v_cndmask_b32_e32 v0, v74, v0, vcc
	v_pk_mul_f32 v[0:1], v[76:77], v[0:1]
	v_cmp_le_f32_e32 vcc, 0, v67
	v_pk_mul_f32 v[0:1], v[220:221], v[0:1] op_sel_hi:[0,1]
	v_cvt_pk_f16_f32 v71, v0, v1
	v_fma_f32 v0, v72, s3, 1.0
	v_fma_f32 v1, v73, s3, 1.0
	v_rcp_f32_e32 v0, v0
	v_rcp_f32_e32 v1, v1
	v_mul_f32_e64 v72, v72, -v72
	v_mul_f32_e64 v73, v73, -v73
	v_mul_f32_e32 v72, 0x3fb8aa3b, v72
	v_pk_fma_f32 v[74:75], v[0:1], s[0:1], v[80:81] op_sel_hi:[1,0,0]
	v_mul_f32_e32 v73, 0x3fb8aa3b, v73
	v_pk_fma_f32 v[74:75], v[74:75], v[0:1], s[2:3] op_sel_hi:[1,1,0]
	v_exp_f32_e32 v72, v72
	v_exp_f32_e32 v73, v73
	v_pk_fma_f32 v[74:75], v[74:75], v[0:1], s[4:5] op_sel_hi:[1,1,0]
	s_nop 0
	v_pk_fma_f32 v[74:75], v[74:75], v[0:1], s[6:7] op_sel_hi:[1,1,0]
	s_nop 0
	v_pk_mul_f32 v[0:1], v[0:1], v[74:75]
	s_nop 0
	v_pk_mul_f32 v[0:1], v[0:1], 0.5 op_sel_hi:[1,0]
	s_nop 0
	v_pk_mul_f32 v[74:75], v[72:73], v[0:1]
	v_pk_fma_f32 v[0:1], v[72:73], v[0:1], 1.0 op_sel_hi:[1,1,0] neg_lo:[1,0,0] neg_hi:[1,0,0]
	s_nop 0
	v_cndmask_b32_e32 v1, v75, v1, vcc
	v_cmp_le_f32_e32 vcc, 0, v66
	s_nop 1
	v_cndmask_b32_e32 v0, v74, v0, vcc
	v_pk_mul_f32 v[0:1], v[66:67], v[0:1]
	v_mul_f32_e64 v66, |v68|, s1
	v_pk_mul_f32 v[0:1], v[220:221], v[0:1] op_sel_hi:[0,1]
	v_mul_f32_e64 v67, |v69|, s1
	v_cvt_pk_f16_f32 v72, v0, v1
	v_fma_f32 v0, v66, s3, 1.0
	v_fma_f32 v1, v67, s3, 1.0
	v_rcp_f32_e32 v0, v0
	v_rcp_f32_e32 v1, v1
	v_mul_f32_e64 v66, v66, -v66
	v_mul_f32_e64 v67, v67, -v67
	v_mul_f32_e32 v66, 0x3fb8aa3b, v66
	v_pk_fma_f32 v[74:75], v[0:1], s[0:1], v[80:81] op_sel_hi:[1,0,0]
	v_mul_f32_e32 v67, 0x3fb8aa3b, v67
	v_pk_fma_f32 v[74:75], v[74:75], v[0:1], s[2:3] op_sel_hi:[1,1,0]
	v_exp_f32_e32 v66, v66
	v_exp_f32_e32 v67, v67
	v_pk_fma_f32 v[74:75], v[74:75], v[0:1], s[4:5] op_sel_hi:[1,1,0]
	v_cmp_le_f32_e32 vcc, 0, v69
	v_pk_fma_f32 v[74:75], v[74:75], v[0:1], s[6:7] op_sel_hi:[1,1,0]
	v_permlane16_swap_b32_e32 v70, v72
	v_pk_mul_f32 v[0:1], v[0:1], v[74:75]
	s_nop 0
	v_pk_mul_f32 v[0:1], v[0:1], 0.5 op_sel_hi:[1,0]
	s_nop 0
	v_pk_mul_f32 v[74:75], v[66:67], v[0:1]
	v_pk_fma_f32 v[0:1], v[66:67], v[0:1], 1.0 op_sel_hi:[1,1,0] neg_lo:[1,0,0] neg_hi:[1,0,0]
	s_nop 0
	v_cndmask_b32_e32 v1, v75, v1, vcc
	v_cmp_le_f32_e32 vcc, 0, v68
	s_nop 1
	v_cndmask_b32_e32 v0, v74, v0, vcc
	v_pk_mul_f32 v[0:1], v[68:69], v[0:1]
	v_cmp_lt_i32_e32 vcc, -1, v218
	v_pk_mul_f32 v[0:1], v[220:221], v[0:1] op_sel_hi:[0,1]
	v_cvt_pk_f16_f32 v73, v0, v1
	s_nop 1
	s_nop 0
	v_permlane16_swap_b32_e32 v71, v73
	s_and_saveexec_b64 s[10:11], vcc
	s_cbranch_execz .LBB2_116
	v_mov_b32_e32 v219, 0
	v_lshlrev_b64 v[0:1], 10, v[218:219]
	v_lshl_add_u64 v[0:1], v[78:79], 0, v[0:1]
	global_store_dwordx4 v[0:1], v[70:73], off sc1
.LBB2_116:
	s_or_b64 exec, exec, s[10:11]
	v_mul_f32_e64 v1, |v62|, s1
	v_mul_f32_e64 v67, |v63|, s1
	v_fma_f32 v0, v1, s3, 1.0
	v_mul_f32_e64 v66, v1, -v1
	v_fma_f32 v1, v67, s3, 1.0
	v_rcp_f32_e32 v0, v0
	v_rcp_f32_e32 v1, v1
	v_mov_b64_e32 v[68:69], s[8:9]
	v_mul_f32_e64 v67, v67, -v67
	v_mul_f32_e32 v66, 0x3fb8aa3b, v66
	v_pk_fma_f32 v[70:71], v[0:1], s[0:1], v[68:69] op_sel_hi:[1,0,0]
	v_mul_f32_e32 v67, 0x3fb8aa3b, v67
	v_pk_fma_f32 v[70:71], v[70:71], v[0:1], s[2:3] op_sel_hi:[1,1,0]
	v_exp_f32_e32 v66, v66
	v_exp_f32_e32 v67, v67
	v_pk_fma_f32 v[70:71], v[70:71], v[0:1], s[4:5] op_sel_hi:[1,1,0]
	v_cmp_le_f32_e32 vcc, 0, v63
	v_pk_fma_f32 v[70:71], v[70:71], v[0:1], s[6:7] op_sel_hi:[1,1,0]
	s_nop 0
	v_pk_mul_f32 v[0:1], v[0:1], v[70:71]
	s_nop 0
	v_pk_mul_f32 v[0:1], v[0:1], 0.5 op_sel_hi:[1,0]
	s_nop 0
	v_pk_mul_f32 v[70:71], v[66:67], v[0:1]
	v_pk_fma_f32 v[0:1], v[66:67], v[0:1], 1.0 op_sel_hi:[1,1,0] neg_lo:[1,0,0] neg_hi:[1,0,0]
	v_mul_f32_e64 v67, |v65|, s1
	v_cndmask_b32_e32 v1, v71, v1, vcc
	v_cmp_le_f32_e32 vcc, 0, v62
	s_nop 1
	v_cndmask_b32_e32 v0, v70, v0, vcc
	v_pk_mul_f32 v[0:1], v[62:63], v[0:1]
	v_mul_f32_e64 v63, |v64|, s1
	v_pk_mul_f32 v[0:1], v[216:217], v[0:1] op_sel_hi:[0,1]
	v_cvt_pk_f16_f32 v62, v0, v1
	v_fma_f32 v0, v63, s3, 1.0
	v_fma_f32 v1, v67, s3, 1.0
	v_rcp_f32_e32 v0, v0
	v_rcp_f32_e32 v1, v1
	v_mul_f32_e64 v63, v63, -v63
	v_mul_f32_e32 v63, 0x3fb8aa3b, v63
	v_exp_f32_e32 v66, v63
	v_pk_fma_f32 v[70:71], v[0:1], s[0:1], v[68:69] op_sel_hi:[1,0,0]
	v_mul_f32_e64 v63, v67, -v67
	v_mul_f32_e32 v63, 0x3fb8aa3b, v63
	v_pk_fma_f32 v[70:71], v[70:71], v[0:1], s[2:3] op_sel_hi:[1,1,0]
	v_exp_f32_e32 v67, v63
	v_pk_fma_f32 v[70:71], v[70:71], v[0:1], s[4:5] op_sel_hi:[1,1,0]
	v_cmp_le_f32_e32 vcc, 0, v65
	v_pk_fma_f32 v[70:71], v[70:71], v[0:1], s[6:7] op_sel_hi:[1,1,0]
	s_nop 0
	v_pk_mul_f32 v[0:1], v[0:1], v[70:71]
	s_nop 0
	v_pk_mul_f32 v[0:1], v[0:1], 0.5 op_sel_hi:[1,0]
	s_nop 0
	v_pk_mul_f32 v[70:71], v[66:67], v[0:1]
	v_pk_fma_f32 v[0:1], v[66:67], v[0:1], 1.0 op_sel_hi:[1,1,0] neg_lo:[1,0,0] neg_hi:[1,0,0]
	s_nop 0
	v_cndmask_b32_e32 v1, v71, v1, vcc
	v_cmp_le_f32_e32 vcc, 0, v64
	s_nop 1
	v_cndmask_b32_e32 v0, v70, v0, vcc
	v_pk_mul_f32 v[0:1], v[64:65], v[0:1]
	v_mul_f32_e64 v64, |v58|, s1
	v_pk_mul_f32 v[0:1], v[216:217], v[0:1] op_sel_hi:[0,1]
	v_mul_f32_e64 v65, |v59|, s1
	v_cvt_pk_f16_f32 v63, v0, v1
	v_fma_f32 v0, v64, s3, 1.0
	v_fma_f32 v1, v65, s3, 1.0
	v_rcp_f32_e32 v0, v0
	v_rcp_f32_e32 v1, v1
	v_mul_f32_e64 v64, v64, -v64
	v_mul_f32_e64 v65, v65, -v65
	v_mul_f32_e32 v64, 0x3fb8aa3b, v64
	v_pk_fma_f32 v[66:67], v[0:1], s[0:1], v[68:69] op_sel_hi:[1,0,0]
	v_mul_f32_e32 v65, 0x3fb8aa3b, v65
	v_pk_fma_f32 v[66:67], v[66:67], v[0:1], s[2:3] op_sel_hi:[1,1,0]
	v_exp_f32_e32 v64, v64
	v_exp_f32_e32 v65, v65
	v_pk_fma_f32 v[66:67], v[66:67], v[0:1], s[4:5] op_sel_hi:[1,1,0]
	v_cmp_le_f32_e32 vcc, 0, v59
	v_pk_fma_f32 v[66:67], v[66:67], v[0:1], s[6:7] op_sel_hi:[1,1,0]
	s_nop 0
	v_pk_mul_f32 v[0:1], v[0:1], v[66:67]
	s_nop 0
	v_pk_mul_f32 v[0:1], v[0:1], 0.5 op_sel_hi:[1,0]
	s_nop 0
	v_pk_mul_f32 v[66:67], v[64:65], v[0:1]
	v_pk_fma_f32 v[0:1], v[64:65], v[0:1], 1.0 op_sel_hi:[1,1,0] neg_lo:[1,0,0] neg_hi:[1,0,0]
	s_nop 0
	v_cndmask_b32_e32 v1, v67, v1, vcc
	v_cmp_le_f32_e32 vcc, 0, v58
	s_nop 1
	v_cndmask_b32_e32 v0, v66, v0, vcc
	v_pk_mul_f32 v[0:1], v[58:59], v[0:1]
	v_mul_f32_e64 v58, |v60|, s1
	v_pk_mul_f32 v[0:1], v[216:217], v[0:1] op_sel_hi:[0,1]
	v_mul_f32_e64 v59, |v61|, s1
	v_cvt_pk_f16_f32 v64, v0, v1
	v_fma_f32 v0, v58, s3, 1.0
	v_fma_f32 v1, v59, s3, 1.0
	v_rcp_f32_e32 v0, v0
	v_rcp_f32_e32 v1, v1
	v_mul_f32_e64 v58, v58, -v58
	v_mul_f32_e64 v59, v59, -v59
	v_mul_f32_e32 v58, 0x3fb8aa3b, v58
	v_pk_fma_f32 v[66:67], v[0:1], s[0:1], v[68:69] op_sel_hi:[1,0,0]
	v_mul_f32_e32 v59, 0x3fb8aa3b, v59
	v_pk_fma_f32 v[66:67], v[66:67], v[0:1], s[2:3] op_sel_hi:[1,1,0]
	v_exp_f32_e32 v58, v58
	v_exp_f32_e32 v59, v59
	v_pk_fma_f32 v[66:67], v[66:67], v[0:1], s[4:5] op_sel_hi:[1,1,0]
	v_cmp_le_f32_e32 vcc, 0, v61
	v_pk_fma_f32 v[66:67], v[66:67], v[0:1], s[6:7] op_sel_hi:[1,1,0]
	v_permlane16_swap_b32_e32 v62, v64
	v_pk_mul_f32 v[0:1], v[0:1], v[66:67]
	s_nop 0
	v_pk_mul_f32 v[0:1], v[0:1], 0.5 op_sel_hi:[1,0]
	s_nop 0
	v_pk_mul_f32 v[66:67], v[58:59], v[0:1]
	v_pk_fma_f32 v[0:1], v[58:59], v[0:1], 1.0 op_sel_hi:[1,1,0] neg_lo:[1,0,0] neg_hi:[1,0,0]
	s_nop 0
	v_cndmask_b32_e32 v1, v67, v1, vcc
	v_cmp_le_f32_e32 vcc, 0, v60
	s_nop 1
	v_cndmask_b32_e32 v0, v66, v0, vcc
	v_pk_mul_f32 v[0:1], v[60:61], v[0:1]
	v_cmp_lt_i32_e32 vcc, -1, v214
	v_pk_mul_f32 v[0:1], v[216:217], v[0:1] op_sel_hi:[0,1]
	v_cvt_pk_f16_f32 v65, v0, v1
	s_nop 1
	s_nop 0
	v_permlane16_swap_b32_e32 v63, v65
	s_and_saveexec_b64 s[0:1], vcc
	s_cbranch_execz .LBB2_118
	v_mov_b32_e32 v215, 0
	v_lshlrev_b64 v[0:1], 10, v[214:215]
	v_lshl_add_u64 v[0:1], v[78:79], 0, v[0:1]
	global_store_dwordx4 v[0:1], v[62:65], off sc1
.LBB2_118:
	s_or_b64 exec, exec, s[0:1]
	s_mov_b32 s1, 0x3f3504f3
	v_mul_f32_e64 v1, |v54|, s1
	v_fma_f32 v0, v1, s3, 1.0
	v_mul_f32_e64 v1, v1, -v1
	v_mul_f32_e32 v1, 0x3fb8aa3b, v1
	v_mul_f32_e64 v59, |v55|, s1
	v_exp_f32_e32 v58, v1
	v_fma_f32 v1, v59, s3, 1.0
	v_rcp_f32_e32 v0, v0
	v_rcp_f32_e32 v1, v1
	s_mov_b32 s0, 0x3f87dc22
	v_mov_b64_e32 v[60:61], s[8:9]
	v_mul_f32_e64 v59, v59, -v59
	v_pk_fma_f32 v[62:63], v[0:1], s[0:1], v[60:61] op_sel_hi:[1,0,0]
	v_mul_f32_e32 v59, 0x3fb8aa3b, v59
	v_pk_fma_f32 v[62:63], v[62:63], v[0:1], s[2:3] op_sel_hi:[1,1,0]
	v_exp_f32_e32 v59, v59
	v_pk_fma_f32 v[62:63], v[62:63], v[0:1], s[4:5] op_sel_hi:[1,1,0]
	v_cmp_le_f32_e32 vcc, 0, v55
	v_pk_fma_f32 v[62:63], v[62:63], v[0:1], s[6:7] op_sel_hi:[1,1,0]
	s_nop 0
	v_pk_mul_f32 v[0:1], v[0:1], v[62:63]
	s_nop 0
	v_pk_mul_f32 v[0:1], v[0:1], 0.5 op_sel_hi:[1,0]
	s_nop 0
	v_pk_mul_f32 v[62:63], v[58:59], v[0:1]
	v_pk_fma_f32 v[0:1], v[58:59], v[0:1], 1.0 op_sel_hi:[1,1,0] neg_lo:[1,0,0] neg_hi:[1,0,0]
	v_mul_f32_e64 v59, |v57|, s1
	v_cndmask_b32_e32 v1, v63, v1, vcc
	v_cmp_le_f32_e32 vcc, 0, v54
	s_nop 1
	v_cndmask_b32_e32 v0, v62, v0, vcc
	v_pk_mul_f32 v[0:1], v[54:55], v[0:1]
	v_mul_f32_e64 v55, |v56|, s1
	v_pk_mul_f32 v[0:1], v[212:213], v[0:1] op_sel_hi:[0,1]
	v_cvt_pk_f16_f32 v54, v0, v1
	v_fma_f32 v0, v55, s3, 1.0
	v_fma_f32 v1, v59, s3, 1.0
	v_rcp_f32_e32 v0, v0
	v_rcp_f32_e32 v1, v1
	v_mul_f32_e64 v55, v55, -v55
	v_mul_f32_e32 v55, 0x3fb8aa3b, v55
	v_exp_f32_e32 v58, v55
	v_pk_fma_f32 v[62:63], v[0:1], s[0:1], v[60:61] op_sel_hi:[1,0,0]
	v_mul_f32_e64 v55, v59, -v59
	v_mul_f32_e32 v55, 0x3fb8aa3b, v55
	v_pk_fma_f32 v[62:63], v[62:63], v[0:1], s[2:3] op_sel_hi:[1,1,0]
	v_exp_f32_e32 v59, v55
	v_pk_fma_f32 v[62:63], v[62:63], v[0:1], s[4:5] op_sel_hi:[1,1,0]
	v_cmp_le_f32_e32 vcc, 0, v57
	v_pk_fma_f32 v[62:63], v[62:63], v[0:1], s[6:7] op_sel_hi:[1,1,0]
	s_nop 0
	v_pk_mul_f32 v[0:1], v[0:1], v[62:63]
	s_nop 0
	v_pk_mul_f32 v[0:1], v[0:1], 0.5 op_sel_hi:[1,0]
	s_nop 0
	v_pk_mul_f32 v[62:63], v[58:59], v[0:1]
	v_pk_fma_f32 v[0:1], v[58:59], v[0:1], 1.0 op_sel_hi:[1,1,0] neg_lo:[1,0,0] neg_hi:[1,0,0]
	s_nop 0
	v_cndmask_b32_e32 v1, v63, v1, vcc
	v_cmp_le_f32_e32 vcc, 0, v56
	s_nop 1
	v_cndmask_b32_e32 v0, v62, v0, vcc
	v_pk_mul_f32 v[0:1], v[56:57], v[0:1]
	v_mul_f32_e64 v56, |v50|, s1
	v_pk_mul_f32 v[0:1], v[212:213], v[0:1] op_sel_hi:[0,1]
	v_mul_f32_e64 v57, |v51|, s1
	v_cvt_pk_f16_f32 v55, v0, v1
	v_fma_f32 v0, v56, s3, 1.0
	v_fma_f32 v1, v57, s3, 1.0
	v_rcp_f32_e32 v0, v0
	v_rcp_f32_e32 v1, v1
	v_mul_f32_e64 v56, v56, -v56
	v_mul_f32_e64 v57, v57, -v57
	v_mul_f32_e32 v56, 0x3fb8aa3b, v56
	v_pk_fma_f32 v[58:59], v[0:1], s[0:1], v[60:61] op_sel_hi:[1,0,0]
	v_mul_f32_e32 v57, 0x3fb8aa3b, v57
	v_pk_fma_f32 v[58:59], v[58:59], v[0:1], s[2:3] op_sel_hi:[1,1,0]
	v_exp_f32_e32 v56, v56
	v_exp_f32_e32 v57, v57
	v_pk_fma_f32 v[58:59], v[58:59], v[0:1], s[4:5] op_sel_hi:[1,1,0]
	v_cmp_le_f32_e32 vcc, 0, v51
	v_pk_fma_f32 v[58:59], v[58:59], v[0:1], s[6:7] op_sel_hi:[1,1,0]
	s_nop 0
	v_pk_mul_f32 v[0:1], v[0:1], v[58:59]
	s_nop 0
	v_pk_mul_f32 v[0:1], v[0:1], 0.5 op_sel_hi:[1,0]
	s_nop 0
	v_pk_mul_f32 v[58:59], v[56:57], v[0:1]
	v_pk_fma_f32 v[0:1], v[56:57], v[0:1], 1.0 op_sel_hi:[1,1,0] neg_lo:[1,0,0] neg_hi:[1,0,0]
	s_nop 0
	v_cndmask_b32_e32 v1, v59, v1, vcc
	v_cmp_le_f32_e32 vcc, 0, v50
	s_nop 1
	v_cndmask_b32_e32 v0, v58, v0, vcc
	v_pk_mul_f32 v[0:1], v[50:51], v[0:1]
	v_mul_f32_e64 v50, |v52|, s1
	v_pk_mul_f32 v[0:1], v[212:213], v[0:1] op_sel_hi:[0,1]
	v_mul_f32_e64 v51, |v53|, s1
	v_cvt_pk_f16_f32 v56, v0, v1
	v_fma_f32 v0, v50, s3, 1.0
	v_fma_f32 v1, v51, s3, 1.0
	v_rcp_f32_e32 v0, v0
	v_rcp_f32_e32 v1, v1
	v_mul_f32_e64 v50, v50, -v50
	v_mul_f32_e64 v51, v51, -v51
	v_mul_f32_e32 v50, 0x3fb8aa3b, v50
	v_pk_fma_f32 v[58:59], v[0:1], s[0:1], v[60:61] op_sel_hi:[1,0,0]
	v_mul_f32_e32 v51, 0x3fb8aa3b, v51
	v_pk_fma_f32 v[58:59], v[58:59], v[0:1], s[2:3] op_sel_hi:[1,1,0]
	v_exp_f32_e32 v50, v50
	v_exp_f32_e32 v51, v51
	v_pk_fma_f32 v[58:59], v[58:59], v[0:1], s[4:5] op_sel_hi:[1,1,0]
	v_cmp_le_f32_e32 vcc, 0, v53
	v_pk_fma_f32 v[58:59], v[58:59], v[0:1], s[6:7] op_sel_hi:[1,1,0]
	v_permlane16_swap_b32_e32 v54, v56
	v_pk_mul_f32 v[0:1], v[0:1], v[58:59]
	s_nop 0
	v_pk_mul_f32 v[0:1], v[0:1], 0.5 op_sel_hi:[1,0]
	s_nop 0
	v_pk_mul_f32 v[58:59], v[50:51], v[0:1]
	v_pk_fma_f32 v[0:1], v[50:51], v[0:1], 1.0 op_sel_hi:[1,1,0] neg_lo:[1,0,0] neg_hi:[1,0,0]
	s_nop 0
	v_cndmask_b32_e32 v1, v59, v1, vcc
	v_cmp_le_f32_e32 vcc, 0, v52
	s_nop 1
	v_cndmask_b32_e32 v0, v58, v0, vcc
	v_pk_mul_f32 v[0:1], v[52:53], v[0:1]
	v_cmp_lt_i32_e32 vcc, -1, v210
	v_pk_mul_f32 v[0:1], v[212:213], v[0:1] op_sel_hi:[0,1]
	v_cvt_pk_f16_f32 v57, v0, v1
	s_nop 1
	s_nop 0
	v_permlane16_swap_b32_e32 v55, v57
	s_and_saveexec_b64 s[10:11], vcc
	s_cbranch_execz .LBB2_120
	v_mov_b32_e32 v211, 0
	v_lshlrev_b64 v[0:1], 10, v[210:211]
	v_lshl_add_u64 v[0:1], v[78:79], 0, v[0:1]
	global_store_dwordx4 v[0:1], v[54:57], off sc1
.LBB2_120:
	s_or_b64 exec, exec, s[10:11]
	v_mul_f32_e64 v1, |v46|, s1
	v_mul_f32_e64 v51, |v47|, s1
	v_fma_f32 v0, v1, s3, 1.0
	v_mul_f32_e64 v50, v1, -v1
	v_fma_f32 v1, v51, s3, 1.0
	v_rcp_f32_e32 v0, v0
	v_rcp_f32_e32 v1, v1
	v_mov_b64_e32 v[52:53], s[8:9]
	v_mul_f32_e64 v51, v51, -v51
	v_mul_f32_e32 v50, 0x3fb8aa3b, v50
	v_pk_fma_f32 v[54:55], v[0:1], s[0:1], v[52:53] op_sel_hi:[1,0,0]
	v_mul_f32_e32 v51, 0x3fb8aa3b, v51
	v_pk_fma_f32 v[54:55], v[54:55], v[0:1], s[2:3] op_sel_hi:[1,1,0]
	v_exp_f32_e32 v50, v50
	v_exp_f32_e32 v51, v51
	v_pk_fma_f32 v[54:55], v[54:55], v[0:1], s[4:5] op_sel_hi:[1,1,0]
	v_cmp_le_f32_e32 vcc, 0, v47
	v_pk_fma_f32 v[54:55], v[54:55], v[0:1], s[6:7] op_sel_hi:[1,1,0]
	s_nop 0
	v_pk_mul_f32 v[0:1], v[0:1], v[54:55]
	s_nop 0
	v_pk_mul_f32 v[0:1], v[0:1], 0.5 op_sel_hi:[1,0]
	s_nop 0
	v_pk_mul_f32 v[54:55], v[50:51], v[0:1]
	v_pk_fma_f32 v[0:1], v[50:51], v[0:1], 1.0 op_sel_hi:[1,1,0] neg_lo:[1,0,0] neg_hi:[1,0,0]
	v_mul_f32_e64 v51, |v49|, s1
	v_cndmask_b32_e32 v1, v55, v1, vcc
	v_cmp_le_f32_e32 vcc, 0, v46
	s_nop 1
	v_cndmask_b32_e32 v0, v54, v0, vcc
	v_pk_mul_f32 v[0:1], v[46:47], v[0:1]
	v_mul_f32_e64 v47, |v48|, s1
	v_pk_mul_f32 v[0:1], v[208:209], v[0:1] op_sel_hi:[0,1]
	v_cvt_pk_f16_f32 v46, v0, v1
	v_fma_f32 v0, v47, s3, 1.0
	v_fma_f32 v1, v51, s3, 1.0
	v_rcp_f32_e32 v0, v0
	v_rcp_f32_e32 v1, v1
	v_mul_f32_e64 v47, v47, -v47
	v_mul_f32_e32 v47, 0x3fb8aa3b, v47
	v_exp_f32_e32 v50, v47
	v_pk_fma_f32 v[54:55], v[0:1], s[0:1], v[52:53] op_sel_hi:[1,0,0]
	v_mul_f32_e64 v47, v51, -v51
	v_mul_f32_e32 v47, 0x3fb8aa3b, v47
	v_pk_fma_f32 v[54:55], v[54:55], v[0:1], s[2:3] op_sel_hi:[1,1,0]
	v_exp_f32_e32 v51, v47
	v_pk_fma_f32 v[54:55], v[54:55], v[0:1], s[4:5] op_sel_hi:[1,1,0]
	v_cmp_le_f32_e32 vcc, 0, v49
	v_pk_fma_f32 v[54:55], v[54:55], v[0:1], s[6:7] op_sel_hi:[1,1,0]
	s_nop 0
	v_pk_mul_f32 v[0:1], v[0:1], v[54:55]
	s_nop 0
	v_pk_mul_f32 v[0:1], v[0:1], 0.5 op_sel_hi:[1,0]
	s_nop 0
	v_pk_mul_f32 v[54:55], v[50:51], v[0:1]
	v_pk_fma_f32 v[0:1], v[50:51], v[0:1], 1.0 op_sel_hi:[1,1,0] neg_lo:[1,0,0] neg_hi:[1,0,0]
	s_nop 0
	v_cndmask_b32_e32 v1, v55, v1, vcc
	v_cmp_le_f32_e32 vcc, 0, v48
	s_nop 1
	v_cndmask_b32_e32 v0, v54, v0, vcc
	v_pk_mul_f32 v[0:1], v[48:49], v[0:1]
	v_mul_f32_e64 v48, |v42|, s1
	v_pk_mul_f32 v[0:1], v[208:209], v[0:1] op_sel_hi:[0,1]
	v_mul_f32_e64 v49, |v43|, s1
	v_cvt_pk_f16_f32 v47, v0, v1
	v_fma_f32 v0, v48, s3, 1.0
	v_fma_f32 v1, v49, s3, 1.0
	v_rcp_f32_e32 v0, v0
	v_rcp_f32_e32 v1, v1
	v_mul_f32_e64 v48, v48, -v48
	v_mul_f32_e64 v49, v49, -v49
	v_mul_f32_e32 v48, 0x3fb8aa3b, v48
	v_pk_fma_f32 v[50:51], v[0:1], s[0:1], v[52:53] op_sel_hi:[1,0,0]
	v_mul_f32_e32 v49, 0x3fb8aa3b, v49
	v_pk_fma_f32 v[50:51], v[50:51], v[0:1], s[2:3] op_sel_hi:[1,1,0]
	v_exp_f32_e32 v48, v48
	v_exp_f32_e32 v49, v49
	v_pk_fma_f32 v[50:51], v[50:51], v[0:1], s[4:5] op_sel_hi:[1,1,0]
	v_cmp_le_f32_e32 vcc, 0, v43
	v_pk_fma_f32 v[50:51], v[50:51], v[0:1], s[6:7] op_sel_hi:[1,1,0]
	s_nop 0
	v_pk_mul_f32 v[0:1], v[0:1], v[50:51]
	s_nop 0
	v_pk_mul_f32 v[0:1], v[0:1], 0.5 op_sel_hi:[1,0]
	s_nop 0
	v_pk_mul_f32 v[50:51], v[48:49], v[0:1]
	v_pk_fma_f32 v[0:1], v[48:49], v[0:1], 1.0 op_sel_hi:[1,1,0] neg_lo:[1,0,0] neg_hi:[1,0,0]
	s_nop 0
	v_cndmask_b32_e32 v1, v51, v1, vcc
	v_cmp_le_f32_e32 vcc, 0, v42
	s_nop 1
	v_cndmask_b32_e32 v0, v50, v0, vcc
	v_pk_mul_f32 v[0:1], v[42:43], v[0:1]
	v_mul_f32_e64 v42, |v44|, s1
	v_pk_mul_f32 v[0:1], v[208:209], v[0:1] op_sel_hi:[0,1]
	v_mul_f32_e64 v43, |v45|, s1
	v_cvt_pk_f16_f32 v48, v0, v1
	v_fma_f32 v0, v42, s3, 1.0
	v_fma_f32 v1, v43, s3, 1.0
	v_rcp_f32_e32 v0, v0
	v_rcp_f32_e32 v1, v1
	v_mul_f32_e64 v42, v42, -v42
	v_mul_f32_e64 v43, v43, -v43
	v_mul_f32_e32 v42, 0x3fb8aa3b, v42
	v_pk_fma_f32 v[50:51], v[0:1], s[0:1], v[52:53] op_sel_hi:[1,0,0]
	v_mul_f32_e32 v43, 0x3fb8aa3b, v43
	v_pk_fma_f32 v[50:51], v[50:51], v[0:1], s[2:3] op_sel_hi:[1,1,0]
	v_exp_f32_e32 v42, v42
	v_exp_f32_e32 v43, v43
	v_pk_fma_f32 v[50:51], v[50:51], v[0:1], s[4:5] op_sel_hi:[1,1,0]
	v_cmp_le_f32_e32 vcc, 0, v45
	v_pk_fma_f32 v[50:51], v[50:51], v[0:1], s[6:7] op_sel_hi:[1,1,0]
	v_permlane16_swap_b32_e32 v46, v48
	v_pk_mul_f32 v[0:1], v[0:1], v[50:51]
	s_nop 0
	v_pk_mul_f32 v[0:1], v[0:1], 0.5 op_sel_hi:[1,0]
	s_nop 0
	v_pk_mul_f32 v[50:51], v[42:43], v[0:1]
	v_pk_fma_f32 v[0:1], v[42:43], v[0:1], 1.0 op_sel_hi:[1,1,0] neg_lo:[1,0,0] neg_hi:[1,0,0]
	s_nop 0
	v_cndmask_b32_e32 v1, v51, v1, vcc
	v_cmp_le_f32_e32 vcc, 0, v44
	s_nop 1
	v_cndmask_b32_e32 v0, v50, v0, vcc
	v_pk_mul_f32 v[0:1], v[44:45], v[0:1]
	v_cmp_lt_i32_e32 vcc, -1, v206
	v_pk_mul_f32 v[0:1], v[208:209], v[0:1] op_sel_hi:[0,1]
	v_cvt_pk_f16_f32 v49, v0, v1
	s_nop 1
	s_nop 0
	v_permlane16_swap_b32_e32 v47, v49
	s_and_saveexec_b64 s[0:1], vcc
	s_cbranch_execz .LBB2_122
	v_mov_b32_e32 v207, 0
	v_lshlrev_b64 v[0:1], 10, v[206:207]
	v_lshl_add_u64 v[0:1], v[78:79], 0, v[0:1]
	global_store_dwordx4 v[0:1], v[46:49], off sc1
.LBB2_122:
	s_or_b64 exec, exec, s[0:1]
	s_mov_b32 s1, 0x3f3504f3
	v_mul_f32_e64 v1, |v38|, s1
	v_fma_f32 v0, v1, s3, 1.0
	v_mul_f32_e64 v1, v1, -v1
	v_mul_f32_e32 v1, 0x3fb8aa3b, v1
	v_mul_f32_e64 v43, |v39|, s1
	v_exp_f32_e32 v42, v1
	v_fma_f32 v1, v43, s3, 1.0
	v_rcp_f32_e32 v0, v0
	v_rcp_f32_e32 v1, v1
	s_mov_b32 s0, 0x3f87dc22
	v_mov_b64_e32 v[44:45], s[8:9]
	v_mul_f32_e64 v43, v43, -v43
	v_pk_fma_f32 v[46:47], v[0:1], s[0:1], v[44:45] op_sel_hi:[1,0,0]
	v_mul_f32_e32 v43, 0x3fb8aa3b, v43
	v_pk_fma_f32 v[46:47], v[46:47], v[0:1], s[2:3] op_sel_hi:[1,1,0]
	v_exp_f32_e32 v43, v43
	v_pk_fma_f32 v[46:47], v[46:47], v[0:1], s[4:5] op_sel_hi:[1,1,0]
	v_cmp_le_f32_e32 vcc, 0, v39
	v_pk_fma_f32 v[46:47], v[46:47], v[0:1], s[6:7] op_sel_hi:[1,1,0]
	s_nop 0
	v_pk_mul_f32 v[0:1], v[0:1], v[46:47]
	s_nop 0
	v_pk_mul_f32 v[0:1], v[0:1], 0.5 op_sel_hi:[1,0]
	s_nop 0
	v_pk_mul_f32 v[46:47], v[42:43], v[0:1]
	v_pk_fma_f32 v[0:1], v[42:43], v[0:1], 1.0 op_sel_hi:[1,1,0] neg_lo:[1,0,0] neg_hi:[1,0,0]
	v_mul_f32_e64 v43, |v41|, s1
	v_cndmask_b32_e32 v1, v47, v1, vcc
	v_cmp_le_f32_e32 vcc, 0, v38
	s_nop 1
	v_cndmask_b32_e32 v0, v46, v0, vcc
	v_pk_mul_f32 v[0:1], v[38:39], v[0:1]
	v_mul_f32_e64 v39, |v40|, s1
	v_pk_mul_f32 v[0:1], v[204:205], v[0:1] op_sel_hi:[0,1]
	v_cvt_pk_f16_f32 v38, v0, v1
	v_fma_f32 v0, v39, s3, 1.0
	v_fma_f32 v1, v43, s3, 1.0
	v_rcp_f32_e32 v0, v0
	v_rcp_f32_e32 v1, v1
	v_mul_f32_e64 v39, v39, -v39
	v_mul_f32_e32 v39, 0x3fb8aa3b, v39
	v_exp_f32_e32 v42, v39
	v_pk_fma_f32 v[46:47], v[0:1], s[0:1], v[44:45] op_sel_hi:[1,0,0]
	v_mul_f32_e64 v39, v43, -v43
	v_mul_f32_e32 v39, 0x3fb8aa3b, v39
	v_pk_fma_f32 v[46:47], v[46:47], v[0:1], s[2:3] op_sel_hi:[1,1,0]
	v_exp_f32_e32 v43, v39
	v_pk_fma_f32 v[46:47], v[46:47], v[0:1], s[4:5] op_sel_hi:[1,1,0]
	v_cmp_le_f32_e32 vcc, 0, v41
	v_pk_fma_f32 v[46:47], v[46:47], v[0:1], s[6:7] op_sel_hi:[1,1,0]
	s_nop 0
	v_pk_mul_f32 v[0:1], v[0:1], v[46:47]
	s_nop 0
	v_pk_mul_f32 v[0:1], v[0:1], 0.5 op_sel_hi:[1,0]
	s_nop 0
	v_pk_mul_f32 v[46:47], v[42:43], v[0:1]
	v_pk_fma_f32 v[0:1], v[42:43], v[0:1], 1.0 op_sel_hi:[1,1,0] neg_lo:[1,0,0] neg_hi:[1,0,0]
	s_nop 0
	v_cndmask_b32_e32 v1, v47, v1, vcc
	v_cmp_le_f32_e32 vcc, 0, v40
	s_nop 1
	v_cndmask_b32_e32 v0, v46, v0, vcc
	v_pk_mul_f32 v[0:1], v[40:41], v[0:1]
	v_mul_f32_e64 v40, |v34|, s1
	v_pk_mul_f32 v[0:1], v[204:205], v[0:1] op_sel_hi:[0,1]
	v_mul_f32_e64 v41, |v35|, s1
	v_cvt_pk_f16_f32 v39, v0, v1
	v_fma_f32 v0, v40, s3, 1.0
	v_fma_f32 v1, v41, s3, 1.0
	v_rcp_f32_e32 v0, v0
	v_rcp_f32_e32 v1, v1
	v_mul_f32_e64 v40, v40, -v40
	v_mul_f32_e64 v41, v41, -v41
	v_mul_f32_e32 v40, 0x3fb8aa3b, v40
	v_pk_fma_f32 v[42:43], v[0:1], s[0:1], v[44:45] op_sel_hi:[1,0,0]
	v_mul_f32_e32 v41, 0x3fb8aa3b, v41
	v_pk_fma_f32 v[42:43], v[42:43], v[0:1], s[2:3] op_sel_hi:[1,1,0]
	v_exp_f32_e32 v40, v40
	v_exp_f32_e32 v41, v41
	v_pk_fma_f32 v[42:43], v[42:43], v[0:1], s[4:5] op_sel_hi:[1,1,0]
	v_cmp_le_f32_e32 vcc, 0, v35
	v_pk_fma_f32 v[42:43], v[42:43], v[0:1], s[6:7] op_sel_hi:[1,1,0]
	s_nop 0
	v_pk_mul_f32 v[0:1], v[0:1], v[42:43]
	s_nop 0
	v_pk_mul_f32 v[0:1], v[0:1], 0.5 op_sel_hi:[1,0]
	s_nop 0
	v_pk_mul_f32 v[42:43], v[40:41], v[0:1]
	v_pk_fma_f32 v[0:1], v[40:41], v[0:1], 1.0 op_sel_hi:[1,1,0] neg_lo:[1,0,0] neg_hi:[1,0,0]
	s_nop 0
	v_cndmask_b32_e32 v1, v43, v1, vcc
	v_cmp_le_f32_e32 vcc, 0, v34
	s_nop 1
	v_cndmask_b32_e32 v0, v42, v0, vcc
	v_pk_mul_f32 v[0:1], v[34:35], v[0:1]
	v_mul_f32_e64 v34, |v36|, s1
	v_pk_mul_f32 v[0:1], v[204:205], v[0:1] op_sel_hi:[0,1]
	v_mul_f32_e64 v35, |v37|, s1
	v_cvt_pk_f16_f32 v40, v0, v1
	v_fma_f32 v0, v34, s3, 1.0
	v_fma_f32 v1, v35, s3, 1.0
	v_rcp_f32_e32 v0, v0
	v_rcp_f32_e32 v1, v1
	v_mul_f32_e64 v34, v34, -v34
	v_mul_f32_e64 v35, v35, -v35
	v_mul_f32_e32 v34, 0x3fb8aa3b, v34
	v_pk_fma_f32 v[42:43], v[0:1], s[0:1], v[44:45] op_sel_hi:[1,0,0]
	v_mul_f32_e32 v35, 0x3fb8aa3b, v35
	v_pk_fma_f32 v[42:43], v[42:43], v[0:1], s[2:3] op_sel_hi:[1,1,0]
	v_exp_f32_e32 v34, v34
	v_exp_f32_e32 v35, v35
	v_pk_fma_f32 v[42:43], v[42:43], v[0:1], s[4:5] op_sel_hi:[1,1,0]
	v_cmp_le_f32_e32 vcc, 0, v37
	v_pk_fma_f32 v[42:43], v[42:43], v[0:1], s[6:7] op_sel_hi:[1,1,0]
	v_permlane16_swap_b32_e32 v38, v40
	v_pk_mul_f32 v[0:1], v[0:1], v[42:43]
	s_nop 0
	v_pk_mul_f32 v[0:1], v[0:1], 0.5 op_sel_hi:[1,0]
	s_nop 0
	v_pk_mul_f32 v[42:43], v[34:35], v[0:1]
	v_pk_fma_f32 v[0:1], v[34:35], v[0:1], 1.0 op_sel_hi:[1,1,0] neg_lo:[1,0,0] neg_hi:[1,0,0]
	s_nop 0
	v_cndmask_b32_e32 v1, v43, v1, vcc
	v_cmp_le_f32_e32 vcc, 0, v36
	s_nop 1
	v_cndmask_b32_e32 v0, v42, v0, vcc
	v_pk_mul_f32 v[0:1], v[36:37], v[0:1]
	v_cmp_lt_i32_e32 vcc, -1, v202
	v_pk_mul_f32 v[0:1], v[204:205], v[0:1] op_sel_hi:[0,1]
	v_cvt_pk_f16_f32 v41, v0, v1
	s_nop 1
	s_nop 0
	v_permlane16_swap_b32_e32 v39, v41
	s_and_saveexec_b64 s[10:11], vcc
	s_cbranch_execz .LBB2_124
	v_mov_b32_e32 v203, 0
	v_lshlrev_b64 v[0:1], 10, v[202:203]
	v_lshl_add_u64 v[0:1], v[78:79], 0, v[0:1]
	global_store_dwordx4 v[0:1], v[38:41], off sc1
.LBB2_124:
	s_or_b64 exec, exec, s[10:11]
	v_mul_f32_e64 v1, |v30|, s1
	v_mul_f32_e64 v35, |v31|, s1
	v_fma_f32 v0, v1, s3, 1.0
	v_mul_f32_e64 v34, v1, -v1
	v_fma_f32 v1, v35, s3, 1.0
	v_rcp_f32_e32 v0, v0
	v_rcp_f32_e32 v1, v1
	v_mov_b64_e32 v[36:37], s[8:9]
	v_mul_f32_e64 v35, v35, -v35
	v_mul_f32_e32 v34, 0x3fb8aa3b, v34
	v_pk_fma_f32 v[38:39], v[0:1], s[0:1], v[36:37] op_sel_hi:[1,0,0]
	v_mul_f32_e32 v35, 0x3fb8aa3b, v35
	v_pk_fma_f32 v[38:39], v[38:39], v[0:1], s[2:3] op_sel_hi:[1,1,0]
	v_exp_f32_e32 v34, v34
	v_exp_f32_e32 v35, v35
	v_pk_fma_f32 v[38:39], v[38:39], v[0:1], s[4:5] op_sel_hi:[1,1,0]
	v_cmp_le_f32_e32 vcc, 0, v31
	v_pk_fma_f32 v[38:39], v[38:39], v[0:1], s[6:7] op_sel_hi:[1,1,0]
	s_nop 0
	v_pk_mul_f32 v[0:1], v[0:1], v[38:39]
	s_nop 0
	v_pk_mul_f32 v[0:1], v[0:1], 0.5 op_sel_hi:[1,0]
	s_nop 0
	v_pk_mul_f32 v[38:39], v[34:35], v[0:1]
	v_pk_fma_f32 v[0:1], v[34:35], v[0:1], 1.0 op_sel_hi:[1,1,0] neg_lo:[1,0,0] neg_hi:[1,0,0]
	v_mul_f32_e64 v35, |v33|, s1
	v_cndmask_b32_e32 v1, v39, v1, vcc
	v_cmp_le_f32_e32 vcc, 0, v30
	s_nop 1
	v_cndmask_b32_e32 v0, v38, v0, vcc
	v_pk_mul_f32 v[0:1], v[30:31], v[0:1]
	v_mul_f32_e64 v31, |v32|, s1
	v_pk_mul_f32 v[0:1], v[200:201], v[0:1] op_sel_hi:[0,1]
	v_cvt_pk_f16_f32 v30, v0, v1
	v_fma_f32 v0, v31, s3, 1.0
	v_fma_f32 v1, v35, s3, 1.0
	v_rcp_f32_e32 v0, v0
	v_rcp_f32_e32 v1, v1
	v_mul_f32_e64 v31, v31, -v31
	v_mul_f32_e32 v31, 0x3fb8aa3b, v31
	v_exp_f32_e32 v34, v31
	v_pk_fma_f32 v[38:39], v[0:1], s[0:1], v[36:37] op_sel_hi:[1,0,0]
	v_mul_f32_e64 v31, v35, -v35
	v_mul_f32_e32 v31, 0x3fb8aa3b, v31
	v_pk_fma_f32 v[38:39], v[38:39], v[0:1], s[2:3] op_sel_hi:[1,1,0]
	v_exp_f32_e32 v35, v31
	v_pk_fma_f32 v[38:39], v[38:39], v[0:1], s[4:5] op_sel_hi:[1,1,0]
	v_cmp_le_f32_e32 vcc, 0, v33
	v_pk_fma_f32 v[38:39], v[38:39], v[0:1], s[6:7] op_sel_hi:[1,1,0]
	s_nop 0
	v_pk_mul_f32 v[0:1], v[0:1], v[38:39]
	s_nop 0
	v_pk_mul_f32 v[0:1], v[0:1], 0.5 op_sel_hi:[1,0]
	s_nop 0
	v_pk_mul_f32 v[38:39], v[34:35], v[0:1]
	v_pk_fma_f32 v[0:1], v[34:35], v[0:1], 1.0 op_sel_hi:[1,1,0] neg_lo:[1,0,0] neg_hi:[1,0,0]
	s_nop 0
	v_cndmask_b32_e32 v1, v39, v1, vcc
	v_cmp_le_f32_e32 vcc, 0, v32
	s_nop 1
	v_cndmask_b32_e32 v0, v38, v0, vcc
	v_pk_mul_f32 v[0:1], v[32:33], v[0:1]
	v_mul_f32_e64 v32, |v26|, s1
	v_pk_mul_f32 v[0:1], v[200:201], v[0:1] op_sel_hi:[0,1]
	v_mul_f32_e64 v33, |v27|, s1
	v_cvt_pk_f16_f32 v31, v0, v1
	v_fma_f32 v0, v32, s3, 1.0
	v_fma_f32 v1, v33, s3, 1.0
	v_rcp_f32_e32 v0, v0
	v_rcp_f32_e32 v1, v1
	v_mul_f32_e64 v32, v32, -v32
	v_mul_f32_e64 v33, v33, -v33
	v_mul_f32_e32 v32, 0x3fb8aa3b, v32
	v_pk_fma_f32 v[34:35], v[0:1], s[0:1], v[36:37] op_sel_hi:[1,0,0]
	v_mul_f32_e32 v33, 0x3fb8aa3b, v33
	v_pk_fma_f32 v[34:35], v[34:35], v[0:1], s[2:3] op_sel_hi:[1,1,0]
	v_exp_f32_e32 v32, v32
	v_exp_f32_e32 v33, v33
	v_pk_fma_f32 v[34:35], v[34:35], v[0:1], s[4:5] op_sel_hi:[1,1,0]
	v_cmp_le_f32_e32 vcc, 0, v27
	v_pk_fma_f32 v[34:35], v[34:35], v[0:1], s[6:7] op_sel_hi:[1,1,0]
	s_nop 0
	v_pk_mul_f32 v[0:1], v[0:1], v[34:35]
	s_nop 0
	v_pk_mul_f32 v[0:1], v[0:1], 0.5 op_sel_hi:[1,0]
	s_nop 0
	v_pk_mul_f32 v[34:35], v[32:33], v[0:1]
	v_pk_fma_f32 v[0:1], v[32:33], v[0:1], 1.0 op_sel_hi:[1,1,0] neg_lo:[1,0,0] neg_hi:[1,0,0]
	s_nop 0
	v_cndmask_b32_e32 v1, v35, v1, vcc
	v_cmp_le_f32_e32 vcc, 0, v26
	s_nop 1
	v_cndmask_b32_e32 v0, v34, v0, vcc
	v_pk_mul_f32 v[0:1], v[26:27], v[0:1]
	v_mul_f32_e64 v26, |v28|, s1
	v_pk_mul_f32 v[0:1], v[200:201], v[0:1] op_sel_hi:[0,1]
	v_mul_f32_e64 v27, |v29|, s1
	v_cvt_pk_f16_f32 v32, v0, v1
	v_fma_f32 v0, v26, s3, 1.0
	v_fma_f32 v1, v27, s3, 1.0
	v_rcp_f32_e32 v0, v0
	v_rcp_f32_e32 v1, v1
	v_mul_f32_e64 v26, v26, -v26
	v_mul_f32_e64 v27, v27, -v27
	v_mul_f32_e32 v26, 0x3fb8aa3b, v26
	v_pk_fma_f32 v[34:35], v[0:1], s[0:1], v[36:37] op_sel_hi:[1,0,0]
	v_mul_f32_e32 v27, 0x3fb8aa3b, v27
	v_pk_fma_f32 v[34:35], v[34:35], v[0:1], s[2:3] op_sel_hi:[1,1,0]
	v_exp_f32_e32 v26, v26
	v_exp_f32_e32 v27, v27
	v_pk_fma_f32 v[34:35], v[34:35], v[0:1], s[4:5] op_sel_hi:[1,1,0]
	v_cmp_le_f32_e32 vcc, 0, v29
	v_pk_fma_f32 v[34:35], v[34:35], v[0:1], s[6:7] op_sel_hi:[1,1,0]
	v_permlane16_swap_b32_e32 v30, v32
	v_pk_mul_f32 v[0:1], v[0:1], v[34:35]
	s_nop 0
	v_pk_mul_f32 v[0:1], v[0:1], 0.5 op_sel_hi:[1,0]
	s_nop 0
	v_pk_mul_f32 v[34:35], v[26:27], v[0:1]
	v_pk_fma_f32 v[0:1], v[26:27], v[0:1], 1.0 op_sel_hi:[1,1,0] neg_lo:[1,0,0] neg_hi:[1,0,0]
	s_nop 0
	v_cndmask_b32_e32 v1, v35, v1, vcc
	v_cmp_le_f32_e32 vcc, 0, v28
	s_nop 1
	v_cndmask_b32_e32 v0, v34, v0, vcc
	v_pk_mul_f32 v[0:1], v[28:29], v[0:1]
	v_cmp_lt_i32_e32 vcc, -1, v198
	v_pk_mul_f32 v[0:1], v[200:201], v[0:1] op_sel_hi:[0,1]
	v_cvt_pk_f16_f32 v33, v0, v1
	s_nop 1
	s_nop 0
	v_permlane16_swap_b32_e32 v31, v33
	s_and_saveexec_b64 s[0:1], vcc
	s_cbranch_execz .LBB2_126
	v_mov_b32_e32 v199, 0
	v_lshlrev_b64 v[0:1], 10, v[198:199]
	v_lshl_add_u64 v[0:1], v[78:79], 0, v[0:1]
	global_store_dwordx4 v[0:1], v[30:33], off sc1
.LBB2_126:
	s_or_b64 exec, exec, s[0:1]
	s_mov_b32 s1, 0x3f3504f3
	v_mul_f32_e64 v1, |v22|, s1
	v_fma_f32 v0, v1, s3, 1.0
	v_mul_f32_e64 v1, v1, -v1
	v_mul_f32_e32 v1, 0x3fb8aa3b, v1
	v_mul_f32_e64 v27, |v23|, s1
	v_exp_f32_e32 v26, v1
	v_fma_f32 v1, v27, s3, 1.0
	v_rcp_f32_e32 v0, v0
	v_rcp_f32_e32 v1, v1
	s_mov_b32 s0, 0x3f87dc22
	v_mov_b64_e32 v[28:29], s[8:9]
	v_mul_f32_e64 v27, v27, -v27
	v_pk_fma_f32 v[30:31], v[0:1], s[0:1], v[28:29] op_sel_hi:[1,0,0]
	v_mul_f32_e32 v27, 0x3fb8aa3b, v27
	v_pk_fma_f32 v[30:31], v[30:31], v[0:1], s[2:3] op_sel_hi:[1,1,0]
	v_exp_f32_e32 v27, v27
	v_pk_fma_f32 v[30:31], v[30:31], v[0:1], s[4:5] op_sel_hi:[1,1,0]
	v_cmp_le_f32_e32 vcc, 0, v23
	v_pk_fma_f32 v[30:31], v[30:31], v[0:1], s[6:7] op_sel_hi:[1,1,0]
	s_nop 0
	v_pk_mul_f32 v[0:1], v[0:1], v[30:31]
	s_nop 0
	v_pk_mul_f32 v[0:1], v[0:1], 0.5 op_sel_hi:[1,0]
	s_nop 0
	v_pk_mul_f32 v[30:31], v[26:27], v[0:1]
	v_pk_fma_f32 v[0:1], v[26:27], v[0:1], 1.0 op_sel_hi:[1,1,0] neg_lo:[1,0,0] neg_hi:[1,0,0]
	v_mul_f32_e64 v27, |v25|, s1
	v_cndmask_b32_e32 v1, v31, v1, vcc
	v_cmp_le_f32_e32 vcc, 0, v22
	s_nop 1
	v_cndmask_b32_e32 v0, v30, v0, vcc
	v_pk_mul_f32 v[0:1], v[22:23], v[0:1]
	v_mul_f32_e64 v23, |v24|, s1
	v_pk_mul_f32 v[0:1], v[196:197], v[0:1] op_sel_hi:[0,1]
	v_cvt_pk_f16_f32 v22, v0, v1
	v_fma_f32 v0, v23, s3, 1.0
	v_fma_f32 v1, v27, s3, 1.0
	v_rcp_f32_e32 v0, v0
	v_rcp_f32_e32 v1, v1
	v_mul_f32_e64 v23, v23, -v23
	v_mul_f32_e32 v23, 0x3fb8aa3b, v23
	v_exp_f32_e32 v26, v23
	v_pk_fma_f32 v[30:31], v[0:1], s[0:1], v[28:29] op_sel_hi:[1,0,0]
	v_mul_f32_e64 v23, v27, -v27
	v_mul_f32_e32 v23, 0x3fb8aa3b, v23
	v_pk_fma_f32 v[30:31], v[30:31], v[0:1], s[2:3] op_sel_hi:[1,1,0]
	v_exp_f32_e32 v27, v23
	v_pk_fma_f32 v[30:31], v[30:31], v[0:1], s[4:5] op_sel_hi:[1,1,0]
	v_cmp_le_f32_e32 vcc, 0, v25
	v_pk_fma_f32 v[30:31], v[30:31], v[0:1], s[6:7] op_sel_hi:[1,1,0]
	s_nop 0
	v_pk_mul_f32 v[0:1], v[0:1], v[30:31]
	s_nop 0
	v_pk_mul_f32 v[0:1], v[0:1], 0.5 op_sel_hi:[1,0]
	s_nop 0
	v_pk_mul_f32 v[30:31], v[26:27], v[0:1]
	v_pk_fma_f32 v[0:1], v[26:27], v[0:1], 1.0 op_sel_hi:[1,1,0] neg_lo:[1,0,0] neg_hi:[1,0,0]
	s_nop 0
	v_cndmask_b32_e32 v1, v31, v1, vcc
	v_cmp_le_f32_e32 vcc, 0, v24
	s_nop 1
	v_cndmask_b32_e32 v0, v30, v0, vcc
	v_pk_mul_f32 v[0:1], v[24:25], v[0:1]
	v_mul_f32_e64 v24, |v18|, s1
	v_pk_mul_f32 v[0:1], v[196:197], v[0:1] op_sel_hi:[0,1]
	v_mul_f32_e64 v25, |v19|, s1
	v_cvt_pk_f16_f32 v23, v0, v1
	v_fma_f32 v0, v24, s3, 1.0
	v_fma_f32 v1, v25, s3, 1.0
	v_rcp_f32_e32 v0, v0
	v_rcp_f32_e32 v1, v1
	v_mul_f32_e64 v24, v24, -v24
	v_mul_f32_e64 v25, v25, -v25
	v_mul_f32_e32 v24, 0x3fb8aa3b, v24
	v_pk_fma_f32 v[26:27], v[0:1], s[0:1], v[28:29] op_sel_hi:[1,0,0]
	v_mul_f32_e32 v25, 0x3fb8aa3b, v25
	v_pk_fma_f32 v[26:27], v[26:27], v[0:1], s[2:3] op_sel_hi:[1,1,0]
	v_exp_f32_e32 v24, v24
	v_exp_f32_e32 v25, v25
	v_pk_fma_f32 v[26:27], v[26:27], v[0:1], s[4:5] op_sel_hi:[1,1,0]
	v_cmp_le_f32_e32 vcc, 0, v19
	v_pk_fma_f32 v[26:27], v[26:27], v[0:1], s[6:7] op_sel_hi:[1,1,0]
	s_nop 0
	v_pk_mul_f32 v[0:1], v[0:1], v[26:27]
	s_nop 0
	v_pk_mul_f32 v[0:1], v[0:1], 0.5 op_sel_hi:[1,0]
	s_nop 0
	v_pk_mul_f32 v[26:27], v[24:25], v[0:1]
	v_pk_fma_f32 v[0:1], v[24:25], v[0:1], 1.0 op_sel_hi:[1,1,0] neg_lo:[1,0,0] neg_hi:[1,0,0]
	s_nop 0
	v_cndmask_b32_e32 v1, v27, v1, vcc
	v_cmp_le_f32_e32 vcc, 0, v18
	s_nop 1
	v_cndmask_b32_e32 v0, v26, v0, vcc
	v_pk_mul_f32 v[0:1], v[18:19], v[0:1]
	v_mul_f32_e64 v18, |v20|, s1
	v_pk_mul_f32 v[0:1], v[196:197], v[0:1] op_sel_hi:[0,1]
	v_mul_f32_e64 v19, |v21|, s1
	v_cvt_pk_f16_f32 v24, v0, v1
	v_fma_f32 v0, v18, s3, 1.0
	v_fma_f32 v1, v19, s3, 1.0
	v_rcp_f32_e32 v0, v0
	v_rcp_f32_e32 v1, v1
	v_mul_f32_e64 v18, v18, -v18
	v_mul_f32_e64 v19, v19, -v19
	v_mul_f32_e32 v18, 0x3fb8aa3b, v18
	v_pk_fma_f32 v[26:27], v[0:1], s[0:1], v[28:29] op_sel_hi:[1,0,0]
	v_mul_f32_e32 v19, 0x3fb8aa3b, v19
	v_pk_fma_f32 v[26:27], v[26:27], v[0:1], s[2:3] op_sel_hi:[1,1,0]
	v_exp_f32_e32 v18, v18
	v_exp_f32_e32 v19, v19
	v_pk_fma_f32 v[26:27], v[26:27], v[0:1], s[4:5] op_sel_hi:[1,1,0]
	v_cmp_le_f32_e32 vcc, 0, v21
	v_pk_fma_f32 v[26:27], v[26:27], v[0:1], s[6:7] op_sel_hi:[1,1,0]
	v_permlane16_swap_b32_e32 v22, v24
	v_pk_mul_f32 v[0:1], v[0:1], v[26:27]
	s_nop 0
	v_pk_mul_f32 v[0:1], v[0:1], 0.5 op_sel_hi:[1,0]
	s_nop 0
	v_pk_mul_f32 v[26:27], v[18:19], v[0:1]
	v_pk_fma_f32 v[0:1], v[18:19], v[0:1], 1.0 op_sel_hi:[1,1,0] neg_lo:[1,0,0] neg_hi:[1,0,0]
	s_nop 0
	v_cndmask_b32_e32 v1, v27, v1, vcc
	v_cmp_le_f32_e32 vcc, 0, v20
	s_nop 1
	v_cndmask_b32_e32 v0, v26, v0, vcc
	v_pk_mul_f32 v[0:1], v[20:21], v[0:1]
	v_cmp_lt_i32_e32 vcc, -1, v194
	v_pk_mul_f32 v[0:1], v[196:197], v[0:1] op_sel_hi:[0,1]
	v_cvt_pk_f16_f32 v25, v0, v1
	s_nop 1
	s_nop 0
	v_permlane16_swap_b32_e32 v23, v25
	s_and_saveexec_b64 s[10:11], vcc
	s_cbranch_execz .LBB2_128
	v_mov_b32_e32 v195, 0
	v_lshlrev_b64 v[0:1], 10, v[194:195]
	v_lshl_add_u64 v[0:1], v[78:79], 0, v[0:1]
	global_store_dwordx4 v[0:1], v[22:25], off sc1
.LBB2_128:
	s_or_b64 exec, exec, s[10:11]
	v_mul_f32_e64 v1, |v14|, s1
	v_mul_f32_e64 v19, |v15|, s1
	v_fma_f32 v0, v1, s3, 1.0
	v_mul_f32_e64 v18, v1, -v1
	v_fma_f32 v1, v19, s3, 1.0
	v_rcp_f32_e32 v0, v0
	v_rcp_f32_e32 v1, v1
	v_mov_b64_e32 v[20:21], s[8:9]
	v_mul_f32_e64 v19, v19, -v19
	v_mul_f32_e32 v18, 0x3fb8aa3b, v18
	v_pk_fma_f32 v[22:23], v[0:1], s[0:1], v[20:21] op_sel_hi:[1,0,0]
	v_mul_f32_e32 v19, 0x3fb8aa3b, v19
	v_pk_fma_f32 v[22:23], v[22:23], v[0:1], s[2:3] op_sel_hi:[1,1,0]
	v_exp_f32_e32 v18, v18
	v_exp_f32_e32 v19, v19
	v_pk_fma_f32 v[22:23], v[22:23], v[0:1], s[4:5] op_sel_hi:[1,1,0]
	v_cmp_le_f32_e32 vcc, 0, v15
	v_pk_fma_f32 v[22:23], v[22:23], v[0:1], s[6:7] op_sel_hi:[1,1,0]
	s_nop 0
	v_pk_mul_f32 v[0:1], v[0:1], v[22:23]
	s_nop 0
	v_pk_mul_f32 v[0:1], v[0:1], 0.5 op_sel_hi:[1,0]
	s_nop 0
	v_pk_mul_f32 v[22:23], v[18:19], v[0:1]
	v_pk_fma_f32 v[0:1], v[18:19], v[0:1], 1.0 op_sel_hi:[1,1,0] neg_lo:[1,0,0] neg_hi:[1,0,0]
	v_mul_f32_e64 v19, |v17|, s1
	v_cndmask_b32_e32 v1, v23, v1, vcc
	v_cmp_le_f32_e32 vcc, 0, v14
	s_nop 1
	v_cndmask_b32_e32 v0, v22, v0, vcc
	v_pk_mul_f32 v[0:1], v[14:15], v[0:1]
	v_mul_f32_e64 v15, |v16|, s1
	v_pk_mul_f32 v[0:1], v[192:193], v[0:1] op_sel_hi:[0,1]
	v_cvt_pk_f16_f32 v14, v0, v1
	v_fma_f32 v0, v15, s3, 1.0
	v_fma_f32 v1, v19, s3, 1.0
	v_rcp_f32_e32 v0, v0
	v_rcp_f32_e32 v1, v1
	v_mul_f32_e64 v15, v15, -v15
	v_mul_f32_e32 v15, 0x3fb8aa3b, v15
	v_exp_f32_e32 v18, v15
	v_pk_fma_f32 v[22:23], v[0:1], s[0:1], v[20:21] op_sel_hi:[1,0,0]
	v_mul_f32_e64 v15, v19, -v19
	v_mul_f32_e32 v15, 0x3fb8aa3b, v15
	v_pk_fma_f32 v[22:23], v[22:23], v[0:1], s[2:3] op_sel_hi:[1,1,0]
	v_exp_f32_e32 v19, v15
	v_pk_fma_f32 v[22:23], v[22:23], v[0:1], s[4:5] op_sel_hi:[1,1,0]
	v_cmp_le_f32_e32 vcc, 0, v17
	v_pk_fma_f32 v[22:23], v[22:23], v[0:1], s[6:7] op_sel_hi:[1,1,0]
	s_nop 0
	v_pk_mul_f32 v[0:1], v[0:1], v[22:23]
	s_nop 0
	v_pk_mul_f32 v[0:1], v[0:1], 0.5 op_sel_hi:[1,0]
	s_nop 0
	v_pk_mul_f32 v[22:23], v[18:19], v[0:1]
	v_pk_fma_f32 v[0:1], v[18:19], v[0:1], 1.0 op_sel_hi:[1,1,0] neg_lo:[1,0,0] neg_hi:[1,0,0]
	s_nop 0
	v_cndmask_b32_e32 v1, v23, v1, vcc
	v_cmp_le_f32_e32 vcc, 0, v16
	s_nop 1
	v_cndmask_b32_e32 v0, v22, v0, vcc
	v_pk_mul_f32 v[0:1], v[16:17], v[0:1]
	v_mul_f32_e64 v16, |v10|, s1
	v_pk_mul_f32 v[0:1], v[192:193], v[0:1] op_sel_hi:[0,1]
	v_mul_f32_e64 v17, |v11|, s1
	v_cvt_pk_f16_f32 v15, v0, v1
	v_fma_f32 v0, v16, s3, 1.0
	v_fma_f32 v1, v17, s3, 1.0
	v_rcp_f32_e32 v0, v0
	v_rcp_f32_e32 v1, v1
	v_mul_f32_e64 v16, v16, -v16
	v_mul_f32_e64 v17, v17, -v17
	v_mul_f32_e32 v16, 0x3fb8aa3b, v16
	v_pk_fma_f32 v[18:19], v[0:1], s[0:1], v[20:21] op_sel_hi:[1,0,0]
	v_mul_f32_e32 v17, 0x3fb8aa3b, v17
	v_pk_fma_f32 v[18:19], v[18:19], v[0:1], s[2:3] op_sel_hi:[1,1,0]
	v_exp_f32_e32 v16, v16
	v_exp_f32_e32 v17, v17
	v_pk_fma_f32 v[18:19], v[18:19], v[0:1], s[4:5] op_sel_hi:[1,1,0]
	v_cmp_le_f32_e32 vcc, 0, v11
	v_pk_fma_f32 v[18:19], v[18:19], v[0:1], s[6:7] op_sel_hi:[1,1,0]
	s_nop 0
	v_pk_mul_f32 v[0:1], v[0:1], v[18:19]
	s_nop 0
	v_pk_mul_f32 v[0:1], v[0:1], 0.5 op_sel_hi:[1,0]
	s_nop 0
	v_pk_mul_f32 v[18:19], v[16:17], v[0:1]
	v_pk_fma_f32 v[0:1], v[16:17], v[0:1], 1.0 op_sel_hi:[1,1,0] neg_lo:[1,0,0] neg_hi:[1,0,0]
	s_nop 0
	v_cndmask_b32_e32 v1, v19, v1, vcc
	v_cmp_le_f32_e32 vcc, 0, v10
	s_nop 1
	v_cndmask_b32_e32 v0, v18, v0, vcc
	v_pk_mul_f32 v[0:1], v[10:11], v[0:1]
	v_mul_f32_e64 v10, |v12|, s1
	v_pk_mul_f32 v[0:1], v[192:193], v[0:1] op_sel_hi:[0,1]
	v_mul_f32_e64 v11, |v13|, s1
	v_cvt_pk_f16_f32 v16, v0, v1
	v_fma_f32 v0, v10, s3, 1.0
	v_fma_f32 v1, v11, s3, 1.0
	v_rcp_f32_e32 v0, v0
	v_rcp_f32_e32 v1, v1
	v_mul_f32_e64 v10, v10, -v10
	v_mul_f32_e64 v11, v11, -v11
	v_mul_f32_e32 v10, 0x3fb8aa3b, v10
	v_pk_fma_f32 v[18:19], v[0:1], s[0:1], v[20:21] op_sel_hi:[1,0,0]
	v_mul_f32_e32 v11, 0x3fb8aa3b, v11
	v_pk_fma_f32 v[18:19], v[18:19], v[0:1], s[2:3] op_sel_hi:[1,1,0]
	v_exp_f32_e32 v10, v10
	v_exp_f32_e32 v11, v11
	v_pk_fma_f32 v[18:19], v[18:19], v[0:1], s[4:5] op_sel_hi:[1,1,0]
	v_cmp_le_f32_e32 vcc, 0, v13
	v_pk_fma_f32 v[18:19], v[18:19], v[0:1], s[6:7] op_sel_hi:[1,1,0]
	v_permlane16_swap_b32_e32 v14, v16
	v_pk_mul_f32 v[0:1], v[0:1], v[18:19]
	s_nop 0
	v_pk_mul_f32 v[0:1], v[0:1], 0.5 op_sel_hi:[1,0]
	s_nop 0
	v_pk_mul_f32 v[18:19], v[10:11], v[0:1]
	v_pk_fma_f32 v[0:1], v[10:11], v[0:1], 1.0 op_sel_hi:[1,1,0] neg_lo:[1,0,0] neg_hi:[1,0,0]
	s_nop 0
	v_cndmask_b32_e32 v1, v19, v1, vcc
	v_cmp_le_f32_e32 vcc, 0, v12
	s_nop 1
	v_cndmask_b32_e32 v0, v18, v0, vcc
	v_pk_mul_f32 v[0:1], v[12:13], v[0:1]
	v_cmp_lt_i32_e32 vcc, -1, v190
	v_pk_mul_f32 v[0:1], v[192:193], v[0:1] op_sel_hi:[0,1]
	v_cvt_pk_f16_f32 v17, v0, v1
	s_nop 1
	s_nop 0
	v_permlane16_swap_b32_e32 v15, v17
	s_and_saveexec_b64 s[0:1], vcc
	s_cbranch_execz .LBB2_130
	v_mov_b32_e32 v191, 0
	v_lshlrev_b64 v[0:1], 10, v[190:191]
	v_lshl_add_u64 v[0:1], v[78:79], 0, v[0:1]
	global_store_dwordx4 v[0:1], v[14:17], off sc1
.LBB2_130:
	s_or_b64 exec, exec, s[0:1]
	s_mov_b32 s1, 0x3f3504f3
	v_mul_f32_e64 v1, |v6|, s1
	v_fma_f32 v0, v1, s3, 1.0
	v_mul_f32_e64 v1, v1, -v1
	v_mul_f32_e32 v1, 0x3fb8aa3b, v1
	v_mul_f32_e64 v11, |v7|, s1
	v_exp_f32_e32 v10, v1
	v_fma_f32 v1, v11, s3, 1.0
	v_rcp_f32_e32 v0, v0
	v_rcp_f32_e32 v1, v1
	s_mov_b32 s2, 0xbfba00e3
	s_mov_b32 s0, 0x3f87dc22
	v_mov_b64_e32 v[12:13], s[2:3]
	v_pk_fma_f32 v[14:15], v[0:1], s[0:1], v[12:13] op_sel_hi:[1,0,0]
	v_mul_f32_e64 v11, v11, -v11
	s_mov_b32 s2, 0x3fb5f0e3
	v_mul_f32_e32 v11, 0x3fb8aa3b, v11
	v_pk_fma_f32 v[14:15], v[14:15], v[0:1], s[2:3] op_sel_hi:[1,1,0]
	v_exp_f32_e32 v11, v11
	v_pk_fma_f32 v[14:15], v[14:15], v[0:1], s[4:5] op_sel_hi:[1,1,0]
	v_cmp_le_f32_e32 vcc, 0, v7
	v_pk_fma_f32 v[14:15], v[14:15], v[0:1], s[6:7] op_sel_hi:[1,1,0]
	s_nop 0
	v_pk_mul_f32 v[0:1], v[0:1], v[14:15]
	s_nop 0
	v_pk_mul_f32 v[0:1], v[0:1], 0.5 op_sel_hi:[1,0]
	s_nop 0
	v_pk_mul_f32 v[14:15], v[10:11], v[0:1]
	v_pk_fma_f32 v[0:1], v[10:11], v[0:1], 1.0 op_sel_hi:[1,1,0] neg_lo:[1,0,0] neg_hi:[1,0,0]
	v_mul_f32_e64 v11, |v9|, s1
	v_cndmask_b32_e32 v1, v15, v1, vcc
	v_cmp_le_f32_e32 vcc, 0, v6
	s_nop 1
	v_cndmask_b32_e32 v0, v14, v0, vcc
	v_pk_mul_f32 v[0:1], v[6:7], v[0:1]
	v_fma_f32 v7, v11, s3, 1.0
	v_pk_mul_f32 v[0:1], v[188:189], v[0:1] op_sel_hi:[0,1]
	v_cvt_pk_f16_f32 v0, v0, v1
	v_mul_f32_e64 v1, |v8|, s1
	v_fma_f32 v6, v1, s3, 1.0
	v_rcp_f32_e32 v6, v6
	v_rcp_f32_e32 v7, v7
	v_mul_f32_e64 v1, v1, -v1
	v_mul_f32_e32 v1, 0x3fb8aa3b, v1
	v_exp_f32_e32 v10, v1
	v_pk_fma_f32 v[14:15], v[6:7], s[0:1], v[12:13] op_sel_hi:[1,0,0]
	v_mul_f32_e64 v1, v11, -v11
	v_mul_f32_e32 v1, 0x3fb8aa3b, v1
	v_pk_fma_f32 v[14:15], v[14:15], v[6:7], s[2:3] op_sel_hi:[1,1,0]
	v_exp_f32_e32 v11, v1
	v_pk_fma_f32 v[14:15], v[14:15], v[6:7], s[4:5] op_sel_hi:[1,1,0]
	v_cmp_le_f32_e32 vcc, 0, v9
	v_pk_fma_f32 v[14:15], v[14:15], v[6:7], s[6:7] op_sel_hi:[1,1,0]
	s_nop 0
	v_pk_mul_f32 v[6:7], v[6:7], v[14:15]
	s_nop 0
	v_pk_mul_f32 v[6:7], v[6:7], 0.5 op_sel_hi:[1,0]
	s_nop 0
	v_pk_mul_f32 v[14:15], v[10:11], v[6:7]
	v_pk_fma_f32 v[6:7], v[10:11], v[6:7], 1.0 op_sel_hi:[1,1,0] neg_lo:[1,0,0] neg_hi:[1,0,0]
	s_nop 0
	v_cndmask_b32_e32 v7, v15, v7, vcc
	v_cmp_le_f32_e32 vcc, 0, v8
	s_nop 1
	v_cndmask_b32_e32 v6, v14, v6, vcc
	v_pk_mul_f32 v[6:7], v[8:9], v[6:7]
	v_mul_f32_e64 v8, |v2|, s1
	v_pk_mul_f32 v[6:7], v[188:189], v[6:7] op_sel_hi:[0,1]
	v_mul_f32_e64 v9, |v3|, s1
	v_cvt_pk_f16_f32 v1, v6, v7
	v_fma_f32 v6, v8, s3, 1.0
	v_fma_f32 v7, v9, s3, 1.0
	v_rcp_f32_e32 v6, v6
	v_rcp_f32_e32 v7, v7
	v_mul_f32_e64 v8, v8, -v8
	v_mul_f32_e64 v9, v9, -v9
	v_mul_f32_e32 v8, 0x3fb8aa3b, v8
	v_pk_fma_f32 v[10:11], v[6:7], s[0:1], v[12:13] op_sel_hi:[1,0,0]
	v_mul_f32_e32 v9, 0x3fb8aa3b, v9
	v_pk_fma_f32 v[10:11], v[10:11], v[6:7], s[2:3] op_sel_hi:[1,1,0]
	v_exp_f32_e32 v8, v8
	v_exp_f32_e32 v9, v9
	v_pk_fma_f32 v[10:11], v[10:11], v[6:7], s[4:5] op_sel_hi:[1,1,0]
	v_cmp_le_f32_e32 vcc, 0, v3
	v_pk_fma_f32 v[10:11], v[10:11], v[6:7], s[6:7] op_sel_hi:[1,1,0]
	s_nop 0
	v_pk_mul_f32 v[6:7], v[6:7], v[10:11]
	s_nop 0
	v_pk_mul_f32 v[6:7], v[6:7], 0.5 op_sel_hi:[1,0]
	s_nop 0
	v_pk_mul_f32 v[10:11], v[8:9], v[6:7]
	v_pk_fma_f32 v[6:7], v[8:9], v[6:7], 1.0 op_sel_hi:[1,1,0] neg_lo:[1,0,0] neg_hi:[1,0,0]
	v_mul_f32_e64 v9, |v5|, s1
	v_cndmask_b32_e32 v7, v11, v7, vcc
	v_cmp_le_f32_e32 vcc, 0, v2
	s_nop 1
	v_cndmask_b32_e32 v6, v10, v6, vcc
	v_pk_mul_f32 v[2:3], v[2:3], v[6:7]
	v_fma_f32 v7, v9, s3, 1.0
	v_pk_mul_f32 v[2:3], v[188:189], v[2:3] op_sel_hi:[0,1]
	v_cvt_pk_f16_f32 v2, v2, v3
	v_mul_f32_e64 v3, |v4|, s1
	v_fma_f32 v6, v3, s3, 1.0
	v_rcp_f32_e32 v6, v6
	v_rcp_f32_e32 v7, v7
	v_mul_f32_e64 v3, v3, -v3
	v_mul_f32_e32 v3, 0x3fb8aa3b, v3
	v_exp_f32_e32 v8, v3
	v_pk_fma_f32 v[10:11], v[6:7], s[0:1], v[12:13] op_sel_hi:[1,0,0]
	v_mul_f32_e64 v3, v9, -v9
	v_mul_f32_e32 v3, 0x3fb8aa3b, v3
	v_pk_fma_f32 v[10:11], v[10:11], v[6:7], s[2:3] op_sel_hi:[1,1,0]
	v_exp_f32_e32 v9, v3
	v_pk_fma_f32 v[10:11], v[10:11], v[6:7], s[4:5] op_sel_hi:[1,1,0]
	v_cmp_le_f32_e32 vcc, 0, v5
	v_pk_fma_f32 v[10:11], v[10:11], v[6:7], s[6:7] op_sel_hi:[1,1,0]
	v_permlane16_swap_b32_e32 v0, v2
	v_pk_mul_f32 v[6:7], v[6:7], v[10:11]
	s_nop 0
	v_pk_mul_f32 v[6:7], v[6:7], 0.5 op_sel_hi:[1,0]
	s_nop 0
	v_pk_mul_f32 v[10:11], v[8:9], v[6:7]
	v_pk_fma_f32 v[6:7], v[8:9], v[6:7], 1.0 op_sel_hi:[1,1,0] neg_lo:[1,0,0] neg_hi:[1,0,0]
	s_nop 0
	v_cndmask_b32_e32 v7, v11, v7, vcc
	v_cmp_le_f32_e32 vcc, 0, v4
	s_nop 1
	v_cndmask_b32_e32 v6, v10, v6, vcc
	v_pk_mul_f32 v[4:5], v[4:5], v[6:7]
	v_cmp_lt_i32_e32 vcc, -1, v186
	v_pk_mul_f32 v[4:5], v[188:189], v[4:5] op_sel_hi:[0,1]
	v_cvt_pk_f16_f32 v3, v4, v5
	s_nop 1
	s_nop 0
	v_permlane16_swap_b32_e32 v1, v3
	s_and_saveexec_b64 s[0:1], vcc
	s_cbranch_execz .LBB2_132
	v_mov_b32_e32 v187, 0
	v_lshlrev_b64 v[4:5], 10, v[186:187]
	v_lshl_add_u64 v[4:5], v[78:79], 0, v[4:5]
	global_store_dwordx4 v[4:5], v[0:3], off sc1

.LBB3_155:
	s_setprio 0
	v_and_b32_e32 v0, 16, v0
	v_lshlrev_b32_e32 v82, 2, v135
	s_lshl_b32 s2, s15, 5
	v_add_u32_e32 v83, 12, v82
	v_cmp_eq_u32_e32 vcc, 0, v0
	s_add_i32 s2, s2, s14
	v_cvt_pk_f16_f32 v81, v80, v81
	v_cndmask_b32_e32 v0, v83, v82, vcc
	v_or_b32_e32 v82, s2, v0
	v_ashrrev_i32_e32 v83, 31, v82
	v_lshl_add_u64 v[84:85], v[82:83], 1, s[0:1]
	v_cvt_pk_f16_f32 v80, v78, v79
	v_cvt_pk_f16_f32 v83, v76, v77
	v_cvt_pk_f16_f32 v82, v74, v75
	s_nop 1
	s_nop 0
	v_permlane16_swap_b32_e32 v80, v82
	v_permlane16_swap_b32_e32 v81, v83
	s_waitcnt vmcnt(0)
	v_cmp_lt_i32_e32 vcc, -1, v134
	s_and_saveexec_b64 s[0:1], vcc
	s_cbranch_execz .LBB3_157
	v_lshlrev_b32_e32 v0, 11, v134
	v_and_b32_e32 v74, 0xfff800, v0
	v_mov_b32_e32 v75, 0
	v_lshl_add_u64 v[74:75], v[84:85], 0, v[74:75]
	global_store_dwordx4 v[74:75], v[80:83], off sc1
.LBB3_157:
	s_or_b64 exec, exec, s[0:1]
	v_cvt_pk_f16_f32 v73, v72, v73
	v_cvt_pk_f16_f32 v72, v70, v71
	v_cvt_pk_f16_f32 v75, v68, v69
	v_cvt_pk_f16_f32 v74, v66, v67
	s_nop 1
	s_nop 0
	v_permlane16_swap_b32_e32 v72, v74
	v_permlane16_swap_b32_e32 v73, v75
	v_cmp_lt_i32_e32 vcc, -1, v131
	s_and_saveexec_b64 s[0:1], vcc
	s_cbranch_execz .LBB3_159
	v_lshlrev_b32_e32 v0, 11, v131
	v_and_b32_e32 v66, 0xfff800, v0
	v_mov_b32_e32 v67, 0
	v_lshl_add_u64 v[66:67], v[84:85], 0, v[66:67]
	global_store_dwordx4 v[66:67], v[72:75], off sc1
.LBB3_159:
	s_or_b64 exec, exec, s[0:1]
	v_cvt_pk_f16_f32 v65, v64, v65
	v_cvt_pk_f16_f32 v64, v62, v63
	v_cvt_pk_f16_f32 v67, v60, v61
	v_cvt_pk_f16_f32 v66, v58, v59
	s_nop 1
	s_nop 0
	v_permlane16_swap_b32_e32 v64, v66
	v_permlane16_swap_b32_e32 v65, v67
	v_cmp_lt_i32_e32 vcc, -1, v133
	s_and_saveexec_b64 s[0:1], vcc
	s_cbranch_execz .LBB3_161
	v_lshlrev_b32_e32 v0, 11, v133
	v_and_b32_e32 v58, 0xfff800, v0
	v_mov_b32_e32 v59, 0
	v_lshl_add_u64 v[58:59], v[84:85], 0, v[58:59]
	global_store_dwordx4 v[58:59], v[64:67], off sc1
.LBB3_161:
	s_or_b64 exec, exec, s[0:1]
	v_cvt_pk_f16_f32 v57, v56, v57
	v_cvt_pk_f16_f32 v56, v54, v55
	v_cvt_pk_f16_f32 v59, v52, v53
	v_cvt_pk_f16_f32 v58, v50, v51
	s_nop 1
	s_nop 0
	v_permlane16_swap_b32_e32 v56, v58
	v_permlane16_swap_b32_e32 v57, v59
	v_cmp_lt_i32_e32 vcc, -1, v129
	s_and_saveexec_b64 s[0:1], vcc
	s_cbranch_execz .LBB3_163
	v_lshlrev_b32_e32 v0, 11, v129
	v_and_b32_e32 v50, 0xfff800, v0
	v_mov_b32_e32 v51, 0
	v_lshl_add_u64 v[50:51], v[84:85], 0, v[50:51]
	global_store_dwordx4 v[50:51], v[56:59], off sc1
.LBB3_163:
	s_or_b64 exec, exec, s[0:1]
	v_cvt_pk_f16_f32 v49, v48, v49
	v_cvt_pk_f16_f32 v48, v46, v47
	v_cvt_pk_f16_f32 v51, v44, v45
	v_cvt_pk_f16_f32 v50, v42, v43
	s_nop 1
	s_nop 0
	v_permlane16_swap_b32_e32 v48, v50
	v_permlane16_swap_b32_e32 v49, v51
	v_cmp_lt_i32_e32 vcc, -1, v132
	s_and_saveexec_b64 s[0:1], vcc
	s_cbranch_execz .LBB3_165
	v_lshlrev_b32_e32 v0, 11, v132
	v_and_b32_e32 v42, 0xfff800, v0
	v_mov_b32_e32 v43, 0
	v_lshl_add_u64 v[42:43], v[84:85], 0, v[42:43]
	global_store_dwordx4 v[42:43], v[48:51], off sc1
.LBB3_165:
	s_or_b64 exec, exec, s[0:1]
	v_cvt_pk_f16_f32 v41, v40, v41
	v_cvt_pk_f16_f32 v40, v38, v39
	v_cvt_pk_f16_f32 v43, v36, v37
	v_cvt_pk_f16_f32 v42, v34, v35
	s_nop 1
	s_nop 0
	v_permlane16_swap_b32_e32 v40, v42
	v_permlane16_swap_b32_e32 v41, v43
	v_cmp_lt_i32_e32 vcc, -1, v127
	s_and_saveexec_b64 s[0:1], vcc
	s_cbranch_execz .LBB3_167
	v_lshlrev_b32_e32 v0, 11, v127
	v_and_b32_e32 v34, 0xfff800, v0
	v_mov_b32_e32 v35, 0
	v_lshl_add_u64 v[34:35], v[84:85], 0, v[34:35]
	global_store_dwordx4 v[34:35], v[40:43], off sc1
.LBB3_167:
	s_or_b64 exec, exec, s[0:1]
	v_cvt_pk_f16_f32 v33, v32, v33
	v_cvt_pk_f16_f32 v32, v30, v31
	v_cvt_pk_f16_f32 v35, v28, v29
	v_cvt_pk_f16_f32 v34, v26, v27
	s_nop 1
	s_nop 0
	v_permlane16_swap_b32_e32 v32, v34
	v_permlane16_swap_b32_e32 v33, v35
	v_cmp_lt_i32_e32 vcc, -1, v130
	s_and_saveexec_b64 s[0:1], vcc
	s_cbranch_execz .LBB3_169
	v_lshlrev_b32_e32 v0, 11, v130
	v_and_b32_e32 v26, 0xfff800, v0
	v_mov_b32_e32 v27, 0
	v_lshl_add_u64 v[26:27], v[84:85], 0, v[26:27]
	global_store_dwordx4 v[26:27], v[32:35], off sc1
.LBB3_169:
	s_or_b64 exec, exec, s[0:1]
	v_cvt_pk_f16_f32 v27, v20, v21
	v_cvt_pk_f16_f32 v26, v18, v19
	v_cvt_pk_f16_f32 v29, v24, v25
	v_cvt_pk_f16_f32 v28, v22, v23
	s_nop 1
	s_nop 0
	v_permlane16_swap_b32_e32 v26, v28
	v_permlane16_swap_b32_e32 v27, v29
	v_cmp_lt_i32_e32 vcc, -1, v1
	s_and_saveexec_b64 s[0:1], vcc
	s_cbranch_execz .LBB3_171
	v_lshlrev_b32_e32 v0, 11, v1
	v_and_b32_e32 v0, 0xfff800, v0
	v_mov_b32_e32 v1, 0
	v_lshl_add_u64 v[0:1], v[84:85], 0, v[0:1]
	global_store_dwordx4 v[0:1], v[26:29], off sc1
.LBB3_171:
	s_or_b64 exec, exec, s[0:1]
	v_cvt_pk_f16_f32 v19, v12, v13
	v_cvt_pk_f16_f32 v18, v10, v11
	v_cvt_pk_f16_f32 v21, v16, v17
	v_cvt_pk_f16_f32 v20, v14, v15
	s_nop 1
	s_nop 0
	v_permlane16_swap_b32_e32 v18, v20
	v_permlane16_swap_b32_e32 v19, v21
	v_cmp_lt_i32_e32 vcc, -1, v128
	s_and_saveexec_b64 s[0:1], vcc
	s_cbranch_execz .LBB3_173
	v_lshlrev_b32_e32 v0, 11, v128
	v_and_b32_e32 v0, 0xfff800, v0
	v_mov_b32_e32 v1, 0
	v_lshl_add_u64 v[0:1], v[84:85], 0, v[0:1]
	global_store_dwordx4 v[0:1], v[18:21], off sc1
.LBB3_173:
	s_or_b64 exec, exec, s[0:1]
	v_cvt_pk_f16_f32 v1, v4, v5
	v_cvt_pk_f16_f32 v0, v2, v3
	v_cvt_pk_f16_f32 v3, v8, v9
	v_cvt_pk_f16_f32 v2, v6, v7
	s_nop 1
	s_nop 0
	v_permlane16_swap_b32_e32 v0, v2
	v_permlane16_swap_b32_e32 v1, v3
	v_cmp_lt_i32_e32 vcc, -1, v126
	s_and_saveexec_b64 s[0:1], vcc
	s_cbranch_execz .LBB3_175
	v_lshlrev_b32_e32 v4, 11, v126
	v_and_b32_e32 v4, 0xfff800, v4
	v_mov_b32_e32 v5, 0
	v_lshl_add_u64 v[4:5], v[84:85], 0, v[4:5]
	global_store_dwordx4 v[4:5], v[0:3], off sc1
